# combined micro-edits on v64: loop-tail SALU moved ahead of loop-back barriers, batched combine-phase parameter staging, nt on single-use input reads, redundant zero-init movs removed in SwiGLU epilogu
# baseline (speedup 1.0000x reference)
; #define PG8_STAGE(bufoff, gbase, voff) do { _Pragma("unroll") for (int _i = 0; _i < 2; ++_i) \
;         __builtin_amdgcn_global_load_lds((const unsigned*)((const char*)(gbase) + (voff)[_i]), (PG8_LAS unsigned*)(lds + (bufoff) + ldsw + _i * 8192), 16, 0, 0); } while (0)
; #define PG8_LDA(dst, b, h) do { _Pragma("unroll") for (int m = 0; m < 4; ++m) _Pragma("unroll") for (int k = 0; k < 2; ++k) dst[m][k] = *(const PG8_LAS bf16x8*)(lds + PG8_SA(b, h) + aoff + m * 2048 + k * 1024); } while (0)
; #define PG8_WAIT_V(n) asm volatile("s_waitcnt vmcnt(" #n ")" ::: "memory")
; #define PG8_WAIT_L(n) asm volatile("s_waitcnt lgkmcnt(" #n ")" ::: "memory")
; template <class Epi, class Sched, bool ALIGN_EPI = false, bool SP2 = false, bool F8 = false, bool BTILED = false, bool ATILED = false>
; __device__ __forceinline__ void gemm_phase(PG8_LAS unsigned char* lds, const Gemm g, const Sched& S, const Epi& E) {
;     ...
;         for (int t = 0; t < nt; t += 2) {
;             const bool last = (t == nt - 2);
;             const char* a1 = cA + (size_t)(t + 1) * kstepA;
;             const char* a2 = last ? nA : cA + (size_t)(t + 2) * kstepA; const char* b2 = last ? nB : cB + (size_t)(t + 2) * kstepB;
;             const char* a3 = a2 + kstepA; const char* b3 = b2 + kstepB;
;             if (last && has_next) S.a_ready(nxt);
;             if constexpr (SP2) {
;             PG8_LDB(B0, 0, 0); PG8_LDB(B1, 0, 1); PG8_SCHED; PG8_LDA(At, 0, 0); PG8_STAGE(PG8_SA(1, 1), a1 + hstepA, voffA);
;             PG8_WAIT_V(8); PG8_WAIT_L(0); PG8_BAR; PG8_MMA(0, 0, At, B0); PG8_MMA(0, 1, At, B1); PG8_BAR; PG8_SCHED;
;             PG8_LDA(At, 0, 1); PG8_STAGE(PG8_SB(0, 0), b2, voffB); PG8_STAGE(PG8_SB(0, 1), b2 + hstepB, voffB); PG8_STAGE(PG8_SA(0, 0), a2, voffA);
;             PG8_WAIT_V(8); PG8_WAIT_L(0); PG8_BAR; PG8_MMA(1, 0, At, B0); PG8_MMA(1, 1, At, B1); PG8_BAR; PG8_SCHED;
;             PG8_LDB(B0, 1, 0); PG8_LDB(B1, 1, 1); PG8_SCHED; PG8_LDA(At, 1, 0); PG8_STAGE(PG8_SA(0, 1), a2 + hstepA, voffA);
;             PG8_WAIT_V(8); PG8_WAIT_L(0); PG8_BAR; PG8_MMA(0, 0, At, B0); PG8_MMA(0, 1, At, B1); PG8_BAR; PG8_SCHED;
;             PG8_LDA(At, 1, 1); PG8_STAGE(PG8_SB(1, 0), b3, voffB); PG8_STAGE(PG8_SB(1, 1), b3 + hstepB, voffB); PG8_STAGE(PG8_SA(1, 0), a3, voffA);
;             PG8_WAIT_V(8); PG8_WAIT_L(0); PG8_BAR; PG8_MMA(1, 0, At, B0); PG8_MMA(1, 1, At, B1); PG8_BAR; PG8_SCHED;
.LBB0_297:
	s_add_u32 s22, s2, 0xfffc0080
	s_addc_u32 s23, s3, -1
	s_add_i32 s50, 0, 0x10000
	s_cmp_eq_u32 s49, 12
	s_cselect_b32 s25, s17, s23
	s_cselect_b32 s24, s45, s22
	v_add_u32_e32 v140, s50, v143
	s_cselect_b32 s23, s15, s48
	s_cselect_b32 s22, s46, s47
	s_add_i32 s52, 0, 0x14000
	ds_read_b128 v[146:149], v140
	ds_read_b128 v[150:153], v140 offset:1024
	ds_read_b128 v[154:157], v140 offset:2048
	ds_read_b128 v[158:161], v140 offset:3072
	v_add_u32_e32 v140, s52, v143
	ds_read_b128 v[162:165], v140
	ds_read_b128 v[166:169], v140 offset:1024
	ds_read_b128 v[170:173], v140 offset:2048
	ds_read_b128 v[174:177], v140 offset:3072
	v_lshl_add_u64 v[140:141], s[2:3], 0, v[136:137]
	s_add_i32 m0, s35, 0xc000
	ds_read_b128 v[178:181], v145
	ds_read_b128 v[186:189], v145 offset:1024
	ds_read_b128 v[190:193], v145 offset:2048
	ds_read_b128 v[194:197], v145 offset:3072
	ds_read_b128 v[198:201], v145 offset:4096
	ds_read_b128 v[202:205], v145 offset:5120
	ds_read_b128 v[206:209], v145 offset:6144
	ds_read_b128 v[210:213], v145 offset:7168
	global_load_lds_dwordx4 v[140:141], off
	v_lshl_add_u64 v[140:141], s[2:3], 0, v[138:139]
	s_add_i32 m0, s35, 0xe000
	s_nop 0
	global_load_lds_dwordx4 v[140:141], off
	s_waitcnt vmcnt(8)
	s_waitcnt lgkmcnt(0)
	s_barrier
	s_setprio 1
	s_waitcnt lgkmcnt(0)
	v_mfma_f32_16x16x32_bf16 v[126:129], v[146:149], v[178:181], v[126:129]
	v_mfma_f32_16x16x32_bf16 v[122:125], v[154:157], v[178:181], v[122:125]
	v_mfma_f32_16x16x32_bf16 v[114:117], v[146:149], v[190:193], v[114:117]
	v_mfma_f32_16x16x32_bf16 v[106:109], v[154:157], v[190:193], v[106:109]
	v_mfma_f32_16x16x32_bf16 v[98:101], v[146:149], v[198:201], v[98:101]
	v_mfma_f32_16x16x32_bf16 v[90:93], v[154:157], v[198:201], v[90:93]
	v_mfma_f32_16x16x32_bf16 v[82:85], v[146:149], v[206:209], v[82:85]
	v_mfma_f32_16x16x32_bf16 v[74:77], v[154:157], v[206:209], v[74:77]
	v_mfma_f32_16x16x32_bf16 v[126:129], v[150:153], v[186:189], v[126:129]
	v_mfma_f32_16x16x32_bf16 v[122:125], v[158:161], v[186:189], v[122:125]
	v_mfma_f32_16x16x32_bf16 v[114:117], v[150:153], v[194:197], v[114:117]
	v_mfma_f32_16x16x32_bf16 v[106:109], v[158:161], v[194:197], v[106:109]
	v_mfma_f32_16x16x32_bf16 v[98:101], v[150:153], v[202:205], v[98:101]
	v_mfma_f32_16x16x32_bf16 v[90:93], v[158:161], v[202:205], v[90:93]
	v_mfma_f32_16x16x32_bf16 v[82:85], v[150:153], v[210:213], v[82:85]
	v_mfma_f32_16x16x32_bf16 v[74:77], v[158:161], v[210:213], v[74:77]
	s_setprio 0
	s_setprio 1
	v_mfma_f32_16x16x32_bf16 v[118:121], v[162:165], v[178:181], v[118:121]
	v_mfma_f32_16x16x32_bf16 v[110:113], v[170:173], v[178:181], v[110:113]
	v_mfma_f32_16x16x32_bf16 v[102:105], v[162:165], v[190:193], v[102:105]
	v_mfma_f32_16x16x32_bf16 v[94:97], v[170:173], v[190:193], v[94:97]
	v_mfma_f32_16x16x32_bf16 v[86:89], v[162:165], v[198:201], v[86:89]
	v_mfma_f32_16x16x32_bf16 v[78:81], v[170:173], v[198:201], v[78:81]
	v_mfma_f32_16x16x32_bf16 v[70:73], v[162:165], v[206:209], v[70:73]
	v_mfma_f32_16x16x32_bf16 v[66:69], v[170:173], v[206:209], v[66:69]
	v_mfma_f32_16x16x32_bf16 v[118:121], v[166:169], v[186:189], v[118:121]
	v_mfma_f32_16x16x32_bf16 v[110:113], v[174:177], v[186:189], v[110:113]
	v_mfma_f32_16x16x32_bf16 v[102:105], v[166:169], v[194:197], v[102:105]
	v_mfma_f32_16x16x32_bf16 v[94:97], v[174:177], v[194:197], v[94:97]
	v_mfma_f32_16x16x32_bf16 v[86:89], v[166:169], v[202:205], v[86:89]
	v_mfma_f32_16x16x32_bf16 v[78:81], v[174:177], v[202:205], v[78:81]
	v_mfma_f32_16x16x32_bf16 v[70:73], v[166:169], v[210:213], v[70:73]
	v_mfma_f32_16x16x32_bf16 v[66:69], v[174:177], v[210:213], v[66:69]
	s_setprio 0
	s_barrier
	s_add_i32 s50, s50, s34
	v_lshl_add_u64 v[140:141], s[22:23], 0, v[182:183]
	s_mov_b32 m0, s50
	ds_read_b128 v[178:181], v145 offset:16384
	ds_read_b128 v[186:189], v145 offset:17408
	ds_read_b128 v[190:193], v145 offset:18432
	ds_read_b128 v[194:197], v145 offset:19456
	ds_read_b128 v[198:201], v145 offset:20480
	ds_read_b128 v[202:205], v145 offset:21504
	ds_read_b128 v[206:209], v145 offset:22528
	ds_read_b128 v[210:213], v145 offset:23552
	global_load_lds_dwordx4 v[140:141], off
	s_add_i32 m0, s50, 0x2000
	s_add_u32 s50, s22, 0x40000
	v_lshl_add_u64 v[214:215], s[22:23], 0, v[130:131]
	s_addc_u32 s51, s23, 0
	s_add_i32 s52, s52, s34
	global_load_lds_dwordx4 v[214:215], off
	v_lshl_add_u64 v[216:217], s[50:51], 0, v[182:183]
	s_mov_b32 m0, s52
	v_lshl_add_u64 v[218:219], s[24:25], 0, v[132:133]
	global_load_lds_dwordx4 v[216:217], off
	v_lshl_add_u64 v[216:217], s[50:51], 0, v[130:131]
	s_add_i32 m0, s52, 0x2000
	s_nop 0
	global_load_lds_dwordx4 v[216:217], off
	v_lshl_add_u64 v[216:217], s[24:25], 0, v[134:135]
	s_mov_b32 m0, s35
	s_nop 0
	global_load_lds_dwordx4 v[216:217], off
	s_mov_b32 m0, s36
	s_nop 0
	global_load_lds_dwordx4 v[218:219], off
	s_waitcnt vmcnt(8)
	s_waitcnt lgkmcnt(0)
	s_barrier
; #define PG8_STAGE(bufoff, gbase, voff) do { _Pragma("unroll") for (int _i = 0; _i < 2; ++_i) \
;         __builtin_amdgcn_global_load_lds((const unsigned*)((const char*)(gbase) + (voff)[_i]), (PG8_LAS unsigned*)(lds + (bufoff) + ldsw + _i * 8192), 16, 0, 0); } while (0)
; #define PG8_LDA(dst, b, h) do { _Pragma("unroll") for (int m = 0; m < 4; ++m) _Pragma("unroll") for (int k = 0; k < 2; ++k) dst[m][k] = *(const PG8_LAS bf16x8*)(lds + PG8_SA(b, h) + aoff + m * 2048 + k * 1024); } while (0)
; #define PG8_WAIT_V(n) asm volatile("s_waitcnt vmcnt(" #n ")" ::: "memory")
; #define PG8_WAIT_L(n) asm volatile("s_waitcnt lgkmcnt(" #n ")" ::: "memory")
; template <class Epi, class Sched, bool ALIGN_EPI = false, bool SP2 = false, bool F8 = false, bool BTILED = false, bool ATILED = false>
; __device__ __forceinline__ void gemm_phase(PG8_LAS unsigned char* lds, const Gemm g, const Sched& S, const Epi& E) {
;     ...
;         for (int t = 0; t < nt; t += 2) {
;             const bool last = (t == nt - 2);
;             const char* a1 = cA + (size_t)(t + 1) * kstepA;
;             const char* a2 = last ? nA : cA + (size_t)(t + 2) * kstepA; const char* b2 = last ? nB : cB + (size_t)(t + 2) * kstepB;
;             const char* a3 = a2 + kstepA; const char* b3 = b2 + kstepB;
;             if (last && has_next) S.a_ready(nxt);
;             if constexpr (SP2) {
;             PG8_LDB(B0, 0, 0); PG8_LDB(B1, 0, 1); PG8_SCHED; PG8_LDA(At, 0, 0); PG8_STAGE(PG8_SA(1, 1), a1 + hstepA, voffA);
;             PG8_WAIT_V(8); PG8_WAIT_L(0); PG8_BAR; PG8_MMA(0, 0, At, B0); PG8_MMA(0, 1, At, B1); PG8_BAR; PG8_SCHED;
;             PG8_LDA(At, 0, 1); PG8_STAGE(PG8_SB(0, 0), b2, voffB); PG8_STAGE(PG8_SB(0, 1), b2 + hstepB, voffB); PG8_STAGE(PG8_SA(0, 0), a2, voffA);
;             PG8_WAIT_V(8); PG8_WAIT_L(0); PG8_BAR; PG8_MMA(1, 0, At, B0); PG8_MMA(1, 1, At, B1); PG8_BAR; PG8_SCHED;
;             PG8_LDB(B0, 1, 0); PG8_LDB(B1, 1, 1); PG8_SCHED; PG8_LDA(At, 1, 0); PG8_STAGE(PG8_SA(0, 1), a2 + hstepA, voffA);
;             PG8_WAIT_V(8); PG8_WAIT_L(0); PG8_BAR; PG8_MMA(0, 0, At, B0); PG8_MMA(0, 1, At, B1); PG8_BAR; PG8_SCHED;
;             PG8_LDA(At, 1, 1); PG8_STAGE(PG8_SB(1, 0), b3, voffB); PG8_STAGE(PG8_SB(1, 1), b3 + hstepB, voffB); PG8_STAGE(PG8_SA(1, 0), a3, voffA);
;             PG8_WAIT_V(8); PG8_WAIT_L(0); PG8_BAR; PG8_MMA(1, 0, At, B0); PG8_MMA(1, 1, At, B1); PG8_BAR; PG8_SCHED;
	s_setprio 1
	s_waitcnt lgkmcnt(0)
	v_mfma_f32_16x16x32_bf16 v[62:65], v[146:149], v[178:181], v[62:65]
	v_mfma_f32_16x16x32_bf16 v[58:61], v[154:157], v[178:181], v[58:61]
	v_mfma_f32_16x16x32_bf16 v[50:53], v[146:149], v[190:193], v[50:53]
	v_mfma_f32_16x16x32_bf16 v[42:45], v[154:157], v[190:193], v[42:45]
	v_mfma_f32_16x16x32_bf16 v[34:37], v[146:149], v[198:201], v[34:37]
	v_mfma_f32_16x16x32_bf16 v[26:29], v[154:157], v[198:201], v[26:29]
	v_mfma_f32_16x16x32_bf16 v[18:21], v[146:149], v[206:209], v[18:21]
	v_mfma_f32_16x16x32_bf16 v[10:13], v[154:157], v[206:209], v[10:13]
	v_mfma_f32_16x16x32_bf16 v[62:65], v[150:153], v[186:189], v[62:65]
	v_mfma_f32_16x16x32_bf16 v[58:61], v[158:161], v[186:189], v[58:61]
	v_mfma_f32_16x16x32_bf16 v[50:53], v[150:153], v[194:197], v[50:53]
	v_mfma_f32_16x16x32_bf16 v[42:45], v[158:161], v[194:197], v[42:45]
	v_mfma_f32_16x16x32_bf16 v[34:37], v[150:153], v[202:205], v[34:37]
	v_mfma_f32_16x16x32_bf16 v[26:29], v[158:161], v[202:205], v[26:29]
	v_mfma_f32_16x16x32_bf16 v[18:21], v[150:153], v[210:213], v[18:21]
	v_mfma_f32_16x16x32_bf16 v[10:13], v[158:161], v[210:213], v[10:13]
	s_setprio 0
	s_setprio 1
	v_mfma_f32_16x16x32_bf16 v[54:57], v[162:165], v[178:181], v[54:57]
	v_mfma_f32_16x16x32_bf16 v[46:49], v[170:173], v[178:181], v[46:49]
	v_mfma_f32_16x16x32_bf16 v[38:41], v[162:165], v[190:193], v[38:41]
	v_mfma_f32_16x16x32_bf16 v[30:33], v[170:173], v[190:193], v[30:33]
	v_mfma_f32_16x16x32_bf16 v[22:25], v[162:165], v[198:201], v[22:25]
	v_mfma_f32_16x16x32_bf16 v[14:17], v[170:173], v[198:201], v[14:17]
	v_mfma_f32_16x16x32_bf16 v[6:9], v[162:165], v[206:209], v[6:9]
	v_mfma_f32_16x16x32_bf16 v[2:5], v[170:173], v[206:209], v[2:5]
	v_mfma_f32_16x16x32_bf16 v[54:57], v[166:169], v[186:189], v[54:57]
	v_mfma_f32_16x16x32_bf16 v[46:49], v[174:177], v[186:189], v[46:49]
	v_mfma_f32_16x16x32_bf16 v[38:41], v[166:169], v[194:197], v[38:41]
	v_mfma_f32_16x16x32_bf16 v[30:33], v[174:177], v[194:197], v[30:33]
	v_mfma_f32_16x16x32_bf16 v[22:25], v[166:169], v[202:205], v[22:25]
	v_mfma_f32_16x16x32_bf16 v[14:17], v[174:177], v[202:205], v[14:17]
	v_mfma_f32_16x16x32_bf16 v[6:9], v[166:169], v[210:213], v[6:9]
	v_mfma_f32_16x16x32_bf16 v[2:5], v[174:177], v[210:213], v[2:5]
	s_setprio 0
	s_barrier
	s_add_i32 s50, 0, 0x18000
	s_add_i32 s51, 0, 0x1c000
	v_add_u32_e32 v158, s50, v143
	v_add_u32_e32 v174, s51, v143
	ds_read_b128 v[146:149], v158
	ds_read_b128 v[150:153], v158 offset:1024
	ds_read_b128 v[154:157], v158 offset:2048
	ds_read_b128 v[158:161], v158 offset:3072
	ds_read_b128 v[162:165], v174
	ds_read_b128 v[166:169], v174 offset:1024
	ds_read_b128 v[170:173], v174 offset:2048
	ds_read_b128 v[174:177], v174 offset:3072
	s_add_u32 s24, s24, 0x40000
	s_addc_u32 s25, s25, 0
	s_mov_b32 m0, s37
	v_lshl_add_u64 v[220:221], s[24:25], 0, v[134:135]
	ds_read_b128 v[178:181], v145 offset:32768
	ds_read_b128 v[186:189], v145 offset:33792
	ds_read_b128 v[190:193], v145 offset:34816
	ds_read_b128 v[194:197], v145 offset:35840
	ds_read_b128 v[198:201], v145 offset:36864
	ds_read_b128 v[202:205], v145 offset:37888
	ds_read_b128 v[206:209], v145 offset:38912
	ds_read_b128 v[210:213], v145 offset:39936
	global_load_lds_dwordx4 v[220:221], off
	v_lshl_add_u64 v[220:221], s[24:25], 0, v[132:133]
	s_mov_b32 m0, s38
	s_nop 0
	global_load_lds_dwordx4 v[220:221], off
	s_waitcnt vmcnt(8)
	s_waitcnt lgkmcnt(0)
	s_barrier
	s_setprio 1
	s_waitcnt lgkmcnt(0)
	v_mfma_f32_16x16x32_bf16 v[126:129], v[146:149], v[178:181], v[126:129]
	v_mfma_f32_16x16x32_bf16 v[122:125], v[154:157], v[178:181], v[122:125]
	v_mfma_f32_16x16x32_bf16 v[114:117], v[146:149], v[190:193], v[114:117]
	v_mfma_f32_16x16x32_bf16 v[106:109], v[154:157], v[190:193], v[106:109]
	v_mfma_f32_16x16x32_bf16 v[98:101], v[146:149], v[198:201], v[98:101]
	v_mfma_f32_16x16x32_bf16 v[90:93], v[154:157], v[198:201], v[90:93]
	v_mfma_f32_16x16x32_bf16 v[82:85], v[146:149], v[206:209], v[82:85]
	v_mfma_f32_16x16x32_bf16 v[74:77], v[154:157], v[206:209], v[74:77]
	v_mfma_f32_16x16x32_bf16 v[126:129], v[150:153], v[186:189], v[126:129]
	v_mfma_f32_16x16x32_bf16 v[122:125], v[158:161], v[186:189], v[122:125]
	v_mfma_f32_16x16x32_bf16 v[114:117], v[150:153], v[194:197], v[114:117]
	v_mfma_f32_16x16x32_bf16 v[106:109], v[158:161], v[194:197], v[106:109]
	v_mfma_f32_16x16x32_bf16 v[98:101], v[150:153], v[202:205], v[98:101]
	v_mfma_f32_16x16x32_bf16 v[90:93], v[158:161], v[202:205], v[90:93]
	v_mfma_f32_16x16x32_bf16 v[82:85], v[150:153], v[210:213], v[82:85]
	v_mfma_f32_16x16x32_bf16 v[74:77], v[158:161], v[210:213], v[74:77]
	s_setprio 0
	s_setprio 1
	v_mfma_f32_16x16x32_bf16 v[118:121], v[162:165], v[178:181], v[118:121]
	v_mfma_f32_16x16x32_bf16 v[110:113], v[170:173], v[178:181], v[110:113]
	v_mfma_f32_16x16x32_bf16 v[102:105], v[162:165], v[190:193], v[102:105]
	v_mfma_f32_16x16x32_bf16 v[94:97], v[170:173], v[190:193], v[94:97]
	v_mfma_f32_16x16x32_bf16 v[86:89], v[162:165], v[198:201], v[86:89]
	v_mfma_f32_16x16x32_bf16 v[78:81], v[170:173], v[198:201], v[78:81]
	v_mfma_f32_16x16x32_bf16 v[70:73], v[162:165], v[206:209], v[70:73]
	v_mfma_f32_16x16x32_bf16 v[66:69], v[170:173], v[206:209], v[66:69]
	v_mfma_f32_16x16x32_bf16 v[118:121], v[166:169], v[186:189], v[118:121]
	v_mfma_f32_16x16x32_bf16 v[110:113], v[174:177], v[186:189], v[110:113]
	v_mfma_f32_16x16x32_bf16 v[102:105], v[166:169], v[194:197], v[102:105]
	v_mfma_f32_16x16x32_bf16 v[94:97], v[174:177], v[194:197], v[94:97]
	v_mfma_f32_16x16x32_bf16 v[86:89], v[166:169], v[202:205], v[86:89]
	v_mfma_f32_16x16x32_bf16 v[78:81], v[174:177], v[202:205], v[78:81]
	v_mfma_f32_16x16x32_bf16 v[70:73], v[166:169], v[210:213], v[70:73]
	v_mfma_f32_16x16x32_bf16 v[66:69], v[174:177], v[210:213], v[66:69]
	s_setprio 0
	s_barrier
; #define PG8_STAGE(bufoff, gbase, voff) do { _Pragma("unroll") for (int _i = 0; _i < 2; ++_i) \
;         __builtin_amdgcn_global_load_lds((const unsigned*)((const char*)(gbase) + (voff)[_i]), (PG8_LAS unsigned*)(lds + (bufoff) + ldsw + _i * 8192), 16, 0, 0); } while (0)
; #define PG8_LDA(dst, b, h) do { _Pragma("unroll") for (int m = 0; m < 4; ++m) _Pragma("unroll") for (int k = 0; k < 2; ++k) dst[m][k] = *(const PG8_LAS bf16x8*)(lds + PG8_SA(b, h) + aoff + m * 2048 + k * 1024); } while (0)
; #define PG8_WAIT_V(n) asm volatile("s_waitcnt vmcnt(" #n ")" ::: "memory")
; #define PG8_WAIT_L(n) asm volatile("s_waitcnt lgkmcnt(" #n ")" ::: "memory")
; template <class Epi, class Sched, bool ALIGN_EPI = false, bool SP2 = false, bool F8 = false, bool BTILED = false, bool ATILED = false>
; __device__ __forceinline__ void gemm_phase(PG8_LAS unsigned char* lds, const Gemm g, const Sched& S, const Epi& E) {
;     ...
;         for (int t = 0; t < nt; t += 2) {
;             const bool last = (t == nt - 2);
;             const char* a1 = cA + (size_t)(t + 1) * kstepA;
;             const char* a2 = last ? nA : cA + (size_t)(t + 2) * kstepA; const char* b2 = last ? nB : cB + (size_t)(t + 2) * kstepB;
;             const char* a3 = a2 + kstepA; const char* b3 = b2 + kstepB;
;             if (last && has_next) S.a_ready(nxt);
;             if constexpr (SP2) {
;             PG8_LDB(B0, 0, 0); PG8_LDB(B1, 0, 1); PG8_SCHED; PG8_LDA(At, 0, 0); PG8_STAGE(PG8_SA(1, 1), a1 + hstepA, voffA);
;             PG8_WAIT_V(8); PG8_WAIT_L(0); PG8_BAR; PG8_MMA(0, 0, At, B0); PG8_MMA(0, 1, At, B1); PG8_BAR; PG8_SCHED;
;             PG8_LDA(At, 0, 1); PG8_STAGE(PG8_SB(0, 0), b2, voffB); PG8_STAGE(PG8_SB(0, 1), b2 + hstepB, voffB); PG8_STAGE(PG8_SA(0, 0), a2, voffA);
;             PG8_WAIT_V(8); PG8_WAIT_L(0); PG8_BAR; PG8_MMA(1, 0, At, B0); PG8_MMA(1, 1, At, B1); PG8_BAR; PG8_SCHED;
;             PG8_LDB(B0, 1, 0); PG8_LDB(B1, 1, 1); PG8_SCHED; PG8_LDA(At, 1, 0); PG8_STAGE(PG8_SA(0, 1), a2 + hstepA, voffA);
;             PG8_WAIT_V(8); PG8_WAIT_L(0); PG8_BAR; PG8_MMA(0, 0, At, B0); PG8_MMA(0, 1, At, B1); PG8_BAR; PG8_SCHED;
;             PG8_LDA(At, 1, 1); PG8_STAGE(PG8_SB(1, 0), b3, voffB); PG8_STAGE(PG8_SB(1, 1), b3 + hstepB, voffB); PG8_STAGE(PG8_SA(1, 0), a3, voffA);
;             PG8_WAIT_V(8); PG8_WAIT_L(0); PG8_BAR; PG8_MMA(1, 0, At, B0); PG8_MMA(1, 1, At, B1); PG8_BAR; PG8_SCHED;
	s_add_i32 s24, s50, s34
	v_lshl_add_u64 v[140:141], v[140:141], 0, s[90:91]
	s_mov_b32 m0, s24
	ds_read_b128 v[178:181], v145 offset:49152
	ds_read_b128 v[186:189], v145 offset:50176
	ds_read_b128 v[190:193], v145 offset:51200
	ds_read_b128 v[194:197], v145 offset:52224
	ds_read_b128 v[198:201], v145 offset:53248
	ds_read_b128 v[202:205], v145 offset:54272
	ds_read_b128 v[206:209], v145 offset:55296
	ds_read_b128 v[210:213], v145 offset:56320
	global_load_lds_dwordx4 v[140:141], off
	s_add_i32 m0, s24, 0x2000
	s_add_u32 s22, s22, 0x40080
	v_lshl_add_u64 v[140:141], v[214:215], 0, s[90:91]
	s_addc_u32 s23, s23, 0
	s_add_i32 s24, s51, s34
	global_load_lds_dwordx4 v[140:141], off
	v_lshl_add_u64 v[140:141], s[22:23], 0, v[182:183]
	s_mov_b32 m0, s24
	s_nop 0
	global_load_lds_dwordx4 v[140:141], off
	v_lshl_add_u64 v[140:141], s[22:23], 0, v[130:131]
	s_add_i32 m0, s24, 0x2000
	s_nop 0
	global_load_lds_dwordx4 v[140:141], off
	v_lshl_add_u64 v[140:141], v[216:217], 0, s[90:91]
	s_mov_b32 m0, s39
	s_nop 0
	global_load_lds_dwordx4 v[140:141], off
	v_lshl_add_u64 v[140:141], v[218:219], 0, s[90:91]
	s_mov_b32 m0, s40
	s_nop 0
	global_load_lds_dwordx4 v[140:141], off
	s_waitcnt vmcnt(8)
	s_waitcnt lgkmcnt(0)
	s_barrier
	s_setprio 1
	s_waitcnt lgkmcnt(0)
	v_mfma_f32_16x16x32_bf16 v[62:65], v[146:149], v[178:181], v[62:65]
	s_add_i32 s49, s49, 2
	s_add_u32 s2, s2, 0x100
	s_addc_u32 s3, s3, 0
	s_add_u32 s47, s47, 0x100
	s_addc_u32 s48, s48, 0
	s_cmp_gt_u32 s49, 13
	v_mfma_f32_16x16x32_bf16 v[58:61], v[154:157], v[178:181], v[58:61]
	v_mfma_f32_16x16x32_bf16 v[50:53], v[146:149], v[190:193], v[50:53]
	v_mfma_f32_16x16x32_bf16 v[42:45], v[154:157], v[190:193], v[42:45]
	v_mfma_f32_16x16x32_bf16 v[34:37], v[146:149], v[198:201], v[34:37]
	v_mfma_f32_16x16x32_bf16 v[26:29], v[154:157], v[198:201], v[26:29]
	v_mfma_f32_16x16x32_bf16 v[18:21], v[146:149], v[206:209], v[18:21]
	v_mfma_f32_16x16x32_bf16 v[10:13], v[154:157], v[206:209], v[10:13]
	v_mfma_f32_16x16x32_bf16 v[62:65], v[150:153], v[186:189], v[62:65]
	v_mfma_f32_16x16x32_bf16 v[58:61], v[158:161], v[186:189], v[58:61]
	v_mfma_f32_16x16x32_bf16 v[50:53], v[150:153], v[194:197], v[50:53]
	v_mfma_f32_16x16x32_bf16 v[42:45], v[158:161], v[194:197], v[42:45]
	v_mfma_f32_16x16x32_bf16 v[34:37], v[150:153], v[202:205], v[34:37]
	v_mfma_f32_16x16x32_bf16 v[26:29], v[158:161], v[202:205], v[26:29]
	v_mfma_f32_16x16x32_bf16 v[18:21], v[150:153], v[210:213], v[18:21]
	v_mfma_f32_16x16x32_bf16 v[10:13], v[158:161], v[210:213], v[10:13]
	s_setprio 0
	s_setprio 1
	v_mfma_f32_16x16x32_bf16 v[54:57], v[162:165], v[178:181], v[54:57]
	v_mfma_f32_16x16x32_bf16 v[46:49], v[170:173], v[178:181], v[46:49]
	v_mfma_f32_16x16x32_bf16 v[38:41], v[162:165], v[190:193], v[38:41]
	v_mfma_f32_16x16x32_bf16 v[30:33], v[170:173], v[190:193], v[30:33]
	v_mfma_f32_16x16x32_bf16 v[22:25], v[162:165], v[198:201], v[22:25]
	v_mfma_f32_16x16x32_bf16 v[14:17], v[170:173], v[198:201], v[14:17]
	v_mfma_f32_16x16x32_bf16 v[6:9], v[162:165], v[206:209], v[6:9]
	v_mfma_f32_16x16x32_bf16 v[2:5], v[170:173], v[206:209], v[2:5]
	v_mfma_f32_16x16x32_bf16 v[54:57], v[166:169], v[186:189], v[54:57]
	v_mfma_f32_16x16x32_bf16 v[46:49], v[174:177], v[186:189], v[46:49]
	v_mfma_f32_16x16x32_bf16 v[38:41], v[166:169], v[194:197], v[38:41]
	v_mfma_f32_16x16x32_bf16 v[30:33], v[174:177], v[194:197], v[30:33]
	v_mfma_f32_16x16x32_bf16 v[22:25], v[166:169], v[202:205], v[22:25]
	v_mfma_f32_16x16x32_bf16 v[14:17], v[174:177], v[202:205], v[14:17]
	v_mfma_f32_16x16x32_bf16 v[6:9], v[166:169], v[210:213], v[6:9]
	v_mfma_f32_16x16x32_bf16 v[2:5], v[174:177], v[210:213], v[2:5]
	s_setprio 0
	s_barrier
	s_cbranch_scc0 .LBB0_297
	s_and_b64 vcc, exec, s[12:13]
	s_cbranch_vccz .LBB0_300
	s_barrier

.LBB0_717:
	v_add_u32_e32 v195, s43, v190
	ds_read_b64_tr_b16 v[196:197], v195 offset:24576
	ds_read_b64_tr_b16 v[198:199], v195 offset:25088
	v_add_f32_e32 v86, v66, v67
	v_add_f32_e32 v86, v68, v86
	v_add_f32_e32 v86, v69, v86
	v_add_f32_e32 v86, v70, v86
	v_add_f32_e32 v86, v71, v86
	v_cvt_pk_bf16_f32 v158, v66, v67
	v_cvt_pk_bf16_f32 v159, v68, v69
	s_waitcnt lgkmcnt(9)
	v_mfma_f32_32x32x16_bf16 v[98:113], v[82:85], v[154:157], v[34:49]
	ds_read_b64_tr_b16 v[66:67], v195 offset:28672
	ds_read_b64_tr_b16 v[68:69], v195 offset:29184
	v_add_f32_e32 v82, v72, v86
	v_add_f32_e32 v82, v73, v82
	v_add_f32_e32 v82, v74, v82
	v_add_f32_e32 v138, v75, v82
	s_waitcnt lgkmcnt(10)
	v_mfma_f32_32x32x16_bf16 v[82:97], v[166:169], v[154:157], v[34:49]
	v_cvt_pk_bf16_f32 v160, v70, v71
	v_cvt_pk_bf16_f32 v161, v72, v73
	ds_read_b64_tr_b16 v[70:71], v195 offset:25600
	ds_read_b64_tr_b16 v[72:73], v195 offset:26112
	v_add_f32_e32 v138, v76, v138
	v_add_f32_e32 v138, v77, v138
	v_add_f32_e32 v138, v78, v138
	v_add_f32_e32 v138, v79, v138
	v_cvt_pk_bf16_f32 v150, v74, v75
	v_cvt_pk_bf16_f32 v151, v76, v77
	s_waitcnt lgkmcnt(11)
	v_mfma_f32_32x32x16_bf16 v[98:113], v[170:173], v[146:149], v[98:113]
	ds_read_b64_tr_b16 v[74:75], v195 offset:29696
	ds_read_b64_tr_b16 v[76:77], v195 offset:30208
	s_waitcnt lgkmcnt(12)
	v_mfma_f32_32x32x16_bf16 v[82:97], v[162:165], v[146:149], v[82:97]
	v_add_f32_e32 v138, v80, v138
	v_add_f32_e32 v138, v81, v138
	v_add_f32_e32 v138, v50, v138
	v_add_f32_e32 v138, v51, v138
	v_cvt_pk_bf16_f32 v152, v78, v79
	v_cvt_pk_bf16_f32 v153, v80, v81
	ds_read_b64_tr_b16 v[78:79], v195 offset:26624
	ds_read_b64_tr_b16 v[80:81], v195 offset:27136
	s_waitcnt lgkmcnt(13)
	v_mfma_f32_32x32x16_bf16 v[98:113], v[126:129], v[134:137], v[98:113]
	v_add_f32_e32 v126, v52, v138
	v_add_f32_e32 v126, v53, v126
	v_add_f32_e32 v126, v54, v126
	v_add_f32_e32 v126, v55, v126
	v_cvt_pk_bf16_f32 v142, v50, v51
	v_cvt_pk_bf16_f32 v143, v52, v53
	ds_read_b64_tr_b16 v[50:51], v195 offset:30720
	ds_read_b64_tr_b16 v[52:53], v195 offset:31232
	s_waitcnt lgkmcnt(14)
	v_mfma_f32_32x32x16_bf16 v[82:97], v[122:125], v[134:137], v[82:97]
	v_add_f32_e32 v122, v56, v126
	v_add_f32_e32 v122, v57, v122
	v_add_f32_e32 v122, v58, v122
	v_add_f32_e32 v122, v59, v122
	v_cvt_pk_bf16_f32 v144, v54, v55
	v_cvt_pk_bf16_f32 v145, v56, v57
	ds_read_b64_tr_b16 v[54:55], v195 offset:27648
	ds_read_b64_tr_b16 v[56:57], v195 offset:28160
	s_waitcnt lgkmcnt(14)
	v_mfma_f32_32x32x16_bf16 v[98:113], v[118:121], v[130:133], v[98:113]
	v_add_f32_e32 v118, v60, v122
	v_add_f32_e32 v118, v61, v118
	v_add_f32_e32 v118, v62, v118
	v_add_f32_e32 v118, v63, v118
	v_cvt_pk_bf16_f32 v138, v58, v59
	v_cvt_pk_bf16_f32 v139, v60, v61
	ds_read_b64_tr_b16 v[58:59], v195 offset:31744
	ds_read_b64_tr_b16 v[60:61], v195 offset:32256
	v_mfma_f32_32x32x16_bf16 v[82:97], v[114:117], v[130:133], v[82:97]
	v_add_f32_e32 v114, v64, v118
	v_add_f32_e32 v114, v65, v114
	v_add_f32_e32 v195, 0, v114
	v_cvt_pk_bf16_f32 v140, v62, v63
	v_cvt_pk_bf16_f32 v141, v64, v65
	v_lshl_add_u64 v[62:63], v[178:179], 0, s[60:61]
	s_add_i32 s2, s42, s27
	s_mov_b32 s3, m0
	s_mov_b32 m0, s2
	s_nop 0
	global_load_lds_dwordx4 v[62:63], off
	s_mov_b32 m0, s3
	v_lshl_add_u64 v[62:63], v[180:181], 0, s[52:53]
	s_add_i32 s2, s31, s26
	s_mov_b32 s3, m0
	s_mov_b32 m0, s2
	s_nop 0
	global_load_lds_dwordx4 v[62:63], off
	s_mov_b32 m0, s3
	s_waitcnt lgkmcnt(14)
	v_mfma_f32_32x32x16_bf16 v[2:17], v[158:161], v[196:199], v[2:17]
	v_exp_f32_e32 v98, v98
	v_exp_f32_e32 v99, v99
	v_exp_f32_e32 v100, v100
	v_exp_f32_e32 v101, v101
	s_waitcnt lgkmcnt(12)
	v_mfma_f32_32x32x16_bf16 v[18:33], v[158:161], v[66:69], v[18:33]
	v_exp_f32_e32 v102, v102
	v_exp_f32_e32 v103, v103
	v_exp_f32_e32 v104, v104
	v_exp_f32_e32 v105, v105
	v_add_u32_e32 v66, s31, v191
	ds_read_b128 v[62:65], v66
	ds_read_b128 v[118:121], v66 offset:512
	s_waitcnt lgkmcnt(12)
	v_mfma_f32_32x32x16_bf16 v[2:17], v[150:153], v[70:73], v[2:17]
	v_exp_f32_e32 v106, v106
	v_exp_f32_e32 v107, v107
	v_exp_f32_e32 v108, v108
	v_exp_f32_e32 v109, v109
	ds_read_b128 v[122:125], v66 offset:2048
	ds_read_b128 v[126:129], v66 offset:2560
	s_waitcnt lgkmcnt(12)
	v_mfma_f32_32x32x16_bf16 v[18:33], v[150:153], v[74:77], v[18:33]
	v_exp_f32_e32 v110, v110
	v_exp_f32_e32 v111, v111
	v_exp_f32_e32 v112, v112
	v_exp_f32_e32 v113, v113
	ds_read_b128 v[162:165], v66 offset:4096
	ds_read_b128 v[166:169], v66 offset:4608
	s_waitcnt lgkmcnt(12)
	v_mfma_f32_32x32x16_bf16 v[2:17], v[142:145], v[78:81], v[2:17]
	v_exp_f32_e32 v82, v82
	v_exp_f32_e32 v83, v83
	v_exp_f32_e32 v84, v84
	v_exp_f32_e32 v85, v85
	ds_read_b128 v[170:173], v66 offset:6144
	ds_read_b128 v[114:117], v66 offset:6656
	s_waitcnt lgkmcnt(12)
	v_mfma_f32_32x32x16_bf16 v[18:33], v[142:145], v[50:53], v[18:33]
	v_exp_f32_e32 v86, v86
	v_exp_f32_e32 v87, v87
	v_exp_f32_e32 v88, v88
	v_exp_f32_e32 v89, v89
	s_waitcnt lgkmcnt(10)
	v_mfma_f32_32x32x16_bf16 v[2:17], v[138:141], v[54:57], v[2:17]
	v_exp_f32_e32 v90, v90
	v_exp_f32_e32 v91, v91
	v_exp_f32_e32 v92, v92
	v_exp_f32_e32 v93, v93
	s_waitcnt lgkmcnt(8)
	v_mfma_f32_32x32x16_bf16 v[18:33], v[138:141], v[58:61], v[18:33]
	v_exp_f32_e32 v94, v94
	v_exp_f32_e32 v95, v95
	v_exp_f32_e32 v96, v96
	v_exp_f32_e32 v97, v97
	s_waitcnt vmcnt(2) lgkmcnt(0)
	s_barrier
; #define WAIT_BAR(N) asm volatile("s_waitcnt vmcnt(" #N ") lgkmcnt(0)\n\ts_barrier":::"memory")
;   #define RESC() do{ if(resc){ asm volatile("s_waitcnt lgkmcnt(0)":::"memory"); \
;       _Pragma("unroll") for(int d_=0;d_<2;++d_) _Pragma("unroll") for(int r=0;r<16;++r)o[d_][r]*=wsf[crow(r,hi)]; } }while(0)
;   #define ROT() do{sl_prev=sl_cur;sl_cur=sl_next;sl_next=(sl_next==(NSLOT-1)*SLOTB)?0:sl_next+SLOTB;}while(0)
;     ...
;   int t=1;
;     ...
;   for(;t+5<NT;t+=2){
;     STEP(pB0,pB1,pA0,pA1,t,true,true,true);     WAIT_BAR(2); RESC(); ROT();
;     STEP(pA0,pA1,pB0,pB1,t+1,true,true,true);   WAIT_BAR(2); RESC(); ROT();
;   }
	s_add_i32 s2, s31, 0x2000
	s_cmpk_lg_i32 s31, 0x4000
	s_cselect_b32 s2, s2, 0
	v_add_u32_e32 v204, s42, v190
	ds_read_b64_tr_b16 v[196:197], v204 offset:24576
	ds_read_b64_tr_b16 v[198:199], v204 offset:25088
	s_waitcnt lgkmcnt(9)
	v_mfma_f32_32x32x16_bf16 v[66:81], v[62:65], v[154:157], v[34:49]
	v_add_f32_e32 v50, v98, v99
	v_add_f32_e32 v50, v100, v50
	v_add_f32_e32 v50, v101, v50
	v_add_f32_e32 v50, v102, v50
	v_add_f32_e32 v50, v103, v50
	v_cvt_pk_bf16_f32 v158, v98, v99
	v_cvt_pk_bf16_f32 v159, v100, v101
	ds_read_b64_tr_b16 v[98:99], v204 offset:28672
	ds_read_b64_tr_b16 v[100:101], v204 offset:29184
	v_add_f32_e32 v50, v104, v50
	v_add_f32_e32 v50, v105, v50
	v_add_f32_e32 v50, v106, v50
	v_add_f32_e32 v138, v107, v50
	s_waitcnt lgkmcnt(10)
	v_mfma_f32_32x32x16_bf16 v[50:65], v[118:121], v[154:157], v[34:49]
	v_cvt_pk_bf16_f32 v160, v102, v103
	v_cvt_pk_bf16_f32 v161, v104, v105
	ds_read_b64_tr_b16 v[102:103], v204 offset:25600
	ds_read_b64_tr_b16 v[104:105], v204 offset:26112
	s_waitcnt lgkmcnt(11)
	v_mfma_f32_32x32x16_bf16 v[66:81], v[122:125], v[146:149], v[66:81]
	v_add_f32_e32 v118, v108, v138
	v_add_f32_e32 v118, v109, v118
	v_add_f32_e32 v118, v110, v118
	v_add_f32_e32 v118, v111, v118
	v_cvt_pk_bf16_f32 v150, v106, v107
	v_cvt_pk_bf16_f32 v151, v108, v109
	ds_read_b64_tr_b16 v[106:107], v204 offset:29696
	ds_read_b64_tr_b16 v[108:109], v204 offset:30208
	s_waitcnt lgkmcnt(12)
	v_mfma_f32_32x32x16_bf16 v[50:65], v[126:129], v[146:149], v[50:65]
	v_add_f32_e32 v118, v112, v118
	v_add_f32_e32 v118, v113, v118
	v_add_f32_e32 v118, v82, v118
	v_add_f32_e32 v118, v83, v118
	v_cvt_pk_bf16_f32 v152, v110, v111
	v_cvt_pk_bf16_f32 v153, v112, v113
	ds_read_b64_tr_b16 v[110:111], v204 offset:26624
	ds_read_b64_tr_b16 v[112:113], v204 offset:27136
	s_waitcnt lgkmcnt(13)
	v_mfma_f32_32x32x16_bf16 v[66:81], v[162:165], v[134:137], v[66:81]
	v_add_f32_e32 v118, v84, v118
	v_add_f32_e32 v118, v85, v118
	v_add_f32_e32 v118, v86, v118
	v_add_f32_e32 v118, v87, v118
	v_cvt_pk_bf16_f32 v142, v82, v83
	v_cvt_pk_bf16_f32 v143, v84, v85
	ds_read_b64_tr_b16 v[200:201], v204 offset:30720
	ds_read_b64_tr_b16 v[202:203], v204 offset:31232
	s_waitcnt lgkmcnt(14)
	v_mfma_f32_32x32x16_bf16 v[50:65], v[166:169], v[134:137], v[50:65]
	v_add_f32_e32 v82, v88, v118
	v_add_f32_e32 v82, v89, v82
	v_add_f32_e32 v82, v90, v82
	v_add_f32_e32 v82, v91, v82
	v_cvt_pk_bf16_f32 v144, v86, v87
	v_cvt_pk_bf16_f32 v145, v88, v89
	ds_read_b64_tr_b16 v[86:87], v204 offset:27648
	ds_read_b64_tr_b16 v[88:89], v204 offset:28160
	s_waitcnt lgkmcnt(14)
	v_mfma_f32_32x32x16_bf16 v[66:81], v[170:173], v[130:133], v[66:81]
	v_add_f32_e32 v82, v92, v82
	v_add_f32_e32 v82, v93, v82
	v_add_f32_e32 v82, v94, v82
	v_add_f32_e32 v82, v95, v82
	v_cvt_pk_bf16_f32 v138, v90, v91
	v_cvt_pk_bf16_f32 v139, v92, v93
	ds_read_b64_tr_b16 v[90:91], v204 offset:31744
	ds_read_b64_tr_b16 v[92:93], v204 offset:32256
	v_mfma_f32_32x32x16_bf16 v[50:65], v[114:117], v[130:133], v[50:65]
	v_add_f32_e32 v82, v96, v82
	v_add_f32_e32 v82, v97, v82
	v_add_f32_e32 v204, 0, v82
	v_cvt_pk_bf16_f32 v140, v94, v95
	v_cvt_pk_bf16_f32 v141, v96, v97
	v_lshl_add_u64 v[82:83], v[178:179], 0, s[46:47]
	s_add_i32 s3, s31, s27
	s_mov_b32 s22, m0
	s_mov_b32 m0, s3
	s_nop 0
	global_load_lds_dwordx4 v[82:83], off
	s_mov_b32 m0, s22
	v_lshl_add_u64 v[180:181], v[180:181], 0, s[54:55]
	s_add_i32 s3, s2, s26
	s_mov_b32 s22, m0
	s_mov_b32 m0, s3
	s_nop 0
	global_load_lds_dwordx4 v[180:181], off
	s_mov_b32 m0, s22
	s_waitcnt lgkmcnt(14)
	v_mfma_f32_32x32x16_bf16 v[2:17], v[158:161], v[196:199], v[2:17]
	v_exp_f32_e32 v66, v66
	v_exp_f32_e32 v67, v67
	v_exp_f32_e32 v68, v68
	v_exp_f32_e32 v69, v69
	s_waitcnt lgkmcnt(12)
	v_mfma_f32_32x32x16_bf16 v[18:33], v[158:161], v[98:101], v[18:33]
	v_exp_f32_e32 v70, v70
	v_exp_f32_e32 v71, v71
	v_exp_f32_e32 v72, v72
	v_exp_f32_e32 v73, v73
	v_add_u32_e32 v94, s2, v191
	ds_read_b128 v[82:85], v94
	ds_read_b128 v[166:169], v94 offset:512
	s_waitcnt lgkmcnt(12)
	v_mfma_f32_32x32x16_bf16 v[2:17], v[150:153], v[102:105], v[2:17]
	v_exp_f32_e32 v74, v74
	v_exp_f32_e32 v75, v75
	v_exp_f32_e32 v76, v76
	v_exp_f32_e32 v77, v77
	ds_read_b128 v[170:173], v94 offset:2048
	ds_read_b128 v[162:165], v94 offset:2560
	s_waitcnt lgkmcnt(12)
	v_mfma_f32_32x32x16_bf16 v[18:33], v[150:153], v[106:109], v[18:33]
	v_exp_f32_e32 v78, v78
	v_exp_f32_e32 v79, v79
	v_exp_f32_e32 v80, v80
	v_exp_f32_e32 v81, v81
	ds_read_b128 v[126:129], v94 offset:4096
	ds_read_b128 v[122:125], v94 offset:4608
	s_waitcnt lgkmcnt(12)
	v_mfma_f32_32x32x16_bf16 v[2:17], v[142:145], v[110:113], v[2:17]
	v_exp_f32_e32 v50, v50
	v_exp_f32_e32 v51, v51
	v_exp_f32_e32 v52, v52
	v_exp_f32_e32 v53, v53
	ds_read_b128 v[118:121], v94 offset:6144
	ds_read_b128 v[114:117], v94 offset:6656
	s_waitcnt lgkmcnt(12)
	v_mfma_f32_32x32x16_bf16 v[18:33], v[142:145], v[200:203], v[18:33]
	v_exp_f32_e32 v54, v54
	v_exp_f32_e32 v55, v55
	v_exp_f32_e32 v56, v56
	v_exp_f32_e32 v57, v57
	s_waitcnt lgkmcnt(10)
	v_mfma_f32_32x32x16_bf16 v[2:17], v[138:141], v[86:89], v[2:17]
	v_exp_f32_e32 v58, v58
	v_exp_f32_e32 v59, v59
	v_exp_f32_e32 v60, v60
	v_exp_f32_e32 v61, v61
	s_waitcnt lgkmcnt(8)
	v_mfma_f32_32x32x16_bf16 v[18:33], v[138:141], v[90:93], v[18:33]
	v_exp_f32_e32 v62, v62
	v_exp_f32_e32 v63, v63
	v_exp_f32_e32 v64, v64
	v_exp_f32_e32 v65, v65
	s_add_i32 s3, s2, 0x2000
	s_cmpk_lg_i32 s2, 0x4000
	v_add_f32_e32 v86, v182, v195
	s_mov_b32 s43, s31
	s_cselect_b32 s31, s3, 0
	s_add_i32 s30, s30, 2
	v_lshl_add_u64 v[178:179], v[178:179], 0, s[54:55]
	s_mov_b32 s42, s2
	v_add_f32_e32 v182, v86, v204
	s_cmp_gt_u32 s30, 56
	s_waitcnt vmcnt(2) lgkmcnt(0)
	s_barrier
; #define WAIT_BAR(N) asm volatile("s_waitcnt vmcnt(" #N ") lgkmcnt(0)\n\ts_barrier":::"memory")
;   #define RESC() do{ if(resc){ asm volatile("s_waitcnt lgkmcnt(0)":::"memory"); \
;       _Pragma("unroll") for(int d_=0;d_<2;++d_) _Pragma("unroll") for(int r=0;r<16;++r)o[d_][r]*=wsf[crow(r,hi)]; } }while(0)
;   #define ROT() do{sl_prev=sl_cur;sl_cur=sl_next;sl_next=(sl_next==(NSLOT-1)*SLOTB)?0:sl_next+SLOTB;}while(0)
;   #define ENDW(tt) do{ if((tt)+3<NT){WAIT_BAR(2);} else if((tt)+2<NT){WAIT_BAR(1);} else {WAIT_BAR(0);} }while(0)
;     ...
;   int t=1;
;     ...
;   for(;t+5<NT;t+=2){
;     STEP(pB0,pB1,pA0,pA1,t,true,true,true);     WAIT_BAR(2); RESC(); ROT();
;     STEP(pA0,pA1,pB0,pB1,t+1,true,true,true);   WAIT_BAR(2); RESC(); ROT();
;   }
;     ...
;   for(;t+1<NT;t+=2){
;     STEP(pB0,pB1,pA0,pA1,t,(t+3<NT),(t+1<NT),(t+1<NT));       ENDW(t);   RESC(); ROT();
;     STEP(pA0,pA1,pB0,pB1,t+1,(t+4<NT),(t+2<NT),(t+2<NT));     ENDW(t+1); RESC(); ROT();
	s_cbranch_scc0 .LBB0_717
	s_and_b32 s3, s29, 0x3fffffc0
	s_cmp_lg_u32 0, -1
	s_cselect_b32 s2, 0, 0
	s_add_i32 s22, s2, 0x6000
	s_lshl_b32 s3, s3, 2
	v_add_u32_e32 v86, s22, v193
	s_add_i32 s22, s3, 0
	v_add3_u32 v178, v86, v192, v194
	ds_read_b64_tr_b16 v[192:193], v190 offset:32768
	ds_read_b64_tr_b16 v[194:195], v190 offset:33280
	v_add_f32_e32 v86, v66, v67
	v_add_f32_e32 v86, v68, v86
	v_add_f32_e32 v86, v69, v86
	v_add_f32_e32 v86, v70, v86
	v_add_f32_e32 v86, v71, v86
	v_cvt_pk_bf16_f32 v158, v66, v67
	v_cvt_pk_bf16_f32 v159, v68, v69
	s_waitcnt lgkmcnt(9)
	v_mfma_f32_32x32x16_bf16 v[98:113], v[82:85], v[154:157], v[34:49]
	ds_read_b64_tr_b16 v[66:67], v190 offset:36864
	ds_read_b64_tr_b16 v[68:69], v190 offset:37376
	v_add_f32_e32 v82, v72, v86
	v_add_f32_e32 v82, v73, v82
	v_add_f32_e32 v82, v74, v82
	v_add_f32_e32 v138, v75, v82
	v_cvt_pk_bf16_f32 v160, v70, v71
	v_cvt_pk_bf16_f32 v161, v72, v73
	s_waitcnt lgkmcnt(10)
	v_mfma_f32_32x32x16_bf16 v[82:97], v[166:169], v[154:157], v[34:49]
	ds_read_b64_tr_b16 v[70:71], v190 offset:33792
	ds_read_b64_tr_b16 v[72:73], v190 offset:34304
	v_add_f32_e32 v138, v76, v138
	v_add_f32_e32 v138, v77, v138
	v_add_f32_e32 v138, v78, v138
	v_add_f32_e32 v138, v79, v138
	v_cvt_pk_bf16_f32 v150, v74, v75
	v_cvt_pk_bf16_f32 v151, v76, v77
	s_waitcnt lgkmcnt(11)
	v_mfma_f32_32x32x16_bf16 v[98:113], v[170:173], v[146:149], v[98:113]
	ds_read_b64_tr_b16 v[74:75], v190 offset:37888
	ds_read_b64_tr_b16 v[76:77], v190 offset:38400
	v_add_f32_e32 v138, v80, v138
	v_add_f32_e32 v138, v81, v138
	v_add_f32_e32 v138, v50, v138
	v_add_f32_e32 v138, v51, v138
	v_cvt_pk_bf16_f32 v152, v78, v79
	v_cvt_pk_bf16_f32 v153, v80, v81
	s_waitcnt lgkmcnt(12)
	v_mfma_f32_32x32x16_bf16 v[82:97], v[162:165], v[146:149], v[82:97]
	ds_read_b64_tr_b16 v[78:79], v190 offset:34816
	ds_read_b64_tr_b16 v[80:81], v190 offset:35328
	s_waitcnt lgkmcnt(13)
	v_mfma_f32_32x32x16_bf16 v[98:113], v[126:129], v[134:137], v[98:113]
	v_add_f32_e32 v126, v52, v138
	v_add_f32_e32 v126, v53, v126
	v_add_f32_e32 v126, v54, v126
	v_add_f32_e32 v126, v55, v126
	v_cvt_pk_bf16_f32 v142, v50, v51
	v_cvt_pk_bf16_f32 v143, v52, v53
	ds_read_b64_tr_b16 v[50:51], v190 offset:38912
	ds_read_b64_tr_b16 v[52:53], v190 offset:39424
	s_waitcnt lgkmcnt(14)
	v_mfma_f32_32x32x16_bf16 v[82:97], v[122:125], v[134:137], v[82:97]
	v_add_f32_e32 v122, v56, v126
	v_add_f32_e32 v122, v57, v122
	v_add_f32_e32 v122, v58, v122
	v_add_f32_e32 v122, v59, v122
	v_cvt_pk_bf16_f32 v144, v54, v55
	v_cvt_pk_bf16_f32 v145, v56, v57
	ds_read_b64_tr_b16 v[54:55], v190 offset:35840
	ds_read_b64_tr_b16 v[56:57], v190 offset:36352
	s_waitcnt lgkmcnt(14)
	v_mfma_f32_32x32x16_bf16 v[98:113], v[118:121], v[130:133], v[98:113]
	v_add_f32_e32 v118, v60, v122
	v_add_f32_e32 v118, v61, v118
	v_add_f32_e32 v118, v62, v118
	v_add_f32_e32 v118, v63, v118
	v_cvt_pk_bf16_f32 v138, v58, v59
	v_cvt_pk_bf16_f32 v139, v60, v61
	ds_read_b64_tr_b16 v[58:59], v190 offset:39936
	ds_read_b64_tr_b16 v[60:61], v190 offset:40448
	v_mfma_f32_32x32x16_bf16 v[82:97], v[114:117], v[130:133], v[82:97]
	v_add_f32_e32 v114, v64, v118
	v_add_f32_e32 v114, v65, v114
	v_add_f32_e32 v114, 0, v114
	v_cvt_pk_bf16_f32 v140, v62, v63
	v_cvt_pk_bf16_f32 v141, v64, v65
	s_mov_b64 s[30:31], 0x1f0000
	s_add_i32 s2, s2, s28
	v_lshl_add_u64 v[62:63], v[176:177], 0, s[30:31]
	s_add_i32 s3, s2, 0x4000
	s_mov_b32 s23, m0
	s_mov_b32 m0, s3
	s_nop 0
	global_load_lds_dwordx4 v[62:63], off
	s_mov_b32 m0, s23
	s_mov_b64 s[28:29], 0x1e0000
	v_lshl_add_u64 v[62:63], v[174:175], 0, s[28:29]
	s_mov_b32 s3, m0
	s_mov_b32 m0, s26
	s_nop 0
	global_load_lds_dwordx4 v[62:63], off
	s_mov_b32 m0, s3
	v_add_f32_e32 v179, v182, v114
	s_waitcnt lgkmcnt(14)
	v_mfma_f32_32x32x16_bf16 v[2:17], v[158:161], v[192:195], v[2:17]
	v_exp_f32_e32 v98, v98
	v_exp_f32_e32 v99, v99
	v_exp_f32_e32 v100, v100
	v_exp_f32_e32 v101, v101
	s_waitcnt lgkmcnt(12)
	v_mfma_f32_32x32x16_bf16 v[18:33], v[158:161], v[66:69], v[18:33]
	v_exp_f32_e32 v102, v102
	v_exp_f32_e32 v103, v103
	v_exp_f32_e32 v104, v104
	v_exp_f32_e32 v105, v105
	ds_read_b128 v[62:65], v191
	ds_read_b128 v[162:165], v191 offset:512
	s_waitcnt lgkmcnt(12)
	v_mfma_f32_32x32x16_bf16 v[2:17], v[150:153], v[70:73], v[2:17]
	v_exp_f32_e32 v106, v106
	v_exp_f32_e32 v107, v107
	v_exp_f32_e32 v108, v108
	v_exp_f32_e32 v109, v109
	ds_read_b128 v[70:73], v191 offset:2048
	ds_read_b128 v[166:169], v191 offset:2560
	s_waitcnt lgkmcnt(12)
	v_mfma_f32_32x32x16_bf16 v[18:33], v[150:153], v[74:77], v[18:33]
	v_exp_f32_e32 v110, v110
	v_exp_f32_e32 v111, v111
	v_exp_f32_e32 v112, v112
	v_exp_f32_e32 v113, v113
	ds_read_b128 v[74:77], v191 offset:4096
	ds_read_b128 v[170:173], v191 offset:4608
	s_waitcnt lgkmcnt(12)
	v_mfma_f32_32x32x16_bf16 v[2:17], v[142:145], v[78:81], v[2:17]
	v_exp_f32_e32 v82, v82
	v_exp_f32_e32 v83, v83
	v_exp_f32_e32 v84, v84
	v_exp_f32_e32 v85, v85
	ds_read_b128 v[78:81], v191 offset:6144
	ds_read_b128 v[66:69], v191 offset:6656
	s_waitcnt lgkmcnt(12)
	v_mfma_f32_32x32x16_bf16 v[18:33], v[142:145], v[50:53], v[18:33]
	v_exp_f32_e32 v86, v86
	v_exp_f32_e32 v87, v87
	v_exp_f32_e32 v88, v88
	v_exp_f32_e32 v89, v89
	s_waitcnt lgkmcnt(10)
	v_mfma_f32_32x32x16_bf16 v[2:17], v[138:141], v[54:57], v[2:17]
	v_exp_f32_e32 v90, v90
	v_exp_f32_e32 v91, v91
	v_exp_f32_e32 v92, v92
	v_exp_f32_e32 v93, v93
	s_waitcnt lgkmcnt(8)
	v_mfma_f32_32x32x16_bf16 v[18:33], v[138:141], v[58:61], v[18:33]
	v_exp_f32_e32 v94, v94
	v_exp_f32_e32 v95, v95
	v_exp_f32_e32 v96, v96
	v_exp_f32_e32 v97, v97
	s_waitcnt vmcnt(2) lgkmcnt(0)
	s_barrier
; #define WAIT_BAR(N) asm volatile("s_waitcnt vmcnt(" #N ") lgkmcnt(0)\n\ts_barrier":::"memory")
;   #define RESC() do{ if(resc){ asm volatile("s_waitcnt lgkmcnt(0)":::"memory"); \
;       _Pragma("unroll") for(int d_=0;d_<2;++d_) _Pragma("unroll") for(int r=0;r<16;++r)o[d_][r]*=wsf[crow(r,hi)]; } }while(0)
;   #define ROT() do{sl_prev=sl_cur;sl_cur=sl_next;sl_next=(sl_next==(NSLOT-1)*SLOTB)?0:sl_next+SLOTB;}while(0)
;   #define ENDW(tt) do{ if((tt)+3<NT){WAIT_BAR(2);} else if((tt)+2<NT){WAIT_BAR(1);} else {WAIT_BAR(0);} }while(0)
;     ...
;   int t=1;
;     ...
;   for(;t+5<NT;t+=2){
;     STEP(pB0,pB1,pA0,pA1,t,true,true,true);     WAIT_BAR(2); RESC(); ROT();
;     STEP(pA0,pA1,pB0,pB1,t+1,true,true,true);   WAIT_BAR(2); RESC(); ROT();
;   }
;     ...
;   for(;t+1<NT;t+=2){
;     STEP(pB0,pB1,pA0,pA1,t,(t+3<NT),(t+1<NT),(t+1<NT));       ENDW(t);   RESC(); ROT();
;     STEP(pA0,pA1,pB0,pB1,t+1,(t+4<NT),(t+2<NT),(t+2<NT));     ENDW(t+1); RESC(); ROT();
	ds_read_b64_tr_b16 v[192:193], v190 offset:40960
	ds_read_b64_tr_b16 v[194:195], v190 offset:41472
	v_add_f32_e32 v50, v98, v99
	v_add_f32_e32 v50, v100, v50
	v_add_f32_e32 v50, v101, v50
	v_add_f32_e32 v50, v102, v50
	v_add_f32_e32 v50, v103, v50
	v_cvt_pk_bf16_f32 v158, v98, v99
	v_cvt_pk_bf16_f32 v159, v100, v101
	s_waitcnt lgkmcnt(9)
	v_mfma_f32_32x32x16_bf16 v[114:129], v[62:65], v[154:157], v[34:49]
	ds_read_b64_tr_b16 v[98:99], v190 offset:45056
	ds_read_b64_tr_b16 v[100:101], v190 offset:45568
	v_add_f32_e32 v50, v104, v50
	v_add_f32_e32 v50, v105, v50
	v_add_f32_e32 v50, v106, v50
	v_add_f32_e32 v138, v107, v50
	s_waitcnt lgkmcnt(10)
	v_mfma_f32_32x32x16_bf16 v[50:65], v[162:165], v[154:157], v[34:49]
	v_cvt_pk_bf16_f32 v160, v102, v103
	v_cvt_pk_bf16_f32 v161, v104, v105
	ds_read_b64_tr_b16 v[102:103], v190 offset:41984
	ds_read_b64_tr_b16 v[104:105], v190 offset:42496
	s_waitcnt lgkmcnt(11)
	v_mfma_f32_32x32x16_bf16 v[114:129], v[70:73], v[146:149], v[114:129]
	v_add_f32_e32 v70, v108, v138
	v_add_f32_e32 v70, v109, v70
	v_add_f32_e32 v70, v110, v70
	v_add_f32_e32 v138, v111, v70
	v_cvt_pk_bf16_f32 v150, v106, v107
	v_cvt_pk_bf16_f32 v151, v108, v109
	ds_read_b64_tr_b16 v[70:71], v190 offset:46080
	ds_read_b64_tr_b16 v[72:73], v190 offset:46592
	s_waitcnt lgkmcnt(12)
	v_mfma_f32_32x32x16_bf16 v[50:65], v[166:169], v[146:149], v[50:65]
	v_add_f32_e32 v106, v112, v138
	v_add_f32_e32 v106, v113, v106
	v_add_f32_e32 v106, v82, v106
	v_add_f32_e32 v138, v83, v106
	v_cvt_pk_bf16_f32 v152, v110, v111
	v_cvt_pk_bf16_f32 v153, v112, v113
	ds_read_b64_tr_b16 v[106:107], v190 offset:43008
	ds_read_b64_tr_b16 v[108:109], v190 offset:43520
	s_waitcnt lgkmcnt(13)
	v_mfma_f32_32x32x16_bf16 v[114:129], v[74:77], v[134:137], v[114:129]
	v_add_f32_e32 v74, v84, v138
	v_add_f32_e32 v74, v85, v74
	v_add_f32_e32 v74, v86, v74
	v_add_f32_e32 v110, v87, v74
	v_cvt_pk_bf16_f32 v142, v82, v83
	v_cvt_pk_bf16_f32 v143, v84, v85
	ds_read_b64_tr_b16 v[74:75], v190 offset:47104
	ds_read_b64_tr_b16 v[76:77], v190 offset:47616
	s_waitcnt lgkmcnt(14)
	v_mfma_f32_32x32x16_bf16 v[50:65], v[170:173], v[134:137], v[50:65]
	v_add_f32_e32 v82, v88, v110
	v_add_f32_e32 v82, v89, v82
	v_add_f32_e32 v82, v90, v82
	v_add_f32_e32 v82, v91, v82
	v_cvt_pk_bf16_f32 v144, v86, v87
	v_cvt_pk_bf16_f32 v145, v88, v89
	ds_read_b64_tr_b16 v[86:87], v190 offset:44032
	ds_read_b64_tr_b16 v[88:89], v190 offset:44544
	s_waitcnt lgkmcnt(14)
	v_mfma_f32_32x32x16_bf16 v[114:129], v[78:81], v[130:133], v[114:129]
	v_add_f32_e32 v78, v92, v82
	v_add_f32_e32 v78, v93, v78
	v_add_f32_e32 v78, v94, v78
	v_add_f32_e32 v82, v95, v78
	v_cvt_pk_bf16_f32 v138, v90, v91
	v_cvt_pk_bf16_f32 v139, v92, v93
	ds_read_b64_tr_b16 v[78:79], v190 offset:48128
	ds_read_b64_tr_b16 v[80:81], v190 offset:48640
	v_mfma_f32_32x32x16_bf16 v[50:65], v[66:69], v[130:133], v[50:65]
	v_add_f32_e32 v66, v96, v82
	v_add_f32_e32 v66, v97, v66
	v_add_f32_e32 v66, 0, v66
	v_cvt_pk_bf16_f32 v140, v94, v95
	v_cvt_pk_bf16_f32 v141, v96, v97
	s_mov_b64 s[42:43], 0x1f8000
	v_add_f32_e32 v179, v179, v66
	v_lshl_add_u64 v[66:67], v[176:177], 0, s[42:43]
	s_mov_b32 s3, m0
	s_mov_b32 m0, s27
	s_nop 0
	global_load_lds_dwordx4 v[66:67], off
	s_mov_b32 m0, s3
	s_mov_b64 s[28:29], 0x1e8000
	v_lshl_add_u64 v[66:67], v[174:175], 0, s[28:29]
	s_add_i32 s3, s2, 0x8000
	s_mov_b32 s23, m0
	s_mov_b32 m0, s3
	s_nop 0
	global_load_lds_dwordx4 v[66:67], off
	s_mov_b32 m0, s23
	s_waitcnt lgkmcnt(14)
	v_mfma_f32_32x32x16_bf16 v[2:17], v[158:161], v[192:195], v[2:17]
	v_exp_f32_e32 v114, v114
	v_exp_f32_e32 v115, v115
	v_exp_f32_e32 v116, v116
	v_exp_f32_e32 v117, v117
	s_waitcnt lgkmcnt(12)
	v_mfma_f32_32x32x16_bf16 v[18:33], v[158:161], v[98:101], v[18:33]
	v_exp_f32_e32 v118, v118
	v_exp_f32_e32 v119, v119
	v_exp_f32_e32 v120, v120
	v_exp_f32_e32 v121, v121
	ds_read_b128 v[66:69], v191 offset:8192
	ds_read_b128 v[90:93], v191 offset:8704
	s_waitcnt lgkmcnt(12)
	v_mfma_f32_32x32x16_bf16 v[2:17], v[150:153], v[102:105], v[2:17]
	v_exp_f32_e32 v122, v122
	v_exp_f32_e32 v123, v123
	v_exp_f32_e32 v124, v124
	v_exp_f32_e32 v125, v125
	ds_read_b128 v[94:97], v191 offset:10240
	ds_read_b128 v[162:165], v191 offset:10752
	s_waitcnt lgkmcnt(12)
	v_mfma_f32_32x32x16_bf16 v[18:33], v[150:153], v[70:73], v[18:33]
	v_exp_f32_e32 v126, v126
	v_exp_f32_e32 v127, v127
	v_exp_f32_e32 v128, v128
	v_exp_f32_e32 v129, v129
	ds_read_b128 v[166:169], v191 offset:12288
	ds_read_b128 v[170:173], v191 offset:12800
	s_waitcnt lgkmcnt(12)
	v_mfma_f32_32x32x16_bf16 v[2:17], v[142:145], v[106:109], v[2:17]
	v_exp_f32_e32 v50, v50
	v_exp_f32_e32 v51, v51
	v_exp_f32_e32 v52, v52
	v_exp_f32_e32 v53, v53
	ds_read_b128 v[192:195], v191 offset:14336
	ds_read_b128 v[82:85], v191 offset:14848
	s_waitcnt lgkmcnt(12)
	v_mfma_f32_32x32x16_bf16 v[18:33], v[142:145], v[74:77], v[18:33]
	v_exp_f32_e32 v54, v54
	v_exp_f32_e32 v55, v55
	v_exp_f32_e32 v56, v56
	v_exp_f32_e32 v57, v57
	s_waitcnt lgkmcnt(10)
	v_mfma_f32_32x32x16_bf16 v[2:17], v[138:141], v[86:89], v[2:17]
	v_exp_f32_e32 v58, v58
	v_exp_f32_e32 v59, v59
	v_exp_f32_e32 v60, v60
	v_exp_f32_e32 v61, v61
	s_waitcnt lgkmcnt(8)
	v_mfma_f32_32x32x16_bf16 v[18:33], v[138:141], v[78:81], v[18:33]
	v_exp_f32_e32 v62, v62
	v_exp_f32_e32 v63, v63
	v_exp_f32_e32 v64, v64
	v_exp_f32_e32 v65, v65
	s_waitcnt vmcnt(2) lgkmcnt(0)
	s_barrier
; #define WAIT_BAR(N) asm volatile("s_waitcnt vmcnt(" #N ") lgkmcnt(0)\n\ts_barrier":::"memory")
;   #define RESC() do{ if(resc){ asm volatile("s_waitcnt lgkmcnt(0)":::"memory"); \
;       _Pragma("unroll") for(int d_=0;d_<2;++d_) _Pragma("unroll") for(int r=0;r<16;++r)o[d_][r]*=wsf[crow(r,hi)]; } }while(0)
;   #define ROT() do{sl_prev=sl_cur;sl_cur=sl_next;sl_next=(sl_next==(NSLOT-1)*SLOTB)?0:sl_next+SLOTB;}while(0)
;   #define ENDW(tt) do{ if((tt)+3<NT){WAIT_BAR(2);} else if((tt)+2<NT){WAIT_BAR(1);} else {WAIT_BAR(0);} }while(0)
;     ...
;   int t=1;
;     ...
;   for(;t+5<NT;t+=2){
;     STEP(pB0,pB1,pA0,pA1,t,true,true,true);     WAIT_BAR(2); RESC(); ROT();
;     STEP(pA0,pA1,pB0,pB1,t+1,true,true,true);   WAIT_BAR(2); RESC(); ROT();
;   }
;     ...
;   for(;t+1<NT;t+=2){
;     STEP(pB0,pB1,pA0,pA1,t,(t+3<NT),(t+1<NT),(t+1<NT));       ENDW(t);   RESC(); ROT();
;     STEP(pA0,pA1,pB0,pB1,t+1,(t+4<NT),(t+2<NT),(t+2<NT));     ENDW(t+1); RESC(); ROT();
	ds_read_b64_tr_b16 v[86:87], v190 offset:24576
	ds_read_b64_tr_b16 v[88:89], v190 offset:25088
	v_add_f32_e32 v70, v114, v115
	v_add_f32_e32 v70, v116, v70
	v_add_f32_e32 v70, v117, v70
	v_add_f32_e32 v70, v118, v70
	v_add_f32_e32 v70, v119, v70
	v_cvt_pk_bf16_f32 v158, v114, v115
	v_cvt_pk_bf16_f32 v159, v116, v117
	s_waitcnt lgkmcnt(9)
	v_mfma_f32_32x32x16_bf16 v[98:113], v[66:69], v[154:157], v[34:49]
	ds_read_b64_tr_b16 v[114:115], v190 offset:28672
	ds_read_b64_tr_b16 v[116:117], v190 offset:29184
	v_add_f32_e32 v66, v120, v70
	v_add_f32_e32 v66, v121, v66
	v_add_f32_e32 v66, v122, v66
	v_add_f32_e32 v138, v123, v66
	v_cvt_pk_bf16_f32 v160, v118, v119
	v_cvt_pk_bf16_f32 v161, v120, v121
	s_waitcnt lgkmcnt(10)
	v_mfma_f32_32x32x16_bf16 v[66:81], v[90:93], v[154:157], v[34:49]
	ds_read_b64_tr_b16 v[90:91], v190 offset:25600
	ds_read_b64_tr_b16 v[92:93], v190 offset:26112
	s_waitcnt lgkmcnt(11)
	v_mfma_f32_32x32x16_bf16 v[98:113], v[94:97], v[146:149], v[98:113]
	v_add_f32_e32 v94, v124, v138
	v_add_f32_e32 v94, v125, v94
	v_add_f32_e32 v94, v126, v94
	v_add_f32_e32 v118, v127, v94
	v_cvt_pk_bf16_f32 v150, v122, v123
	v_cvt_pk_bf16_f32 v151, v124, v125
	ds_read_b64_tr_b16 v[94:95], v190 offset:29696
	ds_read_b64_tr_b16 v[96:97], v190 offset:30208
	v_add_f32_e32 v118, v128, v118
	v_add_f32_e32 v118, v129, v118
	v_add_f32_e32 v118, v50, v118
	v_add_f32_e32 v122, v51, v118
	v_cvt_pk_bf16_f32 v152, v126, v127
	v_cvt_pk_bf16_f32 v153, v128, v129
	s_waitcnt lgkmcnt(12)
	v_mfma_f32_32x32x16_bf16 v[66:81], v[162:165], v[146:149], v[66:81]
	ds_read_b64_tr_b16 v[118:119], v190 offset:26624
	ds_read_b64_tr_b16 v[120:121], v190 offset:27136
	v_add_f32_e32 v122, v52, v122
	v_add_f32_e32 v122, v53, v122
	v_add_f32_e32 v122, v54, v122
	v_add_f32_e32 v122, v55, v122
	v_cvt_pk_bf16_f32 v142, v50, v51
	v_cvt_pk_bf16_f32 v143, v52, v53
	s_waitcnt lgkmcnt(13)
	v_mfma_f32_32x32x16_bf16 v[98:113], v[166:169], v[134:137], v[98:113]
	ds_read_b64_tr_b16 v[50:51], v190 offset:30720
	ds_read_b64_tr_b16 v[52:53], v190 offset:31232
	v_add_f32_e32 v122, v56, v122
	v_add_f32_e32 v122, v57, v122
	v_add_f32_e32 v122, v58, v122
	v_add_f32_e32 v122, v59, v122
	v_cvt_pk_bf16_f32 v144, v54, v55
	v_cvt_pk_bf16_f32 v145, v56, v57
	s_waitcnt lgkmcnt(14)
	v_mfma_f32_32x32x16_bf16 v[66:81], v[170:173], v[134:137], v[66:81]
	ds_read_b64_tr_b16 v[54:55], v190 offset:27648
	ds_read_b64_tr_b16 v[56:57], v190 offset:28160
	v_add_f32_e32 v122, v60, v122
	v_add_f32_e32 v122, v61, v122
	v_add_f32_e32 v122, v62, v122
	v_add_f32_e32 v122, v63, v122
	v_cvt_pk_bf16_f32 v138, v58, v59
	v_cvt_pk_bf16_f32 v139, v60, v61
	s_waitcnt lgkmcnt(14)
	v_mfma_f32_32x32x16_bf16 v[98:113], v[192:195], v[130:133], v[98:113]
	ds_read_b64_tr_b16 v[58:59], v190 offset:31744
	ds_read_b64_tr_b16 v[60:61], v190 offset:32256
	v_mfma_f32_32x32x16_bf16 v[66:81], v[82:85], v[130:133], v[66:81]
	v_add_f32_e32 v82, v64, v122
	v_add_f32_e32 v82, v65, v82
	v_add_f32_e32 v82, 0, v82
	v_cvt_pk_bf16_f32 v140, v62, v63
	v_cvt_pk_bf16_f32 v141, v64, v65
	v_lshl_add_u64 v[62:63], v[174:175], 0, s[30:31]
	s_add_i32 s2, s2, 0xa000
	s_mov_b32 s3, m0
	s_mov_b32 m0, s2
	s_nop 0
	global_load_lds_dwordx4 v[62:63], off
	s_mov_b32 m0, s3
	v_add_f32_e32 v176, v179, v82
	s_waitcnt lgkmcnt(14)
	v_mfma_f32_32x32x16_bf16 v[2:17], v[158:161], v[86:89], v[2:17]
	v_exp_f32_e32 v98, v98
	v_exp_f32_e32 v99, v99
	v_exp_f32_e32 v100, v100
	v_exp_f32_e32 v101, v101
	s_waitcnt lgkmcnt(12)
	v_mfma_f32_32x32x16_bf16 v[18:33], v[158:161], v[114:117], v[18:33]
	v_exp_f32_e32 v102, v102
	v_exp_f32_e32 v103, v103
	v_exp_f32_e32 v104, v104
	v_exp_f32_e32 v105, v105
	ds_read_b128 v[62:65], v191 offset:16384
	ds_read_b128 v[122:125], v191 offset:16896
	s_waitcnt lgkmcnt(12)
	v_mfma_f32_32x32x16_bf16 v[2:17], v[150:153], v[90:93], v[2:17]
	v_exp_f32_e32 v106, v106
	v_exp_f32_e32 v107, v107
	v_exp_f32_e32 v108, v108
	v_exp_f32_e32 v109, v109
	ds_read_b128 v[126:129], v191 offset:18432
	ds_read_b128 v[162:165], v191 offset:18944
	s_waitcnt lgkmcnt(12)
	v_mfma_f32_32x32x16_bf16 v[18:33], v[150:153], v[94:97], v[18:33]
	v_exp_f32_e32 v110, v110
	v_exp_f32_e32 v111, v111
	v_exp_f32_e32 v112, v112
	v_exp_f32_e32 v113, v113
	ds_read_b128 v[166:169], v191 offset:20480
	ds_read_b128 v[170:173], v191 offset:20992
	s_waitcnt lgkmcnt(12)
	v_mfma_f32_32x32x16_bf16 v[2:17], v[142:145], v[118:121], v[2:17]
	v_exp_f32_e32 v66, v66
	v_exp_f32_e32 v67, v67
	v_exp_f32_e32 v68, v68
	v_exp_f32_e32 v69, v69
	ds_read_b128 v[118:121], v191 offset:22528
	ds_read_b128 v[114:117], v191 offset:23040
	s_waitcnt lgkmcnt(12)
	v_mfma_f32_32x32x16_bf16 v[18:33], v[142:145], v[50:53], v[18:33]
	v_exp_f32_e32 v70, v70
	v_exp_f32_e32 v71, v71
	v_exp_f32_e32 v72, v72
	v_exp_f32_e32 v73, v73
	s_waitcnt lgkmcnt(10)
	v_mfma_f32_32x32x16_bf16 v[2:17], v[138:141], v[54:57], v[2:17]
	v_exp_f32_e32 v74, v74
	v_exp_f32_e32 v75, v75
	v_exp_f32_e32 v76, v76
	v_exp_f32_e32 v77, v77
	s_waitcnt lgkmcnt(8)
	v_mfma_f32_32x32x16_bf16 v[18:33], v[138:141], v[58:61], v[18:33]
	v_exp_f32_e32 v78, v78
	v_exp_f32_e32 v79, v79
	v_exp_f32_e32 v80, v80
	v_exp_f32_e32 v81, v81
	s_waitcnt vmcnt(1) lgkmcnt(0)
	s_barrier
; #define WAIT_BAR(N) asm volatile("s_waitcnt vmcnt(" #N ") lgkmcnt(0)\n\ts_barrier":::"memory")
;   #define RESC() do{ if(resc){ asm volatile("s_waitcnt lgkmcnt(0)":::"memory"); \
;       _Pragma("unroll") for(int d_=0;d_<2;++d_) _Pragma("unroll") for(int r=0;r<16;++r)o[d_][r]*=wsf[crow(r,hi)]; } }while(0)
;   #define ROT() do{sl_prev=sl_cur;sl_cur=sl_next;sl_next=(sl_next==(NSLOT-1)*SLOTB)?0:sl_next+SLOTB;}while(0)
;   #define ENDW(tt) do{ if((tt)+3<NT){WAIT_BAR(2);} else if((tt)+2<NT){WAIT_BAR(1);} else {WAIT_BAR(0);} }while(0)
;     ...
;   int t=1;
;     ...
;   for(;t+5<NT;t+=2){
;     STEP(pB0,pB1,pA0,pA1,t,true,true,true);     WAIT_BAR(2); RESC(); ROT();
;     STEP(pA0,pA1,pB0,pB1,t+1,true,true,true);   WAIT_BAR(2); RESC(); ROT();
;   }
;     ...
;   for(;t+1<NT;t+=2){
;     STEP(pB0,pB1,pA0,pA1,t,(t+3<NT),(t+1<NT),(t+1<NT));       ENDW(t);   RESC(); ROT();
;     STEP(pA0,pA1,pB0,pB1,t+1,(t+4<NT),(t+2<NT),(t+2<NT));     ENDW(t+1); RESC(); ROT();
	ds_read_b64_tr_b16 v[192:193], v190 offset:32768
	ds_read_b64_tr_b16 v[194:195], v190 offset:33280
	v_add_f32_e32 v50, v98, v99
	v_add_f32_e32 v50, v100, v50
	v_add_f32_e32 v50, v101, v50
	v_add_f32_e32 v50, v102, v50
	v_add_f32_e32 v50, v103, v50
	v_cvt_pk_bf16_f32 v158, v98, v99
	v_cvt_pk_bf16_f32 v159, v100, v101
	s_waitcnt lgkmcnt(9)
	v_mfma_f32_32x32x16_bf16 v[82:97], v[62:65], v[154:157], v[34:49]
	ds_read_b64_tr_b16 v[98:99], v190 offset:36864
	ds_read_b64_tr_b16 v[100:101], v190 offset:37376
	v_add_f32_e32 v50, v104, v50
	v_add_f32_e32 v50, v105, v50
	v_add_f32_e32 v50, v106, v50
	v_add_f32_e32 v138, v107, v50
	s_waitcnt lgkmcnt(10)
	v_mfma_f32_32x32x16_bf16 v[50:65], v[122:125], v[154:157], v[34:49]
	v_cvt_pk_bf16_f32 v160, v102, v103
	v_cvt_pk_bf16_f32 v161, v104, v105
	ds_read_b64_tr_b16 v[122:123], v190 offset:33792
	ds_read_b64_tr_b16 v[124:125], v190 offset:34304
	v_add_f32_e32 v102, v108, v138
	v_add_f32_e32 v102, v109, v102
	v_add_f32_e32 v102, v110, v102
	v_add_f32_e32 v102, v111, v102
	v_cvt_pk_bf16_f32 v150, v106, v107
	v_cvt_pk_bf16_f32 v151, v108, v109
	s_waitcnt lgkmcnt(11)
	v_mfma_f32_32x32x16_bf16 v[82:97], v[126:129], v[146:149], v[82:97]
	ds_read_b64_tr_b16 v[104:105], v190 offset:37888
	ds_read_b64_tr_b16 v[106:107], v190 offset:38400
	s_waitcnt lgkmcnt(12)
	v_mfma_f32_32x32x16_bf16 v[50:65], v[162:165], v[146:149], v[50:65]
	v_add_f32_e32 v102, v112, v102
	v_add_f32_e32 v102, v113, v102
	v_add_f32_e32 v102, v66, v102
	v_add_f32_e32 v102, v67, v102
	v_cvt_pk_bf16_f32 v152, v110, v111
	v_cvt_pk_bf16_f32 v153, v112, v113
	ds_read_b64_tr_b16 v[108:109], v190 offset:34816
	ds_read_b64_tr_b16 v[110:111], v190 offset:35328
	v_add_f32_e32 v102, v68, v102
	v_add_f32_e32 v102, v69, v102
	v_add_f32_e32 v102, v70, v102
	v_add_f32_e32 v102, v71, v102
	v_cvt_pk_bf16_f32 v142, v66, v67
	v_cvt_pk_bf16_f32 v143, v68, v69
	s_waitcnt lgkmcnt(13)
	v_mfma_f32_32x32x16_bf16 v[82:97], v[166:169], v[134:137], v[82:97]
	ds_read_b64_tr_b16 v[66:67], v190 offset:38912
	ds_read_b64_tr_b16 v[68:69], v190 offset:39424
	s_waitcnt lgkmcnt(14)
	v_mfma_f32_32x32x16_bf16 v[50:65], v[170:173], v[134:137], v[50:65]
	v_add_f32_e32 v102, v72, v102
	v_add_f32_e32 v102, v73, v102
	v_add_f32_e32 v102, v74, v102
	v_add_f32_e32 v102, v75, v102
	v_cvt_pk_bf16_f32 v144, v70, v71
	v_cvt_pk_bf16_f32 v145, v72, v73
	ds_read_b64_tr_b16 v[70:71], v190 offset:35840
	ds_read_b64_tr_b16 v[72:73], v190 offset:36352
	v_add_f32_e32 v102, v76, v102
	v_add_f32_e32 v102, v77, v102
	v_add_f32_e32 v102, v78, v102
	v_add_f32_e32 v102, v79, v102
	v_cvt_pk_bf16_f32 v138, v74, v75
	v_cvt_pk_bf16_f32 v139, v76, v77
	s_waitcnt lgkmcnt(14)
	v_mfma_f32_32x32x16_bf16 v[82:97], v[118:121], v[130:133], v[82:97]
	ds_read_b64_tr_b16 v[74:75], v190 offset:39936
	ds_read_b64_tr_b16 v[76:77], v190 offset:40448
	v_mfma_f32_32x32x16_bf16 v[50:65], v[114:117], v[130:133], v[50:65]
	v_add_f32_e32 v102, v80, v102
	v_add_f32_e32 v102, v81, v102
	v_add_f32_e32 v102, 0, v102
	v_cvt_pk_bf16_f32 v140, v78, v79
	v_cvt_pk_bf16_f32 v141, v80, v81
	v_lshl_add_u64 v[78:79], v[174:175], 0, s[42:43]
	s_mov_b32 s2, m0
	s_mov_b32 m0, s26
	s_nop 0
	global_load_lds_dwordx4 v[78:79], off
	s_mov_b32 m0, s2
	v_add_f32_e32 v102, v176, v102
	s_waitcnt lgkmcnt(14)
	v_mfma_f32_32x32x16_bf16 v[2:17], v[158:161], v[192:195], v[2:17]
	v_exp_f32_e32 v82, v82
	v_exp_f32_e32 v83, v83
	v_exp_f32_e32 v84, v84
	v_exp_f32_e32 v85, v85
	s_waitcnt lgkmcnt(12)
	v_mfma_f32_32x32x16_bf16 v[18:33], v[158:161], v[98:101], v[18:33]
	v_exp_f32_e32 v86, v86
	v_exp_f32_e32 v87, v87
	v_exp_f32_e32 v88, v88
	v_exp_f32_e32 v89, v89
	ds_read_b128 v[112:115], v191
	ds_read_b128 v[116:119], v191 offset:512
	s_waitcnt lgkmcnt(12)
	v_mfma_f32_32x32x16_bf16 v[2:17], v[150:153], v[122:125], v[2:17]
	v_exp_f32_e32 v90, v90
	v_exp_f32_e32 v91, v91
	v_exp_f32_e32 v92, v92
	v_exp_f32_e32 v93, v93
	ds_read_b128 v[120:123], v191 offset:2048
	ds_read_b128 v[124:127], v191 offset:2560
	s_waitcnt lgkmcnt(12)
	v_mfma_f32_32x32x16_bf16 v[18:33], v[150:153], v[104:107], v[18:33]
	v_exp_f32_e32 v94, v94
	v_exp_f32_e32 v95, v95
	v_exp_f32_e32 v96, v96
	v_exp_f32_e32 v97, v97
	ds_read_b128 v[104:107], v191 offset:4096
	ds_read_b128 v[162:165], v191 offset:4608
	s_waitcnt lgkmcnt(12)
	v_mfma_f32_32x32x16_bf16 v[2:17], v[142:145], v[108:111], v[2:17]
	v_exp_f32_e32 v50, v50
	v_exp_f32_e32 v51, v51
	v_exp_f32_e32 v52, v52
	v_exp_f32_e32 v53, v53
	ds_read_b128 v[108:111], v191 offset:6144
	ds_read_b128 v[98:101], v191 offset:6656
	s_waitcnt lgkmcnt(12)
	v_mfma_f32_32x32x16_bf16 v[18:33], v[142:145], v[66:69], v[18:33]
	v_exp_f32_e32 v54, v54
	v_exp_f32_e32 v55, v55
	v_exp_f32_e32 v56, v56
	v_exp_f32_e32 v57, v57
	s_waitcnt lgkmcnt(10)
	v_mfma_f32_32x32x16_bf16 v[2:17], v[138:141], v[70:73], v[2:17]
	v_exp_f32_e32 v58, v58
	v_exp_f32_e32 v59, v59
	v_exp_f32_e32 v60, v60
	v_exp_f32_e32 v61, v61
	s_waitcnt lgkmcnt(8)
	v_mfma_f32_32x32x16_bf16 v[18:33], v[138:141], v[74:77], v[18:33]
	v_exp_f32_e32 v62, v62
	v_exp_f32_e32 v63, v63
	v_exp_f32_e32 v64, v64
	v_exp_f32_e32 v65, v65
	s_waitcnt vmcnt(0) lgkmcnt(0)
	s_barrier
; #define SBAR() __builtin_amdgcn_sched_barrier(0)
; #define WAIT_BAR(N) asm volatile("s_waitcnt vmcnt(" #N ") lgkmcnt(0)\n\ts_barrier":::"memory")
;   #define RESC() do{ if(resc){ asm volatile("s_waitcnt lgkmcnt(0)":::"memory"); \
;       _Pragma("unroll") for(int d_=0;d_<2;++d_) _Pragma("unroll") for(int r=0;r<16;++r)o[d_][r]*=wsf[crow(r,hi)]; } }while(0)
;   #define ROT() do{sl_prev=sl_cur;sl_cur=sl_next;sl_next=(sl_next==(NSLOT-1)*SLOTB)?0:sl_next+SLOTB;}while(0)
;   #define PKW(P,B) cvtpk_s(P[B],P[B+1])
;   #define ENDW(tt) do{ if((tt)+3<NT){WAIT_BAR(2);} else if((tt)+2<NT){WAIT_BAR(1);} else {WAIT_BAR(0);} }while(0)
;     ...
;   int t=1;
;     ...
;   for(;t+5<NT;t+=2){
;     STEP(pB0,pB1,pA0,pA1,t,true,true,true);     WAIT_BAR(2); RESC(); ROT();
;     STEP(pA0,pA1,pB0,pB1,t+1,true,true,true);   WAIT_BAR(2); RESC(); ROT();
;   }
;     ...
;   for(;t+1<NT;t+=2){
;     STEP(pB0,pB1,pA0,pA1,t,(t+3<NT),(t+1<NT),(t+1<NT));       ENDW(t);   RESC(); ROT();
;     STEP(pA0,pA1,pB0,pB1,t+1,(t+4<NT),(t+2<NT),(t+2<NT));     ENDW(t+1); RESC(); ROT();
;   }
;   STEP(pB0,pB1,pA0,pA1,NT-1,false,false,false); RESC();
;   { float sacc=pB0[0]+pB0[1]; _Pragma("unroll") for(int r=2;r<16;++r)sacc+=pB0[r]; _Pragma("unroll") for(int r=0;r<16;++r)sacc+=pB1[r]; l_reg+=sacc;
;     pw0=(u32x4){PKW(pB0,0),PKW(pB0,2),PKW(pB0,4),PKW(pB0,6)};pw1=(u32x4){PKW(pB0,8),PKW(pB0,10),PKW(pB0,12),PKW(pB0,14)};pw2=(u32x4){PKW(pB1,0),PKW(pB1,2),PKW(pB1,4),PKW(pB1,6)};pw3=(u32x4){PKW(pB1,8),PKW(pB1,10),PKW(pB1,12),PKW(pB1,14)};
;     SBAR(); pv(o,vb0+sl_cur,PAF(0),PAF(1),PAF(2),PAF(3)); }
	ds_read_b64_tr_b16 v[166:167], v190 offset:40960
	ds_read_b64_tr_b16 v[168:169], v190 offset:41472
	v_add_f32_e32 v66, v82, v83
	v_add_f32_e32 v66, v84, v66
	v_add_f32_e32 v66, v85, v66
	v_add_f32_e32 v66, v86, v66
	v_add_f32_e32 v103, v87, v66
	v_cvt_pk_bf16_f32 v158, v82, v83
	v_cvt_pk_bf16_f32 v159, v84, v85
	s_waitcnt lgkmcnt(9)
	v_mfma_f32_32x32x16_bf16 v[66:81], v[112:115], v[154:157], v[34:49]
	ds_read_b64_tr_b16 v[82:83], v190 offset:45056
	ds_read_b64_tr_b16 v[84:85], v190 offset:45568
	s_waitcnt lgkmcnt(10)
	v_mfma_f32_32x32x16_bf16 v[34:49], v[116:119], v[154:157], v[34:49]
	v_add_f32_e32 v103, v88, v103
	v_add_f32_e32 v103, v89, v103
	v_add_f32_e32 v103, v90, v103
	v_add_f32_e32 v103, v91, v103
	v_cvt_pk_bf16_f32 v160, v86, v87
	v_cvt_pk_bf16_f32 v161, v88, v89
	ds_read_b64_tr_b16 v[86:87], v190 offset:41984
	ds_read_b64_tr_b16 v[88:89], v190 offset:42496
	v_add_f32_e32 v103, v92, v103
	v_add_f32_e32 v103, v93, v103
	v_add_f32_e32 v103, v94, v103
	v_add_f32_e32 v103, v95, v103
	v_cvt_pk_bf16_f32 v150, v90, v91
	v_cvt_pk_bf16_f32 v151, v92, v93
	s_waitcnt lgkmcnt(11)
	v_mfma_f32_32x32x16_bf16 v[66:81], v[120:123], v[146:149], v[66:81]
	ds_read_b64_tr_b16 v[90:91], v190 offset:46080
	ds_read_b64_tr_b16 v[92:93], v190 offset:46592
	s_waitcnt lgkmcnt(12)
	v_mfma_f32_32x32x16_bf16 v[34:49], v[124:127], v[146:149], v[34:49]
	v_add_f32_e32 v103, v96, v103
	v_add_f32_e32 v103, v97, v103
	v_add_f32_e32 v103, v50, v103
	v_add_f32_e32 v103, v51, v103
	v_cvt_pk_bf16_f32 v152, v94, v95
	v_cvt_pk_bf16_f32 v153, v96, v97
	ds_read_b64_tr_b16 v[94:95], v190 offset:43008
	ds_read_b64_tr_b16 v[96:97], v190 offset:43520
	v_add_f32_e32 v103, v52, v103
	v_add_f32_e32 v103, v53, v103
	v_add_f32_e32 v103, v54, v103
	v_add_f32_e32 v103, v55, v103
	v_cvt_pk_bf16_f32 v142, v50, v51
	v_cvt_pk_bf16_f32 v143, v52, v53
	s_waitcnt lgkmcnt(13)
	v_mfma_f32_32x32x16_bf16 v[66:81], v[104:107], v[134:137], v[66:81]
	ds_read_b64_tr_b16 v[50:51], v190 offset:47104
	ds_read_b64_tr_b16 v[52:53], v190 offset:47616
	s_waitcnt lgkmcnt(14)
	v_mfma_f32_32x32x16_bf16 v[34:49], v[162:165], v[134:137], v[34:49]
	v_add_f32_e32 v103, v56, v103
	v_add_f32_e32 v103, v57, v103
	v_add_f32_e32 v103, v58, v103
	v_add_f32_e32 v103, v59, v103
	v_cvt_pk_bf16_f32 v144, v54, v55
	v_cvt_pk_bf16_f32 v145, v56, v57
	ds_read_b64_tr_b16 v[54:55], v190 offset:44032
	ds_read_b64_tr_b16 v[56:57], v190 offset:44544
	v_add_f32_e32 v103, v60, v103
	v_add_f32_e32 v103, v61, v103
	v_add_f32_e32 v103, v62, v103
	v_add_f32_e32 v103, v63, v103
	v_cvt_pk_bf16_f32 v138, v58, v59
	v_cvt_pk_bf16_f32 v139, v60, v61
	s_waitcnt lgkmcnt(14)
	v_mfma_f32_32x32x16_bf16 v[66:81], v[108:111], v[130:133], v[66:81]
	ds_read_b64_tr_b16 v[58:59], v190 offset:48128
	ds_read_b64_tr_b16 v[60:61], v190 offset:48640
	v_mfma_f32_32x32x16_bf16 v[34:49], v[98:101], v[130:133], v[34:49]
	v_add_f32_e32 v98, v64, v103
	v_add_f32_e32 v98, v65, v98
	v_add_f32_e32 v98, 0, v98
	v_cvt_pk_bf16_f32 v140, v62, v63
	v_cvt_pk_bf16_f32 v141, v64, v65
	s_waitcnt lgkmcnt(14)
	v_mfma_f32_32x32x16_bf16 v[2:17], v[158:161], v[166:169], v[2:17]
	s_nop 1
	v_exp_f32_e32 v66, v66
	v_exp_f32_e32 v67, v67
	v_exp_f32_e32 v68, v68
	v_exp_f32_e32 v69, v69
	s_waitcnt lgkmcnt(12)
	v_mfma_f32_32x32x16_bf16 v[18:33], v[158:161], v[82:85], v[18:33]
	v_exp_f32_e32 v70, v70
	v_exp_f32_e32 v71, v71
	v_exp_f32_e32 v72, v72
	v_exp_f32_e32 v73, v73
	s_waitcnt lgkmcnt(10)
	v_mfma_f32_32x32x16_bf16 v[2:17], v[150:153], v[86:89], v[2:17]
	v_exp_f32_e32 v74, v74
	v_exp_f32_e32 v75, v75
	v_exp_f32_e32 v76, v76
	v_exp_f32_e32 v77, v77
	s_waitcnt lgkmcnt(8)
	v_mfma_f32_32x32x16_bf16 v[18:33], v[150:153], v[90:93], v[18:33]
	v_exp_f32_e32 v78, v78
	v_exp_f32_e32 v79, v79
	v_exp_f32_e32 v80, v80
	v_exp_f32_e32 v81, v81
	s_waitcnt lgkmcnt(6)
	v_mfma_f32_32x32x16_bf16 v[2:17], v[142:145], v[94:97], v[2:17]
	v_exp_f32_e32 v34, v34
	v_exp_f32_e32 v35, v35
	v_exp_f32_e32 v36, v36
	v_exp_f32_e32 v37, v37
	s_waitcnt lgkmcnt(4)
	v_mfma_f32_32x32x16_bf16 v[18:33], v[142:145], v[50:53], v[18:33]
	v_exp_f32_e32 v38, v38
	v_exp_f32_e32 v39, v39
	v_exp_f32_e32 v40, v40
	v_exp_f32_e32 v41, v41
	s_waitcnt lgkmcnt(2)
	v_mfma_f32_32x32x16_bf16 v[2:17], v[138:141], v[54:57], v[2:17]
	v_exp_f32_e32 v42, v42
	v_exp_f32_e32 v43, v43
	v_exp_f32_e32 v44, v44
	v_exp_f32_e32 v45, v45
	s_waitcnt lgkmcnt(0)
	v_mfma_f32_32x32x16_bf16 v[18:33], v[138:141], v[58:61], v[18:33]
	v_exp_f32_e32 v46, v46
	v_exp_f32_e32 v47, v47
	v_exp_f32_e32 v48, v48
	v_exp_f32_e32 v49, v49
	v_add_f32_e32 v50, v66, v67
	v_add_f32_e32 v50, v68, v50
	v_add_f32_e32 v50, v69, v50
	v_add_f32_e32 v50, v70, v50
	v_add_f32_e32 v50, v71, v50
	v_add_f32_e32 v50, v72, v50
	v_add_f32_e32 v50, v73, v50
	v_add_f32_e32 v50, v74, v50
	v_add_f32_e32 v50, v75, v50
	v_add_f32_e32 v50, v76, v50
	v_add_f32_e32 v50, v77, v50
	v_add_f32_e32 v50, v78, v50
	v_add_f32_e32 v50, v79, v50
	v_add_f32_e32 v50, v80, v50
	v_add_f32_e32 v50, v81, v50
	v_add_f32_e32 v50, v34, v50
	v_add_f32_e32 v50, v35, v50
	v_add_f32_e32 v50, v36, v50
	v_add_f32_e32 v50, v37, v50
	v_add_f32_e32 v50, v38, v50
	v_add_f32_e32 v50, v39, v50
	v_add_f32_e32 v50, v40, v50
	v_add_f32_e32 v50, v41, v50
	v_add_f32_e32 v50, v42, v50
	v_add_f32_e32 v50, v43, v50
	v_add_f32_e32 v50, v44, v50
	v_add_f32_e32 v50, v45, v50
	v_add_f32_e32 v50, v46, v50
	v_add_f32_e32 v50, v47, v50
	v_add_f32_e32 v50, v48, v50
	v_add_f32_e32 v50, v49, v50
	v_add_f32_e32 v51, v102, v98
	v_add_f32_e32 v50, v51, v50
	v_cvt_pk_bf16_f32 v34, v34, v35
	v_cvt_pk_bf16_f32 v52, v66, v67
	v_cvt_pk_bf16_f32 v53, v68, v69
	v_cvt_pk_bf16_f32 v54, v70, v71
	v_cvt_pk_bf16_f32 v55, v72, v73
	v_cvt_pk_bf16_f32 v56, v74, v75
	v_cvt_pk_bf16_f32 v57, v76, v77
	v_cvt_pk_bf16_f32 v58, v78, v79
	v_cvt_pk_bf16_f32 v59, v80, v81
	v_cvt_pk_bf16_f32 v35, v36, v37
	v_cvt_pk_bf16_f32 v36, v38, v39
	v_cvt_pk_bf16_f32 v37, v40, v41
	v_cvt_pk_bf16_f32 v38, v42, v43
	v_cvt_pk_bf16_f32 v39, v44, v45
	v_cvt_pk_bf16_f32 v40, v46, v47
	v_cvt_pk_bf16_f32 v41, v48, v49
	ds_read_b64_tr_b16 v[42:43],v178 offset:0
	ds_read_b64_tr_b16 v[44:45],v178 offset:512
	ds_read_b64_tr_b16 v[46:47],v178 offset:1024
	ds_read_b64_tr_b16 v[48:49],v178 offset:1536
	ds_read_b64_tr_b16 v[60:61],v178 offset:2048
	ds_read_b64_tr_b16 v[62:63],v178 offset:2560
	ds_read_b64_tr_b16 v[64:65],v178 offset:3072
	ds_read_b64_tr_b16 v[66:67],v178 offset:3584
	s_waitcnt lgkmcnt(0)
; __device__ __forceinline__ int crow(int r,int hi){return (r&3)+8*(r>>2)+4*hi;}
; #define SBAR() __builtin_amdgcn_sched_barrier(0)
; __device__ __forceinline__ void pv(f32x16*o,int vb,bf16x8 pa0,bf16x8 pa1,bf16x8 pa2,bf16x8 pa3){
;   #pragma unroll
;   for(int d0=0;d0<2;++d0){s16x4 lo[4],hi[4];
;     #pragma unroll
;     for(int ks=0;ks<4;++ks){
;       asm volatile("ds_read_b64_tr_b16 %0,%1 offset:%c2":"=&v"(lo[ks]):"v"(vb),"i"(d0*4096+ks*1024):"memory");
;       asm volatile("ds_read_b64_tr_b16 %0,%1 offset:%c2":"=&v"(hi[ks]):"v"(vb),"i"(d0*4096+ks*1024+512):"memory");}
;     asm volatile("s_waitcnt lgkmcnt(0)":::"memory");SBAR();
;     ...
;     o[d0]=__builtin_amdgcn_mfma_f32_32x32x16_bf16(pa0,PK(0),o[d0],0,0,0);
;     o[d0]=__builtin_amdgcn_mfma_f32_32x32x16_bf16(pa1,PK(1),o[d0],0,0,0);
;     o[d0]=__builtin_amdgcn_mfma_f32_32x32x16_bf16(pa2,PK(2),o[d0],0,0,0);
;     o[d0]=__builtin_amdgcn_mfma_f32_32x32x16_bf16(pa3,PK(3),o[d0],0,0,0);
;     ...
;   {auto rr=__builtin_amdgcn_permlane32_swap(__float_as_uint(l_reg),__float_as_uint(l_reg),false,false);l_reg=__uint_as_float(rr[0])+__uint_as_float(rr[1]);}
;   if(hi==0)wsf[32+r32]=l_reg;asm volatile("s_waitcnt lgkmcnt(0)":::"memory");
;   float rli[16];
;   #pragma unroll
;   for(int r=0;r<16;++r)rli[r]=__builtin_amdgcn_rcpf(wsf[32+crow(r,hi)]);
;   bf16*Ow=O+(rowbase+q0+wid*QBLK)*OP+h*D;
;   { bf16*stg=(bf16*)(shm+LDS_OST)+wid*2048;
;     #pragma unroll
;     for(int r=0;r<16;++r){const int orow=crow(r,hi);
;       #pragma unroll
;       for(int d0=0;d0<2;++d0)stg[orow*64+d0*32+r32]=__float2bfloat16(o[d0][r]*rli[r]);}
;     asm volatile("s_waitcnt lgkmcnt(0)":::"memory");
;     #pragma unroll
;     for(int i=0;i<4;++i){const int row=i*8+(lane>>3),ch=lane&7; const u32x4 v=*(const u32x4*)(stg+row*64+ch*8); ATTN_STORE16(Ow+(long)row*OP+ch*8,v);} }
;   asm volatile("s_waitcnt lgkmcnt(0)\n\ts_barrier":::"memory");
	s_nop 0
	v_mfma_f32_32x32x16_bf16 v[2:17], v[52:55], v[42:45], v[2:17]
	ds_read_b64_tr_b16 v[42:43],v178 offset:4096
	ds_read_b64_tr_b16 v[44:45],v178 offset:4608
	v_mfma_f32_32x32x16_bf16 v[2:17], v[56:59], v[46:49], v[2:17]
	ds_read_b64_tr_b16 v[46:47],v178 offset:5120
	ds_read_b64_tr_b16 v[48:49],v178 offset:5632
	v_mfma_f32_32x32x16_bf16 v[2:17], v[34:37], v[60:63], v[2:17]
	ds_read_b64_tr_b16 v[60:61],v178 offset:6144
	ds_read_b64_tr_b16 v[62:63],v178 offset:6656
	v_mfma_f32_32x32x16_bf16 v[2:17], v[38:41], v[64:67], v[2:17]
	ds_read_b64_tr_b16 v[64:65],v178 offset:7168
	ds_read_b64_tr_b16 v[66:67],v178 offset:7680
	s_waitcnt lgkmcnt(0)
	v_mfma_f32_32x32x16_bf16 v[18:33], v[52:55], v[42:45], v[18:33]
	v_cmp_gt_u32_e32 vcc, 32, v1
	v_mfma_f32_32x32x16_bf16 v[18:33], v[56:59], v[46:49], v[18:33]
	v_mfma_f32_32x32x16_bf16 v[18:33], v[34:37], v[60:63], v[18:33]
	v_mov_b32_e32 v34, v50
	s_nop 1
	v_permlane32_swap_b32_e32 v50, v34
	v_mfma_f32_32x32x16_bf16 v[18:33], v[38:41], v[64:67], v[18:33]
	s_and_saveexec_b64 s[2:3], vcc
	v_add_f32_e32 v34, v50, v34
	v_lshl_add_u32 v35, v188, 2, s22
	ds_write_b32 v35, v34 offset:49280
	s_or_b64 exec, exec, s[2:3]
	s_waitcnt lgkmcnt(0)
	v_lshl_add_u32 v42, v189, 4, s22
	ds_read_b128 v[34:37], v42 offset:49280
	ds_read_b128 v[38:41], v42 offset:49312
	s_lshl_b64 s[2:3], s[6:7], 11
	s_lshl_b32 s6, s25, 12
	s_add_i32 s6, s6, 0
	s_waitcnt lgkmcnt(1)
	v_rcp_f32_e32 v43, v34
	v_rcp_f32_e32 v44, v35
	v_rcp_f32_e32 v45, v36
	v_rcp_f32_e32 v46, v37
	s_waitcnt lgkmcnt(0)
	v_rcp_f32_e32 v47, v38
	ds_read_b128 v[34:37], v42 offset:49344
	v_rcp_f32_e32 v48, v39
	v_rcp_f32_e32 v49, v40
	v_rcp_f32_e32 v50, v41
	ds_read_b128 v[38:41], v42 offset:49376
	v_lshlrev_b32_e32 v42, 9, v189
	v_lshlrev_b32_e32 v51, 1, v188
	v_mul_f32_e32 v2, v2, v43
	v_add3_u32 v42, s6, v42, v51
	v_cvt_pk_bf16_f32 v2, v2, s0
	ds_write_b16 v42, v2 offset:51200
	v_mul_f32_e32 v2, v18, v43
	v_cvt_pk_bf16_f32 v2, v2, s0
	ds_write_b16 v42, v2 offset:51264
	v_mul_f32_e32 v2, v3, v44
	v_cvt_pk_bf16_f32 v2, v2, s0
	ds_write_b16 v42, v2 offset:51328
	v_mul_f32_e32 v2, v19, v44
	v_cvt_pk_bf16_f32 v2, v2, s0
	ds_write_b16 v42, v2 offset:51392
	v_mul_f32_e32 v2, v4, v45
	v_cvt_pk_bf16_f32 v2, v2, s0
	ds_write_b16 v42, v2 offset:51456
	v_mul_f32_e32 v2, v20, v45
	v_cvt_pk_bf16_f32 v2, v2, s0
	ds_write_b16 v42, v2 offset:51520
	v_mul_f32_e32 v2, v5, v46
	v_cvt_pk_bf16_f32 v2, v2, s0
	ds_write_b16 v42, v2 offset:51584
	v_mul_f32_e32 v2, v21, v46
	v_cvt_pk_bf16_f32 v2, v2, s0
	ds_write_b16 v42, v2 offset:51648
	v_mul_f32_e32 v2, v6, v47
	v_cvt_pk_bf16_f32 v2, v2, s0
	ds_write_b16 v42, v2 offset:52224
	v_mul_f32_e32 v2, v22, v47
	v_cvt_pk_bf16_f32 v2, v2, s0
	ds_write_b16 v42, v2 offset:52288
	v_mul_f32_e32 v2, v7, v48
	v_cvt_pk_bf16_f32 v2, v2, s0
	ds_write_b16 v42, v2 offset:52352
	v_mul_f32_e32 v2, v23, v48
	v_cvt_pk_bf16_f32 v2, v2, s0
	ds_write_b16 v42, v2 offset:52416
	v_mul_f32_e32 v2, v8, v49
	v_cvt_pk_bf16_f32 v2, v2, s0
	ds_write_b16 v42, v2 offset:52480
	v_mul_f32_e32 v2, v24, v49
	v_cvt_pk_bf16_f32 v2, v2, s0
	s_waitcnt lgkmcnt(14)
	v_rcp_f32_e32 v34, v34
	ds_write_b16 v42, v2 offset:52544
	v_mul_f32_e32 v2, v9, v50
	v_cvt_pk_bf16_f32 v2, v2, s0
	ds_write_b16 v42, v2 offset:52608
	v_mul_f32_e32 v2, v25, v50
	v_cvt_pk_bf16_f32 v2, v2, s0
	v_rcp_f32_e32 v35, v35
	ds_write_b16 v42, v2 offset:52672
	v_mul_f32_e32 v2, v10, v34
	v_cvt_pk_bf16_f32 v2, v2, s0
	ds_write_b16 v42, v2 offset:53248
	v_mul_f32_e32 v2, v26, v34
	v_cvt_pk_bf16_f32 v2, v2, s0
	v_rcp_f32_e32 v36, v36
	ds_write_b16 v42, v2 offset:53312
	v_mul_f32_e32 v2, v11, v35
	v_cvt_pk_bf16_f32 v2, v2, s0
	ds_write_b16 v42, v2 offset:53376
	v_mul_f32_e32 v2, v27, v35
	v_cvt_pk_bf16_f32 v2, v2, s0
	v_rcp_f32_e32 v37, v37
	ds_write_b16 v42, v2 offset:53440
	v_mul_f32_e32 v2, v12, v36
	v_cvt_pk_bf16_f32 v2, v2, s0
	ds_write_b16 v42, v2 offset:53504
	v_mul_f32_e32 v2, v28, v36
	v_cvt_pk_bf16_f32 v2, v2, s0
	s_waitcnt lgkmcnt(14)
	v_rcp_f32_e32 v38, v38
	ds_write_b16 v42, v2 offset:53568
	v_mul_f32_e32 v2, v13, v37
	v_cvt_pk_bf16_f32 v2, v2, s0
	ds_write_b16 v42, v2 offset:53632
	v_mul_f32_e32 v2, v29, v37
	v_cvt_pk_bf16_f32 v2, v2, s0
	v_rcp_f32_e32 v39, v39
	ds_write_b16 v42, v2 offset:53696
	v_mul_f32_e32 v2, v14, v38
	v_cvt_pk_bf16_f32 v2, v2, s0
	ds_write_b16 v42, v2 offset:54272
	v_mul_f32_e32 v2, v30, v38
	v_cvt_pk_bf16_f32 v2, v2, s0
	v_rcp_f32_e32 v40, v40
	ds_write_b16 v42, v2 offset:54336
	v_mul_f32_e32 v2, v15, v39
	v_cvt_pk_bf16_f32 v2, v2, s0
	ds_write_b16 v42, v2 offset:54400
	v_mul_f32_e32 v2, v31, v39
	v_cvt_pk_bf16_f32 v2, v2, s0
	v_rcp_f32_e32 v41, v41
	ds_write_b16 v42, v2 offset:54464
	v_mul_f32_e32 v2, v16, v40
	v_cvt_pk_bf16_f32 v2, v2, s0
	ds_write_b16 v42, v2 offset:54528
	v_mul_f32_e32 v2, v32, v40
	v_cvt_pk_bf16_f32 v2, v2, s0
	ds_write_b16 v42, v2 offset:54592
	v_mul_f32_e32 v2, v17, v41
	v_cvt_pk_bf16_f32 v2, v2, s0
	ds_write_b16 v42, v2 offset:54656
	v_mul_f32_e32 v2, v33, v41
	v_cvt_pk_bf16_f32 v2, v2, s0
	ds_write_b16 v42, v2 offset:54720
	v_lshlrev_b32_e32 v2, 1, v187
	v_and_b32_e32 v182, 0x70, v2
	v_lshrrev_b32_e32 v1, 3, v1
	v_add_u32_e32 v14, s6, v182
	s_waitcnt lgkmcnt(0)
	v_lshl_add_u32 v2, v1, 7, v14
	v_or_b32_e32 v15, 8, v1
	ds_read_b128 v[2:5], v2 offset:51200
	v_lshl_add_u32 v6, v15, 7, v14
	s_add_u32 s2, s39, s2
	ds_read_b128 v[6:9], v6 offset:51200
	s_addc_u32 s3, s40, s3
	v_lshl_add_u64 v[10:11], s[2:3], 0, v[182:183]
	v_lshlrev_b32_e32 v182, 11, v1
	v_lshl_add_u64 v[12:13], v[10:11], 0, v[182:183]
	v_lshlrev_b32_e32 v182, 11, v15
	s_waitcnt lgkmcnt(1)
	global_store_dwordx4 v[12:13], v[2:5], off
	s_mov_b64 s[2:3], 0
	s_nop 0
	v_lshl_add_u64 v[2:3], v[10:11], 0, v[182:183]
	s_waitcnt lgkmcnt(0)
	global_store_dwordx4 v[2:3], v[6:9], off
	s_nop 1
	v_or_b32_e32 v6, 16, v1
	v_lshl_add_u32 v2, v6, 7, v14
	v_or_b32_e32 v1, 24, v1
	ds_read_b128 v[2:5], v2 offset:51200
	v_lshlrev_b32_e32 v182, 11, v6
	v_lshl_add_u32 v6, v1, 7, v14
	ds_read_b128 v[6:9], v6 offset:51200
	v_lshl_add_u64 v[12:13], v[10:11], 0, v[182:183]
	v_lshlrev_b32_e32 v182, 11, v1
	s_waitcnt lgkmcnt(1)
	global_store_dwordx4 v[12:13], v[2:5], off
	s_nop 1
	v_lshl_add_u64 v[2:3], v[10:11], 0, v[182:183]
	s_waitcnt lgkmcnt(0)
	global_store_dwordx4 v[2:3], v[6:9], off
	s_waitcnt lgkmcnt(0)
	s_barrier

; #define PG8_STAGE(bufoff, gbase, voff) do { _Pragma("unroll") for (int _i = 0; _i < 2; ++_i) \
;         __builtin_amdgcn_global_load_lds((const unsigned*)((const char*)(gbase) + (voff)[_i]), (PG8_LAS unsigned*)(lds + (bufoff) + ldsw + _i * 8192), 16, 0, 0); } while (0)
; #define PG8_LDA(dst, b, h) do { _Pragma("unroll") for (int m = 0; m < 4; ++m) _Pragma("unroll") for (int k = 0; k < 2; ++k) dst[m][k] = *(const PG8_LAS bf16x8*)(lds + PG8_SA(b, h) + aoff + m * 2048 + k * 1024); } while (0)
; #define PG8_LDB(dst, b, h) do { _Pragma("unroll") for (int n = 0; n < 2; ++n) _Pragma("unroll") for (int k = 0; k < 2; ++k) dst[n][k] = *(const PG8_LAS bf16x8*)(lds + PG8_SB(b, h) + boff + n * 2048 + k * 1024); } while (0)
; #define PG8_WAIT_V(n) asm volatile("s_waitcnt vmcnt(" #n ")" ::: "memory")
; #define PG8_WAIT_L(n) asm volatile("s_waitcnt lgkmcnt(" #n ")" ::: "memory")
; #define PG8_BAR __builtin_amdgcn_s_barrier()
; template <class Epi, class Sched, bool ALIGN_EPI = false, bool SP2 = false, bool F8 = false, bool BTILED = false, bool ATILED = false>
; __device__ __forceinline__ void gemm_phase(PG8_LAS unsigned char* lds, const Gemm g, const Sched& S, const Epi& E) {
;     ...
;         for (int t = 0; t < nt; t += 2) {
;             const bool last = (t == nt - 2);
;             const char* a1 = cA + (size_t)(t + 1) * kstepA;
;             const char* a2 = last ? nA : cA + (size_t)(t + 2) * kstepA; const char* b2 = last ? nB : cB + (size_t)(t + 2) * kstepB;
;             const char* a3 = a2 + kstepA; const char* b3 = b2 + kstepB;
;             if (last && has_next) S.a_ready(nxt);
;             if constexpr (SP2) {
;             PG8_LDB(B0, 0, 0); PG8_LDB(B1, 0, 1); PG8_SCHED; PG8_LDA(At, 0, 0); PG8_STAGE(PG8_SA(1, 1), a1 + hstepA, voffA);
;             PG8_WAIT_V(8); PG8_WAIT_L(0); PG8_BAR; PG8_MMA(0, 0, At, B0); PG8_MMA(0, 1, At, B1); PG8_BAR; PG8_SCHED;
;             PG8_LDA(At, 0, 1); PG8_STAGE(PG8_SB(0, 0), b2, voffB); PG8_STAGE(PG8_SB(0, 1), b2 + hstepB, voffB); PG8_STAGE(PG8_SA(0, 0), a2, voffA);
;             PG8_WAIT_V(8); PG8_WAIT_L(0); PG8_BAR; PG8_MMA(1, 0, At, B0); PG8_MMA(1, 1, At, B1); PG8_BAR; PG8_SCHED;
;             PG8_LDB(B0, 1, 0); PG8_LDB(B1, 1, 1); PG8_SCHED; PG8_LDA(At, 1, 0); PG8_STAGE(PG8_SA(0, 1), a2 + hstepA, voffA);
;             PG8_WAIT_V(8); PG8_WAIT_L(0); PG8_BAR; PG8_MMA(0, 0, At, B0); PG8_MMA(0, 1, At, B1); PG8_BAR; PG8_SCHED;
.LBB0_1078:
	s_add_u32 s20, s2, 0xfffc0080
	s_addc_u32 s21, s3, -1
	s_add_i32 s48, 0, 0x10000
	s_cmp_eq_u32 s47, 12
	s_cselect_b32 s23, s15, s21
	s_cselect_b32 s22, s43, s20
	v_add_u32_e32 v140, s48, v143
	s_cselect_b32 s21, s13, s46
	s_cselect_b32 s20, s44, s45
	s_add_i32 s50, 0, 0x14000
	ds_read_b128 v[146:149], v140
	ds_read_b128 v[150:153], v140 offset:1024
	ds_read_b128 v[154:157], v140 offset:2048
	ds_read_b128 v[158:161], v140 offset:3072
	v_add_u32_e32 v140, s50, v143
	ds_read_b128 v[162:165], v140
	ds_read_b128 v[166:169], v140 offset:1024
	ds_read_b128 v[170:173], v140 offset:2048
	ds_read_b128 v[174:177], v140 offset:3072
	v_lshl_add_u64 v[140:141], s[2:3], 0, v[136:137]
	s_add_i32 m0, s31, 0xc000
	ds_read_b128 v[178:181], v145
	ds_read_b128 v[186:189], v145 offset:1024
	ds_read_b128 v[190:193], v145 offset:2048
	ds_read_b128 v[194:197], v145 offset:3072
	ds_read_b128 v[198:201], v145 offset:4096
	ds_read_b128 v[202:205], v145 offset:5120
	ds_read_b128 v[206:209], v145 offset:6144
	ds_read_b128 v[210:213], v145 offset:7168
	global_load_lds_dwordx4 v[140:141], off
	v_lshl_add_u64 v[140:141], s[2:3], 0, v[138:139]
	s_add_i32 m0, s31, 0xe000
	s_nop 0
	global_load_lds_dwordx4 v[140:141], off
	s_waitcnt vmcnt(8)
	s_waitcnt lgkmcnt(0)
	s_barrier
	s_setprio 1
	s_waitcnt lgkmcnt(0)
	v_mfma_f32_16x16x32_bf16 v[126:129], v[146:149], v[178:181], v[126:129]
	v_mfma_f32_16x16x32_bf16 v[122:125], v[154:157], v[178:181], v[122:125]
	v_mfma_f32_16x16x32_bf16 v[118:121], v[146:149], v[190:193], v[118:121]
	v_mfma_f32_16x16x32_bf16 v[110:113], v[154:157], v[190:193], v[110:113]
	v_mfma_f32_16x16x32_bf16 v[102:105], v[146:149], v[198:201], v[102:105]
	v_mfma_f32_16x16x32_bf16 v[94:97], v[154:157], v[198:201], v[94:97]
	v_mfma_f32_16x16x32_bf16 v[86:89], v[146:149], v[206:209], v[86:89]
	v_mfma_f32_16x16x32_bf16 v[78:81], v[154:157], v[206:209], v[78:81]
	v_mfma_f32_16x16x32_bf16 v[126:129], v[150:153], v[186:189], v[126:129]
	v_mfma_f32_16x16x32_bf16 v[122:125], v[158:161], v[186:189], v[122:125]
	v_mfma_f32_16x16x32_bf16 v[118:121], v[150:153], v[194:197], v[118:121]
	v_mfma_f32_16x16x32_bf16 v[110:113], v[158:161], v[194:197], v[110:113]
	v_mfma_f32_16x16x32_bf16 v[102:105], v[150:153], v[202:205], v[102:105]
	v_mfma_f32_16x16x32_bf16 v[94:97], v[158:161], v[202:205], v[94:97]
	v_mfma_f32_16x16x32_bf16 v[86:89], v[150:153], v[210:213], v[86:89]
	v_mfma_f32_16x16x32_bf16 v[78:81], v[158:161], v[210:213], v[78:81]
	s_setprio 0
	s_setprio 1
	v_mfma_f32_16x16x32_bf16 v[114:117], v[162:165], v[178:181], v[114:117]
	v_mfma_f32_16x16x32_bf16 v[106:109], v[170:173], v[178:181], v[106:109]
	v_mfma_f32_16x16x32_bf16 v[98:101], v[162:165], v[190:193], v[98:101]
	v_mfma_f32_16x16x32_bf16 v[90:93], v[170:173], v[190:193], v[90:93]
	v_mfma_f32_16x16x32_bf16 v[82:85], v[162:165], v[198:201], v[82:85]
	v_mfma_f32_16x16x32_bf16 v[74:77], v[170:173], v[198:201], v[74:77]
	v_mfma_f32_16x16x32_bf16 v[70:73], v[162:165], v[206:209], v[70:73]
	v_mfma_f32_16x16x32_bf16 v[66:69], v[170:173], v[206:209], v[66:69]
	v_mfma_f32_16x16x32_bf16 v[114:117], v[166:169], v[186:189], v[114:117]
	v_mfma_f32_16x16x32_bf16 v[106:109], v[174:177], v[186:189], v[106:109]
	v_mfma_f32_16x16x32_bf16 v[98:101], v[166:169], v[194:197], v[98:101]
	v_mfma_f32_16x16x32_bf16 v[90:93], v[174:177], v[194:197], v[90:93]
	v_mfma_f32_16x16x32_bf16 v[82:85], v[166:169], v[202:205], v[82:85]
	v_mfma_f32_16x16x32_bf16 v[74:77], v[174:177], v[202:205], v[74:77]
	v_mfma_f32_16x16x32_bf16 v[70:73], v[166:169], v[210:213], v[70:73]
	v_mfma_f32_16x16x32_bf16 v[66:69], v[174:177], v[210:213], v[66:69]
	s_setprio 0
	s_barrier
	s_add_i32 s48, s48, s30
	v_lshl_add_u64 v[140:141], s[20:21], 0, v[182:183]
	s_mov_b32 m0, s48
	ds_read_b128 v[178:181], v145 offset:16384
	ds_read_b128 v[186:189], v145 offset:17408
	ds_read_b128 v[190:193], v145 offset:18432
	ds_read_b128 v[194:197], v145 offset:19456
	ds_read_b128 v[198:201], v145 offset:20480
	ds_read_b128 v[202:205], v145 offset:21504
	ds_read_b128 v[206:209], v145 offset:22528
	ds_read_b128 v[210:213], v145 offset:23552
	global_load_lds_dwordx4 v[140:141], off
	s_add_i32 m0, s48, 0x2000
	s_add_u32 s48, s20, 0x40000
	v_lshl_add_u64 v[214:215], s[20:21], 0, v[130:131]
	s_addc_u32 s49, s21, 0
	s_add_i32 s50, s50, s30
	global_load_lds_dwordx4 v[214:215], off
	v_lshl_add_u64 v[216:217], s[48:49], 0, v[182:183]
	s_mov_b32 m0, s50
	v_lshl_add_u64 v[218:219], s[22:23], 0, v[132:133]
	global_load_lds_dwordx4 v[216:217], off
	v_lshl_add_u64 v[216:217], s[48:49], 0, v[130:131]
	s_add_i32 m0, s50, 0x2000
	s_nop 0
	global_load_lds_dwordx4 v[216:217], off
	v_lshl_add_u64 v[216:217], s[22:23], 0, v[134:135]
	s_mov_b32 m0, s31
	s_nop 0
	global_load_lds_dwordx4 v[216:217], off
	s_mov_b32 m0, s34
	s_nop 0
	global_load_lds_dwordx4 v[218:219], off
	s_waitcnt vmcnt(8)
	s_waitcnt lgkmcnt(0)
	s_barrier
; #define PG8_STAGE(bufoff, gbase, voff) do { _Pragma("unroll") for (int _i = 0; _i < 2; ++_i) \
;         __builtin_amdgcn_global_load_lds((const unsigned*)((const char*)(gbase) + (voff)[_i]), (PG8_LAS unsigned*)(lds + (bufoff) + ldsw + _i * 8192), 16, 0, 0); } while (0)
; #define PG8_LDA(dst, b, h) do { _Pragma("unroll") for (int m = 0; m < 4; ++m) _Pragma("unroll") for (int k = 0; k < 2; ++k) dst[m][k] = *(const PG8_LAS bf16x8*)(lds + PG8_SA(b, h) + aoff + m * 2048 + k * 1024); } while (0)
; #define PG8_LDB(dst, b, h) do { _Pragma("unroll") for (int n = 0; n < 2; ++n) _Pragma("unroll") for (int k = 0; k < 2; ++k) dst[n][k] = *(const PG8_LAS bf16x8*)(lds + PG8_SB(b, h) + boff + n * 2048 + k * 1024); } while (0)
; #define PG8_WAIT_V(n) asm volatile("s_waitcnt vmcnt(" #n ")" ::: "memory")
; #define PG8_WAIT_L(n) asm volatile("s_waitcnt lgkmcnt(" #n ")" ::: "memory")
; #define PG8_BAR __builtin_amdgcn_s_barrier()
; #define PG8_SCHED __builtin_amdgcn_sched_barrier(0)
; template <class Epi, class Sched, bool ALIGN_EPI = false, bool SP2 = false, bool F8 = false, bool BTILED = false, bool ATILED = false>
; __device__ __forceinline__ void gemm_phase(PG8_LAS unsigned char* lds, const Gemm g, const Sched& S, const Epi& E) {
;     ...
;             PG8_LDA(At, 0, 1); PG8_STAGE(PG8_SB(0, 0), b2, voffB); PG8_STAGE(PG8_SB(0, 1), b2 + hstepB, voffB); PG8_STAGE(PG8_SA(0, 0), a2, voffA);
;             PG8_WAIT_V(8); PG8_WAIT_L(0); PG8_BAR; PG8_MMA(1, 0, At, B0); PG8_MMA(1, 1, At, B1); PG8_BAR; PG8_SCHED;
;             PG8_LDB(B0, 1, 0); PG8_LDB(B1, 1, 1); PG8_SCHED; PG8_LDA(At, 1, 0); PG8_STAGE(PG8_SA(0, 1), a2 + hstepA, voffA);
;             PG8_WAIT_V(8); PG8_WAIT_L(0); PG8_BAR; PG8_MMA(0, 0, At, B0); PG8_MMA(0, 1, At, B1); PG8_BAR; PG8_SCHED;
;             PG8_LDA(At, 1, 1); PG8_STAGE(PG8_SB(1, 0), b3, voffB); PG8_STAGE(PG8_SB(1, 1), b3 + hstepB, voffB); PG8_STAGE(PG8_SA(1, 0), a3, voffA);
;             PG8_WAIT_V(8); PG8_WAIT_L(0); PG8_BAR; PG8_MMA(1, 0, At, B0); PG8_MMA(1, 1, At, B1); PG8_BAR; PG8_SCHED;
	s_setprio 1
	s_waitcnt lgkmcnt(0)
	v_mfma_f32_16x16x32_bf16 v[62:65], v[146:149], v[178:181], v[62:65]
	v_mfma_f32_16x16x32_bf16 v[58:61], v[154:157], v[178:181], v[58:61]
	v_mfma_f32_16x16x32_bf16 v[54:57], v[146:149], v[190:193], v[54:57]
	v_mfma_f32_16x16x32_bf16 v[46:49], v[154:157], v[190:193], v[46:49]
	v_mfma_f32_16x16x32_bf16 v[38:41], v[146:149], v[198:201], v[38:41]
	v_mfma_f32_16x16x32_bf16 v[30:33], v[154:157], v[198:201], v[30:33]
	v_mfma_f32_16x16x32_bf16 v[22:25], v[146:149], v[206:209], v[22:25]
	v_mfma_f32_16x16x32_bf16 v[14:17], v[154:157], v[206:209], v[14:17]
	v_mfma_f32_16x16x32_bf16 v[62:65], v[150:153], v[186:189], v[62:65]
	v_mfma_f32_16x16x32_bf16 v[58:61], v[158:161], v[186:189], v[58:61]
	v_mfma_f32_16x16x32_bf16 v[54:57], v[150:153], v[194:197], v[54:57]
	v_mfma_f32_16x16x32_bf16 v[46:49], v[158:161], v[194:197], v[46:49]
	v_mfma_f32_16x16x32_bf16 v[38:41], v[150:153], v[202:205], v[38:41]
	v_mfma_f32_16x16x32_bf16 v[30:33], v[158:161], v[202:205], v[30:33]
	v_mfma_f32_16x16x32_bf16 v[22:25], v[150:153], v[210:213], v[22:25]
	v_mfma_f32_16x16x32_bf16 v[14:17], v[158:161], v[210:213], v[14:17]
	s_setprio 0
	s_setprio 1
	v_mfma_f32_16x16x32_bf16 v[50:53], v[162:165], v[178:181], v[50:53]
	v_mfma_f32_16x16x32_bf16 v[42:45], v[170:173], v[178:181], v[42:45]
	v_mfma_f32_16x16x32_bf16 v[34:37], v[162:165], v[190:193], v[34:37]
	v_mfma_f32_16x16x32_bf16 v[26:29], v[170:173], v[190:193], v[26:29]
	v_mfma_f32_16x16x32_bf16 v[18:21], v[162:165], v[198:201], v[18:21]
	v_mfma_f32_16x16x32_bf16 v[10:13], v[170:173], v[198:201], v[10:13]
	v_mfma_f32_16x16x32_bf16 v[6:9], v[162:165], v[206:209], v[6:9]
	v_mfma_f32_16x16x32_bf16 v[2:5], v[170:173], v[206:209], v[2:5]
	v_mfma_f32_16x16x32_bf16 v[50:53], v[166:169], v[186:189], v[50:53]
	v_mfma_f32_16x16x32_bf16 v[42:45], v[174:177], v[186:189], v[42:45]
	v_mfma_f32_16x16x32_bf16 v[34:37], v[166:169], v[194:197], v[34:37]
	v_mfma_f32_16x16x32_bf16 v[26:29], v[174:177], v[194:197], v[26:29]
	v_mfma_f32_16x16x32_bf16 v[18:21], v[166:169], v[202:205], v[18:21]
	v_mfma_f32_16x16x32_bf16 v[10:13], v[174:177], v[202:205], v[10:13]
	v_mfma_f32_16x16x32_bf16 v[6:9], v[166:169], v[210:213], v[6:9]
	v_mfma_f32_16x16x32_bf16 v[2:5], v[174:177], v[210:213], v[2:5]
	s_setprio 0
	s_barrier
	s_add_i32 s48, 0, 0x18000
	s_add_i32 s49, 0, 0x1c000
	v_add_u32_e32 v158, s48, v143
	v_add_u32_e32 v174, s49, v143
	ds_read_b128 v[146:149], v158
	ds_read_b128 v[150:153], v158 offset:1024
	ds_read_b128 v[154:157], v158 offset:2048
	ds_read_b128 v[158:161], v158 offset:3072
	ds_read_b128 v[162:165], v174
	ds_read_b128 v[166:169], v174 offset:1024
	ds_read_b128 v[170:173], v174 offset:2048
	ds_read_b128 v[174:177], v174 offset:3072
	s_add_u32 s22, s22, 0x40000
	s_addc_u32 s23, s23, 0
	s_mov_b32 m0, s35
	v_lshl_add_u64 v[220:221], s[22:23], 0, v[134:135]
	ds_read_b128 v[178:181], v145 offset:32768
	ds_read_b128 v[186:189], v145 offset:33792
	ds_read_b128 v[190:193], v145 offset:34816
	ds_read_b128 v[194:197], v145 offset:35840
	ds_read_b128 v[198:201], v145 offset:36864
	ds_read_b128 v[202:205], v145 offset:37888
	ds_read_b128 v[206:209], v145 offset:38912
	ds_read_b128 v[210:213], v145 offset:39936
	global_load_lds_dwordx4 v[220:221], off
	v_lshl_add_u64 v[220:221], s[22:23], 0, v[132:133]
	s_mov_b32 m0, s36
	s_nop 0
	global_load_lds_dwordx4 v[220:221], off
	s_waitcnt vmcnt(8)
	s_waitcnt lgkmcnt(0)
	s_barrier
	s_setprio 1
	s_waitcnt lgkmcnt(0)
	v_mfma_f32_16x16x32_bf16 v[126:129], v[146:149], v[178:181], v[126:129]
	v_mfma_f32_16x16x32_bf16 v[122:125], v[154:157], v[178:181], v[122:125]
	v_mfma_f32_16x16x32_bf16 v[118:121], v[146:149], v[190:193], v[118:121]
	v_mfma_f32_16x16x32_bf16 v[110:113], v[154:157], v[190:193], v[110:113]
	v_mfma_f32_16x16x32_bf16 v[102:105], v[146:149], v[198:201], v[102:105]
	v_mfma_f32_16x16x32_bf16 v[94:97], v[154:157], v[198:201], v[94:97]
	v_mfma_f32_16x16x32_bf16 v[86:89], v[146:149], v[206:209], v[86:89]
	v_mfma_f32_16x16x32_bf16 v[78:81], v[154:157], v[206:209], v[78:81]
	v_mfma_f32_16x16x32_bf16 v[126:129], v[150:153], v[186:189], v[126:129]
	v_mfma_f32_16x16x32_bf16 v[122:125], v[158:161], v[186:189], v[122:125]
	v_mfma_f32_16x16x32_bf16 v[118:121], v[150:153], v[194:197], v[118:121]
	v_mfma_f32_16x16x32_bf16 v[110:113], v[158:161], v[194:197], v[110:113]
	v_mfma_f32_16x16x32_bf16 v[102:105], v[150:153], v[202:205], v[102:105]
	v_mfma_f32_16x16x32_bf16 v[94:97], v[158:161], v[202:205], v[94:97]
	v_mfma_f32_16x16x32_bf16 v[86:89], v[150:153], v[210:213], v[86:89]
	v_mfma_f32_16x16x32_bf16 v[78:81], v[158:161], v[210:213], v[78:81]
	s_setprio 0
	s_setprio 1
	v_mfma_f32_16x16x32_bf16 v[114:117], v[162:165], v[178:181], v[114:117]
	v_mfma_f32_16x16x32_bf16 v[106:109], v[170:173], v[178:181], v[106:109]
	v_mfma_f32_16x16x32_bf16 v[98:101], v[162:165], v[190:193], v[98:101]
	v_mfma_f32_16x16x32_bf16 v[90:93], v[170:173], v[190:193], v[90:93]
	v_mfma_f32_16x16x32_bf16 v[82:85], v[162:165], v[198:201], v[82:85]
	v_mfma_f32_16x16x32_bf16 v[74:77], v[170:173], v[198:201], v[74:77]
	v_mfma_f32_16x16x32_bf16 v[70:73], v[162:165], v[206:209], v[70:73]
	v_mfma_f32_16x16x32_bf16 v[66:69], v[170:173], v[206:209], v[66:69]
	v_mfma_f32_16x16x32_bf16 v[114:117], v[166:169], v[186:189], v[114:117]
	v_mfma_f32_16x16x32_bf16 v[106:109], v[174:177], v[186:189], v[106:109]
	v_mfma_f32_16x16x32_bf16 v[98:101], v[166:169], v[194:197], v[98:101]
	v_mfma_f32_16x16x32_bf16 v[90:93], v[174:177], v[194:197], v[90:93]
	v_mfma_f32_16x16x32_bf16 v[82:85], v[166:169], v[202:205], v[82:85]
	v_mfma_f32_16x16x32_bf16 v[74:77], v[174:177], v[202:205], v[74:77]
	v_mfma_f32_16x16x32_bf16 v[70:73], v[166:169], v[210:213], v[70:73]
	v_mfma_f32_16x16x32_bf16 v[66:69], v[174:177], v[210:213], v[66:69]
	s_setprio 0
	s_barrier
; #define PG8_STAGE(bufoff, gbase, voff) do { _Pragma("unroll") for (int _i = 0; _i < 2; ++_i) \
;         __builtin_amdgcn_global_load_lds((const unsigned*)((const char*)(gbase) + (voff)[_i]), (PG8_LAS unsigned*)(lds + (bufoff) + ldsw + _i * 8192), 16, 0, 0); } while (0)
; #define PG8_LDA(dst, b, h) do { _Pragma("unroll") for (int m = 0; m < 4; ++m) _Pragma("unroll") for (int k = 0; k < 2; ++k) dst[m][k] = *(const PG8_LAS bf16x8*)(lds + PG8_SA(b, h) + aoff + m * 2048 + k * 1024); } while (0)
; #define PG8_WAIT_V(n) asm volatile("s_waitcnt vmcnt(" #n ")" ::: "memory")
; #define PG8_WAIT_L(n) asm volatile("s_waitcnt lgkmcnt(" #n ")" ::: "memory")
; #define PG8_BAR __builtin_amdgcn_s_barrier()
; #define PG8_SCHED __builtin_amdgcn_sched_barrier(0)
; template <class Epi, class Sched, bool ALIGN_EPI = false, bool SP2 = false, bool F8 = false, bool BTILED = false, bool ATILED = false>
; __device__ __forceinline__ void gemm_phase(PG8_LAS unsigned char* lds, const Gemm g, const Sched& S, const Epi& E) {
;     ...
;         for (int t = 0; t < nt; t += 2) {
;     ...
;             PG8_LDA(At, 1, 1); PG8_STAGE(PG8_SB(1, 0), b3, voffB); PG8_STAGE(PG8_SB(1, 1), b3 + hstepB, voffB); PG8_STAGE(PG8_SA(1, 0), a3, voffA);
;             PG8_WAIT_V(8); PG8_WAIT_L(0); PG8_BAR; PG8_MMA(1, 0, At, B0); PG8_MMA(1, 1, At, B1); PG8_BAR; PG8_SCHED;
	s_add_i32 s22, s48, s30
	v_lshl_add_u64 v[140:141], v[140:141], 0, s[90:91]
	s_mov_b32 m0, s22
	ds_read_b128 v[178:181], v145 offset:49152
	ds_read_b128 v[186:189], v145 offset:50176
	ds_read_b128 v[190:193], v145 offset:51200
	ds_read_b128 v[194:197], v145 offset:52224
	ds_read_b128 v[198:201], v145 offset:53248
	ds_read_b128 v[202:205], v145 offset:54272
	ds_read_b128 v[206:209], v145 offset:55296
	ds_read_b128 v[210:213], v145 offset:56320
	global_load_lds_dwordx4 v[140:141], off
	s_add_i32 m0, s22, 0x2000
	s_add_u32 s20, s20, 0x40080
	v_lshl_add_u64 v[140:141], v[214:215], 0, s[90:91]
	s_addc_u32 s21, s21, 0
	s_add_i32 s22, s49, s30
	global_load_lds_dwordx4 v[140:141], off
	v_lshl_add_u64 v[140:141], s[20:21], 0, v[182:183]
	s_mov_b32 m0, s22
	s_nop 0
	global_load_lds_dwordx4 v[140:141], off
	v_lshl_add_u64 v[140:141], s[20:21], 0, v[130:131]
	s_add_i32 m0, s22, 0x2000
	s_nop 0
	global_load_lds_dwordx4 v[140:141], off
	v_lshl_add_u64 v[140:141], v[216:217], 0, s[90:91]
	s_mov_b32 m0, s37
	s_nop 0
	global_load_lds_dwordx4 v[140:141], off
	v_lshl_add_u64 v[140:141], v[218:219], 0, s[90:91]
	s_mov_b32 m0, s38
	s_nop 0
	global_load_lds_dwordx4 v[140:141], off
	s_waitcnt vmcnt(8)
	s_waitcnt lgkmcnt(0)
	s_barrier
	s_setprio 1
	s_waitcnt lgkmcnt(0)
	v_mfma_f32_16x16x32_bf16 v[62:65], v[146:149], v[178:181], v[62:65]
	s_add_i32 s47, s47, 2
	s_add_u32 s2, s2, 0x100
	s_addc_u32 s3, s3, 0
	s_add_u32 s45, s45, 0x100
	s_addc_u32 s46, s46, 0
	s_cmp_gt_u32 s47, 13
	v_mfma_f32_16x16x32_bf16 v[58:61], v[154:157], v[178:181], v[58:61]
	v_mfma_f32_16x16x32_bf16 v[54:57], v[146:149], v[190:193], v[54:57]
	v_mfma_f32_16x16x32_bf16 v[46:49], v[154:157], v[190:193], v[46:49]
	v_mfma_f32_16x16x32_bf16 v[38:41], v[146:149], v[198:201], v[38:41]
	v_mfma_f32_16x16x32_bf16 v[30:33], v[154:157], v[198:201], v[30:33]
	v_mfma_f32_16x16x32_bf16 v[22:25], v[146:149], v[206:209], v[22:25]
	v_mfma_f32_16x16x32_bf16 v[14:17], v[154:157], v[206:209], v[14:17]
	v_mfma_f32_16x16x32_bf16 v[62:65], v[150:153], v[186:189], v[62:65]
	v_mfma_f32_16x16x32_bf16 v[58:61], v[158:161], v[186:189], v[58:61]
	v_mfma_f32_16x16x32_bf16 v[54:57], v[150:153], v[194:197], v[54:57]
	v_mfma_f32_16x16x32_bf16 v[46:49], v[158:161], v[194:197], v[46:49]
	v_mfma_f32_16x16x32_bf16 v[38:41], v[150:153], v[202:205], v[38:41]
	v_mfma_f32_16x16x32_bf16 v[30:33], v[158:161], v[202:205], v[30:33]
	v_mfma_f32_16x16x32_bf16 v[22:25], v[150:153], v[210:213], v[22:25]
	v_mfma_f32_16x16x32_bf16 v[14:17], v[158:161], v[210:213], v[14:17]
	s_setprio 0
	s_setprio 1
	v_mfma_f32_16x16x32_bf16 v[50:53], v[162:165], v[178:181], v[50:53]
	v_mfma_f32_16x16x32_bf16 v[42:45], v[170:173], v[178:181], v[42:45]
	v_mfma_f32_16x16x32_bf16 v[34:37], v[162:165], v[190:193], v[34:37]
	v_mfma_f32_16x16x32_bf16 v[26:29], v[170:173], v[190:193], v[26:29]
	v_mfma_f32_16x16x32_bf16 v[18:21], v[162:165], v[198:201], v[18:21]
	v_mfma_f32_16x16x32_bf16 v[10:13], v[170:173], v[198:201], v[10:13]
	v_mfma_f32_16x16x32_bf16 v[6:9], v[162:165], v[206:209], v[6:9]
	v_mfma_f32_16x16x32_bf16 v[2:5], v[170:173], v[206:209], v[2:5]
	v_mfma_f32_16x16x32_bf16 v[50:53], v[166:169], v[186:189], v[50:53]
	v_mfma_f32_16x16x32_bf16 v[42:45], v[174:177], v[186:189], v[42:45]
	v_mfma_f32_16x16x32_bf16 v[34:37], v[166:169], v[194:197], v[34:37]
	v_mfma_f32_16x16x32_bf16 v[26:29], v[174:177], v[194:197], v[26:29]
	v_mfma_f32_16x16x32_bf16 v[18:21], v[166:169], v[202:205], v[18:21]
	v_mfma_f32_16x16x32_bf16 v[10:13], v[174:177], v[202:205], v[10:13]
	v_mfma_f32_16x16x32_bf16 v[6:9], v[166:169], v[210:213], v[6:9]
	v_mfma_f32_16x16x32_bf16 v[2:5], v[174:177], v[210:213], v[2:5]
	s_setprio 0
	s_barrier
	s_cbranch_scc0 .LBB0_1078
	s_and_b64 vcc, exec, s[10:11]
	s_cbranch_vccz .LBB0_1081
	s_barrier

; #define PG8_STAGE(bufoff, gbase, voff) do { _Pragma("unroll") for (int _i = 0; _i < 2; ++_i) \
;         __builtin_amdgcn_global_load_lds((const unsigned*)((const char*)(gbase) + (voff)[_i]), (PG8_LAS unsigned*)(lds + (bufoff) + ldsw + _i * 8192), 16, 0, 0); } while (0)
; #define PG8_LDA(dst, b, h) do { _Pragma("unroll") for (int m = 0; m < 4; ++m) _Pragma("unroll") for (int k = 0; k < 2; ++k) dst[m][k] = *(const PG8_LAS bf16x8*)(lds + PG8_SA(b, h) + aoff + m * 2048 + k * 1024); } while (0)
; #define PG8_LDB(dst, b, h) do { _Pragma("unroll") for (int n = 0; n < 2; ++n) _Pragma("unroll") for (int k = 0; k < 2; ++k) dst[n][k] = *(const PG8_LAS bf16x8*)(lds + PG8_SB(b, h) + boff + n * 2048 + k * 1024); } while (0)
; #define PG8_WAIT_V(n) asm volatile("s_waitcnt vmcnt(" #n ")" ::: "memory")
; #define PG8_WAIT_L(n) asm volatile("s_waitcnt lgkmcnt(" #n ")" ::: "memory")
; #define PG8_BAR __builtin_amdgcn_s_barrier()
; template <class Epi, class Sched, bool ALIGN_EPI = false, bool SP2 = false, bool F8 = false, bool BTILED = false, bool ATILED = false>
; __device__ __forceinline__ void gemm_phase(PG8_LAS unsigned char* lds, const Gemm g, const Sched& S, const Epi& E) {
;     ...
;         for (int t = 0; t < nt; t += 2) {
;             const bool last = (t == nt - 2);
;             const char* a1 = cA + (size_t)(t + 1) * kstepA;
;             const char* a2 = last ? nA : cA + (size_t)(t + 2) * kstepA; const char* b2 = last ? nB : cB + (size_t)(t + 2) * kstepB;
;             const char* a3 = a2 + kstepA; const char* b3 = b2 + kstepB;
;             if (last && has_next) S.a_ready(nxt);
;             if constexpr (SP2) {
;             PG8_LDB(B0, 0, 0); PG8_LDB(B1, 0, 1); PG8_SCHED; PG8_LDA(At, 0, 0); PG8_STAGE(PG8_SA(1, 1), a1 + hstepA, voffA);
;             PG8_WAIT_V(8); PG8_WAIT_L(0); PG8_BAR; PG8_MMA(0, 0, At, B0); PG8_MMA(0, 1, At, B1); PG8_BAR; PG8_SCHED;
;             PG8_LDA(At, 0, 1); PG8_STAGE(PG8_SB(0, 0), b2, voffB); PG8_STAGE(PG8_SB(0, 1), b2 + hstepB, voffB); PG8_STAGE(PG8_SA(0, 0), a2, voffA);
;             PG8_WAIT_V(8); PG8_WAIT_L(0); PG8_BAR; PG8_MMA(1, 0, At, B0); PG8_MMA(1, 1, At, B1); PG8_BAR; PG8_SCHED;
;             PG8_LDB(B0, 1, 0); PG8_LDB(B1, 1, 1); PG8_SCHED; PG8_LDA(At, 1, 0); PG8_STAGE(PG8_SA(0, 1), a2 + hstepA, voffA);
;             PG8_WAIT_V(8); PG8_WAIT_L(0); PG8_BAR; PG8_MMA(0, 0, At, B0); PG8_MMA(0, 1, At, B1); PG8_BAR; PG8_SCHED;
.LBB0_1657:
	s_add_u32 s20, s2, 0xfffe0080
	s_addc_u32 s21, s3, -1
	s_add_i32 s49, 0, 0x10000
	s_cmp_eq_u32 s48, 4
	s_cselect_b32 s23, s11, s21
	s_cselect_b32 s22, s44, s20
	s_cselect_b32 s21, s13, s47
	s_cselect_b32 s20, s45, s46
	s_add_i32 s50, 0, 0x14000
	v_add_u32_e32 v2, s49, v178
	v_add_u32_e32 v6, s50, v178
	ds_read_b128 v[26:29], v2
	ds_read_b128 v[30:33], v2 offset:1024
	ds_read_b128 v[18:21], v2 offset:2048
	ds_read_b128 v[22:25], v2 offset:3072
	ds_read_b128 v[10:13], v6
	ds_read_b128 v[14:17], v6 offset:1024
	ds_read_b128 v[2:5], v6 offset:2048
	ds_read_b128 v[6:9], v6 offset:3072
	v_lshl_add_u64 v[174:175], s[2:3], 0, v[170:171]
	s_add_i32 m0, s19, 0xc000
	ds_read_b128 v[186:189], v179
	ds_read_b128 v[190:193], v179 offset:1024
	ds_read_b128 v[194:197], v179 offset:2048
	ds_read_b128 v[198:201], v179 offset:3072
	ds_read_b128 v[202:205], v179 offset:4096
	ds_read_b128 v[206:209], v179 offset:5120
	ds_read_b128 v[210:213], v179 offset:6144
	ds_read_b128 v[214:217], v179 offset:7168
	global_load_lds_dwordx4 v[174:175], off
	v_lshl_add_u64 v[174:175], s[2:3], 0, v[172:173]
	s_add_i32 m0, s19, 0xe000
	s_nop 0
	global_load_lds_dwordx4 v[174:175], off
	s_waitcnt vmcnt(8)
	s_waitcnt lgkmcnt(0)
	s_barrier
	s_setprio 1
	s_waitcnt lgkmcnt(0)
	v_mfma_f32_16x16x128_f8f6f4 v[158:161], v[26:33], v[186:193], v[158:161]
	v_mfma_f32_16x16x128_f8f6f4 v[150:153], v[18:25], v[186:193], v[150:153]
	v_mfma_f32_16x16x128_f8f6f4 v[138:141], v[26:33], v[194:201], v[138:141]
	v_mfma_f32_16x16x128_f8f6f4 v[130:133], v[18:25], v[194:201], v[130:133]
	v_mfma_f32_16x16x128_f8f6f4 v[122:125], v[26:33], v[202:209], v[122:125]
	v_mfma_f32_16x16x128_f8f6f4 v[114:117], v[18:25], v[202:209], v[114:117]
	v_mfma_f32_16x16x128_f8f6f4 v[106:109], v[26:33], v[210:217], v[106:109]
	v_mfma_f32_16x16x128_f8f6f4 v[98:101], v[18:25], v[210:217], v[98:101]
	s_setprio 0
	s_setprio 1
	v_mfma_f32_16x16x128_f8f6f4 v[154:157], v[10:17], v[186:193], v[154:157]
	v_mfma_f32_16x16x128_f8f6f4 v[146:149], v[2:9], v[186:193], v[146:149]
	v_mfma_f32_16x16x128_f8f6f4 v[142:145], v[10:17], v[194:201], v[142:145]
	v_mfma_f32_16x16x128_f8f6f4 v[134:137], v[2:9], v[194:201], v[134:137]
	v_mfma_f32_16x16x128_f8f6f4 v[126:129], v[10:17], v[202:209], v[126:129]
	v_mfma_f32_16x16x128_f8f6f4 v[118:121], v[2:9], v[202:209], v[118:121]
	v_mfma_f32_16x16x128_f8f6f4 v[110:113], v[10:17], v[210:217], v[110:113]
	v_mfma_f32_16x16x128_f8f6f4 v[102:105], v[2:9], v[210:217], v[102:105]
	s_setprio 0
	s_barrier
	s_add_i32 s49, s49, s31
	v_lshl_add_u64 v[174:175], s[20:21], 0, v[166:167]
	s_mov_b32 m0, s49
	ds_read_b128 v[186:189], v179 offset:16384
	ds_read_b128 v[190:193], v179 offset:17408
	ds_read_b128 v[194:197], v179 offset:18432
	ds_read_b128 v[198:201], v179 offset:19456
	ds_read_b128 v[202:205], v179 offset:20480
	ds_read_b128 v[206:209], v179 offset:21504
	ds_read_b128 v[210:213], v179 offset:22528
	ds_read_b128 v[214:217], v179 offset:23552
	global_load_lds_dwordx4 v[174:175], off
	s_add_i32 m0, s49, 0x2000
	s_add_u32 s52, s20, 0x2000
	v_lshl_add_u64 v[174:175], s[20:21], 0, v[162:163]
	s_addc_u32 s53, s21, 0
	s_add_i32 s49, s50, s31
	global_load_lds_dwordx4 v[174:175], off
	v_lshl_add_u64 v[174:175], s[52:53], 0, v[166:167]
	s_mov_b32 m0, s49
	v_lshl_add_u64 v[176:177], s[22:23], 0, v[164:165]
	global_load_lds_dwordx4 v[174:175], off
	v_lshl_add_u64 v[174:175], s[52:53], 0, v[162:163]
	s_add_i32 m0, s49, 0x2000
	s_nop 0
	global_load_lds_dwordx4 v[174:175], off
	v_lshl_add_u64 v[174:175], s[22:23], 0, v[182:183]
	s_mov_b32 m0, s19
	s_nop 0
	global_load_lds_dwordx4 v[174:175], off
	s_mov_b32 m0, s34
	s_nop 0
	global_load_lds_dwordx4 v[176:177], off
	s_waitcnt vmcnt(8)
	s_waitcnt lgkmcnt(0)
	s_barrier
	s_setprio 1
	s_waitcnt lgkmcnt(0)
	v_mfma_f32_16x16x128_f8f6f4 v[90:93], v[26:33], v[186:193], v[90:93]
	v_mfma_f32_16x16x128_f8f6f4 v[82:85], v[18:25], v[186:193], v[82:85]
	v_mfma_f32_16x16x128_f8f6f4 v[74:77], v[26:33], v[194:201], v[74:77]
	v_mfma_f32_16x16x128_f8f6f4 v[66:69], v[18:25], v[194:201], v[66:69]
	v_mfma_f32_16x16x128_f8f6f4 v[58:61], v[26:33], v[202:209], v[58:61]
	v_mfma_f32_16x16x128_f8f6f4 v[50:53], v[18:25], v[202:209], v[50:53]
	v_mfma_f32_16x16x128_f8f6f4 v[42:45], v[26:33], v[210:217], v[42:45]
	v_mfma_f32_16x16x128_f8f6f4 v[38:41], v[18:25], v[210:217], v[38:41]
	s_setprio 0
	s_setprio 1
	v_mfma_f32_16x16x128_f8f6f4 v[94:97], v[10:17], v[186:193], v[94:97]
	v_mfma_f32_16x16x128_f8f6f4 v[86:89], v[2:9], v[186:193], v[86:89]
	v_mfma_f32_16x16x128_f8f6f4 v[78:81], v[10:17], v[194:201], v[78:81]
	v_mfma_f32_16x16x128_f8f6f4 v[70:73], v[2:9], v[194:201], v[70:73]
	v_mfma_f32_16x16x128_f8f6f4 v[62:65], v[10:17], v[202:209], v[62:65]
	v_mfma_f32_16x16x128_f8f6f4 v[54:57], v[2:9], v[202:209], v[54:57]
	v_mfma_f32_16x16x128_f8f6f4 v[46:49], v[10:17], v[210:217], v[46:49]
	v_mfma_f32_16x16x128_f8f6f4 v[34:37], v[2:9], v[210:217], v[34:37]
	s_setprio 0
	s_barrier
	s_add_i32 s49, 0, 0x18000
	s_add_i32 s50, 0, 0x1c000
	v_add_u32_e32 v14, s49, v178
	v_add_u32_e32 v30, s50, v178
	ds_read_b128 v[2:5], v14
	ds_read_b128 v[6:9], v14 offset:1024
	ds_read_b128 v[10:13], v14 offset:2048
	ds_read_b128 v[14:17], v14 offset:3072
	ds_read_b128 v[18:21], v30
	ds_read_b128 v[22:25], v30 offset:1024
	ds_read_b128 v[26:29], v30 offset:2048
	ds_read_b128 v[30:33], v30 offset:3072
	s_add_u32 s22, s22, 0x20000
	s_addc_u32 s23, s23, 0
	s_mov_b32 m0, s35
	v_lshl_add_u64 v[180:181], s[22:23], 0, v[182:183]
	ds_read_b128 v[186:189], v179 offset:32768
	ds_read_b128 v[190:193], v179 offset:33792
	ds_read_b128 v[194:197], v179 offset:34816
	ds_read_b128 v[198:201], v179 offset:35840
	ds_read_b128 v[202:205], v179 offset:36864
	ds_read_b128 v[206:209], v179 offset:37888
	ds_read_b128 v[210:213], v179 offset:38912
	ds_read_b128 v[214:217], v179 offset:39936
	global_load_lds_dwordx4 v[180:181], off
	v_lshl_add_u64 v[180:181], s[22:23], 0, v[164:165]
	s_mov_b32 m0, s36
	s_nop 0
	global_load_lds_dwordx4 v[180:181], off
	s_waitcnt vmcnt(8)
	s_waitcnt lgkmcnt(0)
	s_barrier
; __device__ __forceinline__ unsigned pk4_fp8(float a, float b, float c, float d) {
;     a = __builtin_amdgcn_fmed3f(a, -448.f, 448.f); b = __builtin_amdgcn_fmed3f(b, -448.f, 448.f); c = __builtin_amdgcn_fmed3f(c, -448.f, 448.f); d = __builtin_amdgcn_fmed3f(d, -448.f, 448.f);
;     unsigned r = 0u; r = __builtin_amdgcn_cvt_pk_fp8_f32(a, b, r, false); r = __builtin_amdgcn_cvt_pk_fp8_f32(c, d, r, true); return r; }
;     __device__ __forceinline__ f32x2 silu_mul2(f32x2 G, f32x2 U, float ka, float ks) const {
;         const f32x2 a = G * ka; f32x2 ex; ex.x = __builtin_amdgcn_exp2f(a.x); ex.y = __builtin_amdgcn_exp2f(a.y);
;         const f32x2 d = ex * ks + ks; f32x2 r; r.x = __builtin_amdgcn_rcpf(d.x); r.y = __builtin_amdgcn_rcpf(d.y);
;         return (G * U) * r; }
;     __device__ __forceinline__ void operator()(const f32x4 (&acc)[2][2][4][2], const Unit& u, int wr, int wc, int fr, int fq) const {
;         typedef unsigned u32x2 __attribute__((ext_vector_type(2)));
;         const int c = wc * 32 + 8 * fq;
;         unsigned char* blk = O + ((size_t)u.pm * ntk + u.pc) * 32768 + (c >> 6) * 16384 + (c & 63) + (size_t)(wr * 64 + fr) * 64;
;         const float ka = -1.44269504089f * isc, ks = 1.0f / (isc * isc);
; #pragma unroll
;         for (int ai = 0; ai < 2; ++ai)
; #pragma unroll
;             for (int m = 0; m < 4; ++m) { unsigned char* rowp = blk + (ai * HALF + m * 16) * 64;
;                 const f32x4 g0 = acc[ai][0][m][0], g1 = acc[ai][0][m][1], u0 = acc[ai][1][m][0], u1 = acc[ai][1][m][1];
;                 const f32x2 h0 = silu_mul2((f32x2){g0[0], g0[1]}, (f32x2){u0[0], u0[1]}, ka, ks), h1 = silu_mul2((f32x2){g0[2], g0[3]}, (f32x2){u0[2], u0[3]}, ka, ks);
;                 const f32x2 h2 = silu_mul2((f32x2){g1[0], g1[1]}, (f32x2){u1[0], u1[1]}, ka, ks), h3 = silu_mul2((f32x2){g1[2], g1[3]}, (f32x2){u1[2], u1[3]}, ka, ks);
; template <class Epi, class Sched, bool ALIGN_EPI = false, bool SP2 = false, bool F8 = false, bool BTILED = false, bool ATILED = false>
; __device__ __forceinline__ void gemm_phase(PG8_LAS unsigned char* lds, const Gemm g, const Sched& S, const Epi& E) {
;     ...
;             PG8_LDA(At, 1, 1); PG8_STAGE(PG8_SB(1, 0), b3, voffB); PG8_STAGE(PG8_SB(1, 1), b3 + hstepB, voffB); PG8_STAGE(PG8_SA(1, 0), a3, voffA);
;             PG8_WAIT_V(8); PG8_WAIT_L(0); PG8_BAR; PG8_MMA(1, 0, At, B0); PG8_MMA(1, 1, At, B1); PG8_BAR; PG8_SCHED;
	s_setprio 1
	s_waitcnt lgkmcnt(0)
	v_mfma_f32_16x16x128_f8f6f4 v[158:161], v[2:9], v[186:193], v[158:161]
	v_mfma_f32_16x16x128_f8f6f4 v[150:153], v[10:17], v[186:193], v[150:153]
	v_mfma_f32_16x16x128_f8f6f4 v[138:141], v[2:9], v[194:201], v[138:141]
	v_mfma_f32_16x16x128_f8f6f4 v[130:133], v[10:17], v[194:201], v[130:133]
	v_mfma_f32_16x16x128_f8f6f4 v[122:125], v[2:9], v[202:209], v[122:125]
	v_mfma_f32_16x16x128_f8f6f4 v[114:117], v[10:17], v[202:209], v[114:117]
	v_mfma_f32_16x16x128_f8f6f4 v[106:109], v[2:9], v[210:217], v[106:109]
	v_mfma_f32_16x16x128_f8f6f4 v[98:101], v[10:17], v[210:217], v[98:101]
	s_setprio 0
	s_setprio 1
	v_mfma_f32_16x16x128_f8f6f4 v[154:157], v[18:25], v[186:193], v[154:157]
	v_mfma_f32_16x16x128_f8f6f4 v[146:149], v[26:33], v[186:193], v[146:149]
	v_mfma_f32_16x16x128_f8f6f4 v[142:145], v[18:25], v[194:201], v[142:145]
	v_mfma_f32_16x16x128_f8f6f4 v[134:137], v[26:33], v[194:201], v[134:137]
	v_mfma_f32_16x16x128_f8f6f4 v[126:129], v[18:25], v[202:209], v[126:129]
	v_mfma_f32_16x16x128_f8f6f4 v[118:121], v[26:33], v[202:209], v[118:121]
	v_mfma_f32_16x16x128_f8f6f4 v[110:113], v[18:25], v[210:217], v[110:113]
	v_mfma_f32_16x16x128_f8f6f4 v[102:105], v[26:33], v[210:217], v[102:105]
	s_setprio 0
	s_barrier
	s_add_u32 s22, s20, 0x8000
	s_addc_u32 s23, s21, 0
	s_add_i32 s49, s49, s31
	v_lshl_add_u64 v[180:181], s[22:23], 0, v[166:167]
	s_mov_b32 m0, s49
	ds_read_b128 v[186:189], v179 offset:49152
	ds_read_b128 v[190:193], v179 offset:50176
	ds_read_b128 v[194:197], v179 offset:51200
	ds_read_b128 v[198:201], v179 offset:52224
	ds_read_b128 v[202:205], v179 offset:53248
	ds_read_b128 v[206:209], v179 offset:54272
	ds_read_b128 v[210:213], v179 offset:55296
	ds_read_b128 v[214:217], v179 offset:56320
	global_load_lds_dwordx4 v[180:181], off
	s_add_i32 m0, s49, 0x2000
	s_add_u32 s20, s20, 0xa000
	v_lshl_add_u64 v[180:181], s[22:23], 0, v[162:163]
	s_addc_u32 s21, s21, 0
	s_add_i32 s22, s50, s31
	global_load_lds_dwordx4 v[180:181], off
	v_lshl_add_u64 v[180:181], s[20:21], 0, v[166:167]
	s_mov_b32 m0, s22
	v_lshl_add_u64 v[174:175], v[174:175], 0, s[90:91]
	global_load_lds_dwordx4 v[180:181], off
	v_lshl_add_u64 v[180:181], s[20:21], 0, v[162:163]
	s_add_i32 m0, s22, 0x2000
	s_nop 0
	global_load_lds_dwordx4 v[180:181], off
	s_mov_b32 m0, s37
	s_nop 0
	global_load_lds_dwordx4 v[174:175], off
	v_lshl_add_u64 v[174:175], v[176:177], 0, s[90:91]
	s_mov_b32 m0, s38
	s_nop 0
	global_load_lds_dwordx4 v[174:175], off
	s_waitcnt vmcnt(8)
	s_waitcnt lgkmcnt(0)
	s_barrier
	s_setprio 1
	s_waitcnt lgkmcnt(0)
	v_mfma_f32_16x16x128_f8f6f4 v[90:93], v[2:9], v[186:193], v[90:93]
	s_add_i32 s48, s48, 2
	s_add_u32 s46, s46, 0x10000
	s_addc_u32 s47, s47, 0
	s_add_u32 s2, s2, 0x100
	s_addc_u32 s3, s3, 0
	s_cmp_gt_u32 s48, 5
	v_mfma_f32_16x16x128_f8f6f4 v[82:85], v[10:17], v[186:193], v[82:85]
	v_mfma_f32_16x16x128_f8f6f4 v[74:77], v[2:9], v[194:201], v[74:77]
	v_mfma_f32_16x16x128_f8f6f4 v[66:69], v[10:17], v[194:201], v[66:69]
	v_mfma_f32_16x16x128_f8f6f4 v[58:61], v[2:9], v[202:209], v[58:61]
	v_mfma_f32_16x16x128_f8f6f4 v[50:53], v[10:17], v[202:209], v[50:53]
	v_mfma_f32_16x16x128_f8f6f4 v[42:45], v[2:9], v[210:217], v[42:45]
	v_mfma_f32_16x16x128_f8f6f4 v[38:41], v[10:17], v[210:217], v[38:41]
	s_setprio 0
	s_setprio 1
	v_mfma_f32_16x16x128_f8f6f4 v[94:97], v[18:25], v[186:193], v[94:97]
	v_mfma_f32_16x16x128_f8f6f4 v[86:89], v[26:33], v[186:193], v[86:89]
	v_mfma_f32_16x16x128_f8f6f4 v[78:81], v[18:25], v[194:201], v[78:81]
	v_mfma_f32_16x16x128_f8f6f4 v[70:73], v[26:33], v[194:201], v[70:73]
	v_mfma_f32_16x16x128_f8f6f4 v[62:65], v[18:25], v[202:209], v[62:65]
	v_mfma_f32_16x16x128_f8f6f4 v[54:57], v[26:33], v[202:209], v[54:57]
	v_mfma_f32_16x16x128_f8f6f4 v[46:49], v[18:25], v[210:217], v[46:49]
	v_mfma_f32_16x16x128_f8f6f4 v[34:37], v[26:33], v[210:217], v[34:37]
	s_setprio 0
	s_barrier
	s_cbranch_scc0 .LBB0_1657
	s_and_b64 vcc, exec, s[8:9]
	s_cbranch_vccz .LBB0_1660
	s_barrier
.LBB0_1660:
	s_mul_hi_i32 s3, s18, 22
	s_mul_i32 s2, s18, 22
	s_mov_b32 s18, 0xbcb8aa3b
	v_pk_mul_f32 v[2:3], v[158:159], s[18:19] op_sel_hi:[1,0]
	v_pk_mul_f32 v[4:5], v[160:161], s[18:19] op_sel_hi:[1,0]
	v_exp_f32_e32 v2, v2
	v_exp_f32_e32 v3, v3
	v_exp_f32_e32 v4, v4
	v_exp_f32_e32 v5, v5
	s_mov_b32 s20, 0x45800000
	v_pk_fma_f32 v[2:3], v[2:3], s[20:21], s[20:21] op_sel_hi:[1,0,0]
	v_pk_mul_f32 v[6:7], v[160:161], v[156:157]
	v_pk_fma_f32 v[4:5], v[4:5], s[20:21], s[20:21] op_sel_hi:[1,0,0]
	v_rcp_f32_e32 v2, v2
	v_rcp_f32_e32 v3, v3
	v_rcp_f32_e32 v4, v4
	v_rcp_f32_e32 v5, v5
	v_pk_mul_f32 v[8:9], v[158:159], v[154:155]
	v_pk_mul_f32 v[10:11], v[152:153], v[148:149]
	v_pk_mul_f32 v[2:3], v[8:9], v[2:3]
	v_pk_mul_f32 v[4:5], v[6:7], v[4:5]
	v_pk_mul_f32 v[6:7], v[150:151], s[18:19] op_sel_hi:[1,0]
	v_pk_mul_f32 v[8:9], v[152:153], s[18:19] op_sel_hi:[1,0]
	v_exp_f32_e32 v6, v6
	v_exp_f32_e32 v7, v7
	v_exp_f32_e32 v8, v8
	v_exp_f32_e32 v9, v9
	v_pk_mul_f32 v[12:13], v[150:151], v[146:147]
	v_pk_fma_f32 v[6:7], v[6:7], s[20:21], s[20:21] op_sel_hi:[1,0,0]
	v_med3_f32 v2, v2, s33, v226
	v_pk_fma_f32 v[8:9], v[8:9], s[20:21], s[20:21] op_sel_hi:[1,0,0]
	v_rcp_f32_e32 v6, v6
	v_rcp_f32_e32 v7, v7
	v_rcp_f32_e32 v8, v8
	v_rcp_f32_e32 v9, v9
	v_med3_f32 v3, v3, s33, v226
	v_pk_mul_f32 v[6:7], v[12:13], v[6:7]
	s_ashr_i32 s11, s43, 31
	v_pk_mul_f32 v[8:9], v[10:11], v[8:9]
	v_med3_f32 v10, v4, s33, v226
	v_med3_f32 v11, v5, s33, v226
	v_cvt_pk_fp8_f32 v4, v2, v3
	v_med3_f32 v2, v6, s33, v226
	v_med3_f32 v3, v7, s33, v226
	v_cvt_pk_fp8_f32 v5, v2, v3
	v_med3_f32 v2, v8, s33, v226
	v_med3_f32 v3, v9, s33, v226
	s_add_u32 s2, s2, s43
; __device__ __forceinline__ unsigned pk4_fp8(float a, float b, float c, float d) {
;     a = __builtin_amdgcn_fmed3f(a, -448.f, 448.f); b = __builtin_amdgcn_fmed3f(b, -448.f, 448.f); c = __builtin_amdgcn_fmed3f(c, -448.f, 448.f); d = __builtin_amdgcn_fmed3f(d, -448.f, 448.f);
;     unsigned r = 0u; r = __builtin_amdgcn_cvt_pk_fp8_f32(a, b, r, false); r = __builtin_amdgcn_cvt_pk_fp8_f32(c, d, r, true); return r; }
;     __device__ __forceinline__ f32x2 silu_mul2(f32x2 G, f32x2 U, float ka, float ks) const {
;         const f32x2 a = G * ka; f32x2 ex; ex.x = __builtin_amdgcn_exp2f(a.x); ex.y = __builtin_amdgcn_exp2f(a.y);
;         const f32x2 d = ex * ks + ks; f32x2 r; r.x = __builtin_amdgcn_rcpf(d.x); r.y = __builtin_amdgcn_rcpf(d.y);
;         return (G * U) * r; }
;     __device__ __forceinline__ void operator()(const f32x4 (&acc)[2][2][4][2], const Unit& u, int wr, int wc, int fr, int fq) const {
;         typedef unsigned u32x2 __attribute__((ext_vector_type(2)));
;         const int c = wc * 32 + 8 * fq;
;         unsigned char* blk = O + ((size_t)u.pm * ntk + u.pc) * 32768 + (c >> 6) * 16384 + (c & 63) + (size_t)(wr * 64 + fr) * 64;
;         const float ka = -1.44269504089f * isc, ks = 1.0f / (isc * isc);
; #pragma unroll
;         for (int ai = 0; ai < 2; ++ai)
; #pragma unroll
;             for (int m = 0; m < 4; ++m) { unsigned char* rowp = blk + (ai * HALF + m * 16) * 64;
;                 const f32x4 g0 = acc[ai][0][m][0], g1 = acc[ai][0][m][1], u0 = acc[ai][1][m][0], u1 = acc[ai][1][m][1];
;                 const f32x2 h0 = silu_mul2((f32x2){g0[0], g0[1]}, (f32x2){u0[0], u0[1]}, ka, ks), h1 = silu_mul2((f32x2){g0[2], g0[3]}, (f32x2){u0[2], u0[3]}, ka, ks);
;                 const f32x2 h2 = silu_mul2((f32x2){g1[0], g1[1]}, (f32x2){u1[0], u1[1]}, ka, ks), h3 = silu_mul2((f32x2){g1[2], g1[3]}, (f32x2){u1[2], u1[3]}, ka, ks);
;                 u32x2 w; w.x = pk4_fp8(h0.x, h0.y, h1.x, h1.y); w.y = pk4_fp8(h2.x, h2.y, h3.x, h3.y);
;                 *(u32x2*)rowp = w; __builtin_amdgcn_sched_barrier(0); }
	v_cvt_pk_fp8_f32 v4, v10, v11 op_sel:[0,0,1]
	v_cvt_pk_fp8_f32 v5, v2, v3 op_sel:[0,0,1]
	s_nop 15
	s_nop 15
	s_addc_u32 s3, s3, s11
	s_lshl_b64 s[2:3], s[2:3], 15
	v_lshl_add_u64 v[2:3], v[168:169], 0, s[2:3]
	global_store_dwordx2 v[2:3], v[4:5], off
	v_pk_mul_f32 v[4:5], v[138:139], s[18:19] op_sel_hi:[1,0]
	v_pk_mul_f32 v[8:9], v[138:139], v[142:143]
	v_exp_f32_e32 v4, v4
	v_exp_f32_e32 v5, v5
	v_pk_mul_f32 v[6:7], v[140:141], v[144:145]
	v_pk_mul_f32 v[12:13], v[130:131], v[134:135]
	v_pk_mul_f32 v[10:11], v[132:133], v[136:137]
	v_pk_fma_f32 v[4:5], v[4:5], s[20:21], s[20:21] op_sel_hi:[1,0,0]
	s_nop 0
	v_rcp_f32_e32 v4, v4
	v_rcp_f32_e32 v5, v5
	s_nop 0
	v_pk_mul_f32 v[4:5], v[8:9], v[4:5]
	v_pk_mul_f32 v[8:9], v[140:141], s[18:19] op_sel_hi:[1,0]
	v_med3_f32 v5, v5, s33, v226
	v_exp_f32_e32 v8, v8
	v_exp_f32_e32 v9, v9
	s_nop 0
	v_pk_fma_f32 v[8:9], v[8:9], s[20:21], s[20:21] op_sel_hi:[1,0,0]
	s_nop 0
	v_rcp_f32_e32 v8, v8
	v_rcp_f32_e32 v9, v9
	s_nop 0
	v_pk_mul_f32 v[6:7], v[6:7], v[8:9]
	v_pk_mul_f32 v[8:9], v[130:131], s[18:19] op_sel_hi:[1,0]
	v_med3_f32 v6, v6, s33, v226
	v_exp_f32_e32 v8, v8
	v_exp_f32_e32 v9, v9
	v_med3_f32 v7, v7, s33, v226
	v_pk_fma_f32 v[8:9], v[8:9], s[20:21], s[20:21] op_sel_hi:[1,0,0]
	s_nop 0
	v_rcp_f32_e32 v8, v8
	v_rcp_f32_e32 v9, v9
	s_nop 0
	v_pk_mul_f32 v[8:9], v[12:13], v[8:9]
	v_pk_mul_f32 v[12:13], v[132:133], s[18:19] op_sel_hi:[1,0]
	s_nop 0
	v_exp_f32_e32 v12, v12
	v_exp_f32_e32 v13, v13
	s_nop 0
	v_pk_fma_f32 v[12:13], v[12:13], s[20:21], s[20:21] op_sel_hi:[1,0,0]
	s_nop 0
	v_rcp_f32_e32 v12, v12
	v_rcp_f32_e32 v13, v13
	s_nop 0
	v_pk_mul_f32 v[10:11], v[10:11], v[12:13]
	v_med3_f32 v12, v4, s33, v226
	v_cvt_pk_fp8_f32 v4, v12, v5
	v_cvt_pk_fp8_f32 v4, v6, v7 op_sel:[0,0,1]
	v_med3_f32 v6, v8, s33, v226
	v_med3_f32 v7, v9, s33, v226
	v_cvt_pk_fp8_f32 v5, v6, v7
	v_med3_f32 v8, v10, s33, v226
	v_med3_f32 v9, v11, s33, v226
	v_cvt_pk_fp8_f32 v5, v8, v9 op_sel:[0,0,1]
	global_store_dwordx2 v[2:3], v[4:5], off offset:1024
	v_pk_mul_f32 v[4:5], v[122:123], s[18:19] op_sel_hi:[1,0]
	v_pk_mul_f32 v[8:9], v[122:123], v[126:127]
	v_exp_f32_e32 v4, v4
	v_exp_f32_e32 v5, v5
	v_pk_mul_f32 v[6:7], v[124:125], v[128:129]
	v_pk_mul_f32 v[12:13], v[114:115], v[118:119]
	v_pk_mul_f32 v[10:11], v[116:117], v[120:121]
	v_pk_fma_f32 v[4:5], v[4:5], s[20:21], s[20:21] op_sel_hi:[1,0,0]
	s_nop 0
	v_rcp_f32_e32 v4, v4
	v_rcp_f32_e32 v5, v5
	s_nop 0
	v_pk_mul_f32 v[4:5], v[8:9], v[4:5]
	v_pk_mul_f32 v[8:9], v[124:125], s[18:19] op_sel_hi:[1,0]
	v_med3_f32 v5, v5, s33, v226
	v_exp_f32_e32 v8, v8
	v_exp_f32_e32 v9, v9
	s_nop 0
	v_pk_fma_f32 v[8:9], v[8:9], s[20:21], s[20:21] op_sel_hi:[1,0,0]
	s_nop 0
	v_rcp_f32_e32 v8, v8
	v_rcp_f32_e32 v9, v9
	s_nop 0
	v_pk_mul_f32 v[6:7], v[6:7], v[8:9]
	v_pk_mul_f32 v[8:9], v[114:115], s[18:19] op_sel_hi:[1,0]
	v_med3_f32 v6, v6, s33, v226
	v_exp_f32_e32 v8, v8
	v_exp_f32_e32 v9, v9
	v_med3_f32 v7, v7, s33, v226
	v_pk_fma_f32 v[8:9], v[8:9], s[20:21], s[20:21] op_sel_hi:[1,0,0]
	s_nop 0
	v_rcp_f32_e32 v8, v8
	v_rcp_f32_e32 v9, v9
	s_nop 0
	v_pk_mul_f32 v[8:9], v[12:13], v[8:9]
	v_pk_mul_f32 v[12:13], v[116:117], s[18:19] op_sel_hi:[1,0]
	s_nop 0
	v_exp_f32_e32 v12, v12
	v_exp_f32_e32 v13, v13
	s_nop 0
	v_pk_fma_f32 v[12:13], v[12:13], s[20:21], s[20:21] op_sel_hi:[1,0,0]
	s_nop 0
	v_rcp_f32_e32 v12, v12
	v_rcp_f32_e32 v13, v13
	s_nop 0
	v_pk_mul_f32 v[10:11], v[10:11], v[12:13]
	v_med3_f32 v12, v4, s33, v226
	v_cvt_pk_fp8_f32 v4, v12, v5
	v_cvt_pk_fp8_f32 v4, v6, v7 op_sel:[0,0,1]
	v_med3_f32 v6, v8, s33, v226
	v_med3_f32 v7, v9, s33, v226
	v_cvt_pk_fp8_f32 v5, v6, v7
	v_med3_f32 v8, v10, s33, v226
	v_med3_f32 v9, v11, s33, v226
	v_cvt_pk_fp8_f32 v5, v8, v9 op_sel:[0,0,1]
	global_store_dwordx2 v[2:3], v[4:5], off offset:2048
	v_pk_mul_f32 v[4:5], v[106:107], s[18:19] op_sel_hi:[1,0]
	v_pk_mul_f32 v[8:9], v[106:107], v[110:111]
	v_exp_f32_e32 v4, v4
	v_exp_f32_e32 v5, v5
	v_pk_mul_f32 v[6:7], v[108:109], v[112:113]
	v_pk_mul_f32 v[12:13], v[98:99], v[102:103]
	v_pk_mul_f32 v[10:11], v[100:101], v[104:105]
	v_pk_fma_f32 v[4:5], v[4:5], s[20:21], s[20:21] op_sel_hi:[1,0,0]
	s_nop 0
	v_rcp_f32_e32 v4, v4
	v_rcp_f32_e32 v5, v5
	s_nop 0
	v_pk_mul_f32 v[4:5], v[8:9], v[4:5]
	v_pk_mul_f32 v[8:9], v[108:109], s[18:19] op_sel_hi:[1,0]
	v_med3_f32 v5, v5, s33, v226
	v_exp_f32_e32 v8, v8
	v_exp_f32_e32 v9, v9
	s_nop 0
	v_pk_fma_f32 v[8:9], v[8:9], s[20:21], s[20:21] op_sel_hi:[1,0,0]
	s_nop 0
	v_rcp_f32_e32 v8, v8
	v_rcp_f32_e32 v9, v9
	s_nop 0
	v_pk_mul_f32 v[6:7], v[6:7], v[8:9]
	v_pk_mul_f32 v[8:9], v[98:99], s[18:19] op_sel_hi:[1,0]
	v_med3_f32 v6, v6, s33, v226
	v_exp_f32_e32 v8, v8
	v_exp_f32_e32 v9, v9
	v_med3_f32 v7, v7, s33, v226
	v_pk_fma_f32 v[8:9], v[8:9], s[20:21], s[20:21] op_sel_hi:[1,0,0]
	s_nop 0
	v_rcp_f32_e32 v8, v8
	v_rcp_f32_e32 v9, v9
	s_nop 0
	v_pk_mul_f32 v[8:9], v[12:13], v[8:9]
	v_pk_mul_f32 v[12:13], v[100:101], s[18:19] op_sel_hi:[1,0]
	s_nop 0
	v_exp_f32_e32 v12, v12
	v_exp_f32_e32 v13, v13
	s_nop 0
	v_pk_fma_f32 v[12:13], v[12:13], s[20:21], s[20:21] op_sel_hi:[1,0,0]
	s_nop 0
	v_rcp_f32_e32 v12, v12
	v_rcp_f32_e32 v13, v13
	s_nop 0
	v_pk_mul_f32 v[10:11], v[10:11], v[12:13]
	v_med3_f32 v12, v4, s33, v226
	v_cvt_pk_fp8_f32 v4, v12, v5
	v_cvt_pk_fp8_f32 v4, v6, v7 op_sel:[0,0,1]
	v_med3_f32 v6, v8, s33, v226
	v_med3_f32 v7, v9, s33, v226
	v_cvt_pk_fp8_f32 v5, v6, v7
	v_med3_f32 v8, v10, s33, v226
	v_med3_f32 v9, v11, s33, v226
	v_cvt_pk_fp8_f32 v5, v8, v9 op_sel:[0,0,1]
	global_store_dwordx2 v[2:3], v[4:5], off offset:3072
	v_pk_mul_f32 v[4:5], v[90:91], s[18:19] op_sel_hi:[1,0]
	v_pk_mul_f32 v[8:9], v[90:91], v[94:95]
	v_exp_f32_e32 v4, v4
	v_exp_f32_e32 v5, v5
;     __device__ __forceinline__ f32x2 silu_mul2(f32x2 G, f32x2 U, float ka, float ks) const {
;         const f32x2 a = G * ka; f32x2 ex; ex.x = __builtin_amdgcn_exp2f(a.x); ex.y = __builtin_amdgcn_exp2f(a.y);
;         const f32x2 d = ex * ks + ks; f32x2 r; r.x = __builtin_amdgcn_rcpf(d.x); r.y = __builtin_amdgcn_rcpf(d.y);
;         return (G * U) * r; }
;     __device__ __forceinline__ void operator()(const f32x4 (&acc)[2][2][4][2], const Unit& u, int wr, int wc, int fr, int fq) const {
;         typedef unsigned u32x2 __attribute__((ext_vector_type(2)));
;         const int c = wc * 32 + 8 * fq;
;         unsigned char* blk = O + ((size_t)u.pm * ntk + u.pc) * 32768 + (c >> 6) * 16384 + (c & 63) + (size_t)(wr * 64 + fr) * 64;
;         const float ka = -1.44269504089f * isc, ks = 1.0f / (isc * isc);
; #pragma unroll
;         for (int ai = 0; ai < 2; ++ai)
; #pragma unroll
;             for (int m = 0; m < 4; ++m) { unsigned char* rowp = blk + (ai * HALF + m * 16) * 64;
;                 const f32x4 g0 = acc[ai][0][m][0], g1 = acc[ai][0][m][1], u0 = acc[ai][1][m][0], u1 = acc[ai][1][m][1];
;                 const f32x2 h0 = silu_mul2((f32x2){g0[0], g0[1]}, (f32x2){u0[0], u0[1]}, ka, ks), h1 = silu_mul2((f32x2){g0[2], g0[3]}, (f32x2){u0[2], u0[3]}, ka, ks);
;                 const f32x2 h2 = silu_mul2((f32x2){g1[0], g1[1]}, (f32x2){u1[0], u1[1]}, ka, ks), h3 = silu_mul2((f32x2){g1[2], g1[3]}, (f32x2){u1[2], u1[3]}, ka, ks);
;                 u32x2 w; w.x = pk4_fp8(h0.x, h0.y, h1.x, h1.y); w.y = pk4_fp8(h2.x, h2.y, h3.x, h3.y);
;                 *(u32x2*)rowp = w; __builtin_amdgcn_sched_barrier(0); }
; template <class Epi, class Sched, bool ALIGN_EPI = false, bool SP2 = false, bool F8 = false, bool BTILED = false, bool ATILED = false>
; __device__ __forceinline__ void gemm_phase(PG8_LAS unsigned char* lds, const Gemm g, const Sched& S, const Epi& E) {
;     ...
;         if constexpr (!Epi::AFTER_DRAIN) { E(acc, cur, wr, wc, fr, fq); S.done(cur); }
;         if (!has_next) break;
	v_pk_mul_f32 v[6:7], v[92:93], v[96:97]
	v_pk_mul_f32 v[12:13], v[82:83], v[86:87]
	v_pk_mul_f32 v[10:11], v[84:85], v[88:89]
	v_pk_fma_f32 v[4:5], v[4:5], s[20:21], s[20:21] op_sel_hi:[1,0,0]
	v_add_co_u32_e32 v2, vcc, s64, v2
	v_rcp_f32_e32 v4, v4
	v_rcp_f32_e32 v5, v5
	v_addc_co_u32_e32 v3, vcc, 0, v3, vcc
	v_pk_mul_f32 v[4:5], v[8:9], v[4:5]
	v_pk_mul_f32 v[8:9], v[92:93], s[18:19] op_sel_hi:[1,0]
	v_med3_f32 v5, v5, s33, v226
	v_exp_f32_e32 v8, v8
	v_exp_f32_e32 v9, v9
	s_nop 0
	v_pk_fma_f32 v[8:9], v[8:9], s[20:21], s[20:21] op_sel_hi:[1,0,0]
	s_nop 0
	v_rcp_f32_e32 v8, v8
	v_rcp_f32_e32 v9, v9
	s_nop 0
	v_pk_mul_f32 v[6:7], v[6:7], v[8:9]
	v_pk_mul_f32 v[8:9], v[82:83], s[18:19] op_sel_hi:[1,0]
	v_med3_f32 v6, v6, s33, v226
	v_exp_f32_e32 v8, v8
	v_exp_f32_e32 v9, v9
	v_med3_f32 v7, v7, s33, v226
	v_pk_fma_f32 v[8:9], v[8:9], s[20:21], s[20:21] op_sel_hi:[1,0,0]
	s_nop 0
	v_rcp_f32_e32 v8, v8
	v_rcp_f32_e32 v9, v9
	s_nop 0
	v_pk_mul_f32 v[8:9], v[12:13], v[8:9]
	v_pk_mul_f32 v[12:13], v[84:85], s[18:19] op_sel_hi:[1,0]
	s_nop 0
	v_exp_f32_e32 v12, v12
	v_exp_f32_e32 v13, v13
	s_nop 0
	v_pk_fma_f32 v[12:13], v[12:13], s[20:21], s[20:21] op_sel_hi:[1,0,0]
	s_nop 0
	v_rcp_f32_e32 v12, v12
	v_rcp_f32_e32 v13, v13
	s_nop 0
	v_pk_mul_f32 v[10:11], v[10:11], v[12:13]
	v_med3_f32 v12, v4, s33, v226
	v_cvt_pk_fp8_f32 v4, v12, v5
	v_cvt_pk_fp8_f32 v4, v6, v7 op_sel:[0,0,1]
	v_med3_f32 v6, v8, s33, v226
	v_med3_f32 v7, v9, s33, v226
	v_cvt_pk_fp8_f32 v5, v6, v7
	v_med3_f32 v8, v10, s33, v226
	v_med3_f32 v9, v11, s33, v226
	v_cvt_pk_fp8_f32 v5, v8, v9 op_sel:[0,0,1]
	global_store_dwordx2 v[2:3], v[4:5], off
	v_pk_mul_f32 v[4:5], v[74:75], s[18:19] op_sel_hi:[1,0]
	v_pk_mul_f32 v[8:9], v[74:75], v[78:79]
	v_exp_f32_e32 v4, v4
	v_exp_f32_e32 v5, v5
	v_pk_mul_f32 v[6:7], v[76:77], v[80:81]
	v_pk_mul_f32 v[12:13], v[66:67], v[70:71]
	v_pk_mul_f32 v[10:11], v[68:69], v[72:73]
	v_pk_fma_f32 v[4:5], v[4:5], s[20:21], s[20:21] op_sel_hi:[1,0,0]
	s_nop 0
	v_rcp_f32_e32 v4, v4
	v_rcp_f32_e32 v5, v5
	s_nop 0
	v_pk_mul_f32 v[4:5], v[8:9], v[4:5]
	v_pk_mul_f32 v[8:9], v[76:77], s[18:19] op_sel_hi:[1,0]
	v_med3_f32 v5, v5, s33, v226
	v_exp_f32_e32 v8, v8
	v_exp_f32_e32 v9, v9
	s_nop 0
	v_pk_fma_f32 v[8:9], v[8:9], s[20:21], s[20:21] op_sel_hi:[1,0,0]
	s_nop 0
	v_rcp_f32_e32 v8, v8
	v_rcp_f32_e32 v9, v9
	s_nop 0
	v_pk_mul_f32 v[6:7], v[6:7], v[8:9]
	v_pk_mul_f32 v[8:9], v[66:67], s[18:19] op_sel_hi:[1,0]
	v_med3_f32 v6, v6, s33, v226
	v_exp_f32_e32 v8, v8
	v_exp_f32_e32 v9, v9
	v_med3_f32 v7, v7, s33, v226
	v_pk_fma_f32 v[8:9], v[8:9], s[20:21], s[20:21] op_sel_hi:[1,0,0]
	s_nop 0
	v_rcp_f32_e32 v8, v8
	v_rcp_f32_e32 v9, v9
	s_nop 0
	v_pk_mul_f32 v[8:9], v[12:13], v[8:9]
	v_pk_mul_f32 v[12:13], v[68:69], s[18:19] op_sel_hi:[1,0]
	s_nop 0
	v_exp_f32_e32 v12, v12
	v_exp_f32_e32 v13, v13
	s_nop 0
	v_pk_fma_f32 v[12:13], v[12:13], s[20:21], s[20:21] op_sel_hi:[1,0,0]
	s_nop 0
	v_rcp_f32_e32 v12, v12
	v_rcp_f32_e32 v13, v13
	s_nop 0
	v_pk_mul_f32 v[10:11], v[10:11], v[12:13]
	v_med3_f32 v12, v4, s33, v226
	v_cvt_pk_fp8_f32 v4, v12, v5
	v_cvt_pk_fp8_f32 v4, v6, v7 op_sel:[0,0,1]
	v_med3_f32 v6, v8, s33, v226
	v_med3_f32 v7, v9, s33, v226
	v_cvt_pk_fp8_f32 v5, v6, v7
	v_med3_f32 v8, v10, s33, v226
	v_med3_f32 v9, v11, s33, v226
	v_cvt_pk_fp8_f32 v5, v8, v9 op_sel:[0,0,1]
	global_store_dwordx2 v[2:3], v[4:5], off offset:1024
	v_pk_mul_f32 v[4:5], v[58:59], s[18:19] op_sel_hi:[1,0]
	v_pk_mul_f32 v[8:9], v[58:59], v[62:63]
	v_exp_f32_e32 v4, v4
	v_exp_f32_e32 v5, v5
	v_pk_mul_f32 v[6:7], v[60:61], v[64:65]
	v_pk_mul_f32 v[12:13], v[50:51], v[54:55]
	v_pk_mul_f32 v[10:11], v[52:53], v[56:57]
	v_pk_fma_f32 v[4:5], v[4:5], s[20:21], s[20:21] op_sel_hi:[1,0,0]
	s_nop 0
	v_rcp_f32_e32 v4, v4
	v_rcp_f32_e32 v5, v5
	s_nop 0
	v_pk_mul_f32 v[4:5], v[8:9], v[4:5]
	v_pk_mul_f32 v[8:9], v[60:61], s[18:19] op_sel_hi:[1,0]
	v_med3_f32 v5, v5, s33, v226
	v_exp_f32_e32 v8, v8
	v_exp_f32_e32 v9, v9
	s_nop 0
	v_pk_fma_f32 v[8:9], v[8:9], s[20:21], s[20:21] op_sel_hi:[1,0,0]
	s_nop 0
	v_rcp_f32_e32 v8, v8
	v_rcp_f32_e32 v9, v9
	s_nop 0
	v_pk_mul_f32 v[6:7], v[6:7], v[8:9]
	v_pk_mul_f32 v[8:9], v[50:51], s[18:19] op_sel_hi:[1,0]
	v_med3_f32 v6, v6, s33, v226
	v_exp_f32_e32 v8, v8
	v_exp_f32_e32 v9, v9
	v_med3_f32 v7, v7, s33, v226
	v_pk_fma_f32 v[8:9], v[8:9], s[20:21], s[20:21] op_sel_hi:[1,0,0]
	s_nop 0
	v_rcp_f32_e32 v8, v8
	v_rcp_f32_e32 v9, v9
	s_nop 0
	v_pk_mul_f32 v[8:9], v[12:13], v[8:9]
	v_pk_mul_f32 v[12:13], v[52:53], s[18:19] op_sel_hi:[1,0]
	s_nop 0
	v_exp_f32_e32 v12, v12
	v_exp_f32_e32 v13, v13
	s_nop 0
	v_pk_fma_f32 v[12:13], v[12:13], s[20:21], s[20:21] op_sel_hi:[1,0,0]
	s_nop 0
	v_rcp_f32_e32 v12, v12
	v_rcp_f32_e32 v13, v13
	s_nop 0
	v_pk_mul_f32 v[10:11], v[10:11], v[12:13]
	v_med3_f32 v12, v4, s33, v226
	v_cvt_pk_fp8_f32 v4, v12, v5
	v_cvt_pk_fp8_f32 v4, v6, v7 op_sel:[0,0,1]
	v_med3_f32 v6, v8, s33, v226
	v_med3_f32 v7, v9, s33, v226
	v_cvt_pk_fp8_f32 v5, v6, v7
	v_med3_f32 v8, v10, s33, v226
	v_med3_f32 v9, v11, s33, v226
	v_cvt_pk_fp8_f32 v5, v8, v9 op_sel:[0,0,1]
	global_store_dwordx2 v[2:3], v[4:5], off offset:2048
	v_pk_mul_f32 v[4:5], v[42:43], s[18:19] op_sel_hi:[1,0]
	v_pk_mul_f32 v[8:9], v[42:43], v[46:47]
	v_exp_f32_e32 v4, v4
	v_exp_f32_e32 v5, v5
	v_pk_mul_f32 v[6:7], v[44:45], v[48:49]
	v_pk_mul_f32 v[12:13], v[38:39], v[34:35]
	v_pk_mul_f32 v[10:11], v[40:41], v[36:37]
	v_pk_fma_f32 v[4:5], v[4:5], s[20:21], s[20:21] op_sel_hi:[1,0,0]
	s_nop 0
	v_rcp_f32_e32 v4, v4
	v_rcp_f32_e32 v5, v5
	s_nop 0
	v_pk_mul_f32 v[4:5], v[8:9], v[4:5]
	v_pk_mul_f32 v[8:9], v[44:45], s[18:19] op_sel_hi:[1,0]
	v_med3_f32 v5, v5, s33, v226
	v_exp_f32_e32 v8, v8
	v_exp_f32_e32 v9, v9
	s_nop 0
	v_pk_fma_f32 v[8:9], v[8:9], s[20:21], s[20:21] op_sel_hi:[1,0,0]
	s_nop 0
	v_rcp_f32_e32 v8, v8
	v_rcp_f32_e32 v9, v9
	s_nop 0
	v_pk_mul_f32 v[6:7], v[6:7], v[8:9]
	v_pk_mul_f32 v[8:9], v[38:39], s[18:19] op_sel_hi:[1,0]
	v_med3_f32 v6, v6, s33, v226
	v_exp_f32_e32 v8, v8
	v_exp_f32_e32 v9, v9
	v_med3_f32 v7, v7, s33, v226
	v_pk_fma_f32 v[8:9], v[8:9], s[20:21], s[20:21] op_sel_hi:[1,0,0]
	s_nop 0
	v_rcp_f32_e32 v8, v8
	v_rcp_f32_e32 v9, v9
	s_nop 0
	v_pk_mul_f32 v[8:9], v[12:13], v[8:9]
	v_pk_mul_f32 v[12:13], v[40:41], s[18:19] op_sel_hi:[1,0]
	s_nop 0
	v_exp_f32_e32 v12, v12
	v_exp_f32_e32 v13, v13
	s_nop 0
	v_pk_fma_f32 v[12:13], v[12:13], s[20:21], s[20:21] op_sel_hi:[1,0,0]
	s_nop 0
	v_rcp_f32_e32 v12, v12
	v_rcp_f32_e32 v13, v13
	s_nop 0
	v_pk_mul_f32 v[10:11], v[10:11], v[12:13]
	v_med3_f32 v12, v4, s33, v226
	v_cvt_pk_fp8_f32 v4, v12, v5
	v_cvt_pk_fp8_f32 v4, v6, v7 op_sel:[0,0,1]
	v_med3_f32 v6, v8, s33, v226
	v_med3_f32 v7, v9, s33, v226
	v_cvt_pk_fp8_f32 v5, v6, v7
	v_med3_f32 v8, v10, s33, v226
	v_med3_f32 v9, v11, s33, v226
	v_cvt_pk_fp8_f32 v5, v8, v9 op_sel:[0,0,1]
	global_store_dwordx2 v[2:3], v[4:5], off offset:3072
	s_andn2_b64 vcc, exec, s[4:5]
	s_mov_b64 s[2:3], -1
	s_cbranch_vccnz .LBB0_1653
	s_andn2_b64 vcc, exec, s[6:7]
	s_cbranch_vccnz .LBB0_1652
	s_barrier
	s_branch .LBB0_1652

; #define PG8_STAGE(bufoff, gbase, voff) do { _Pragma("unroll") for (int _i = 0; _i < 2; ++_i) \
;         __builtin_amdgcn_global_load_lds((const unsigned*)((const char*)(gbase) + (voff)[_i]), (PG8_LAS unsigned*)(lds + (bufoff) + ldsw + _i * 8192), 16, 0, 0); } while (0)
; #define PG8_LDA(dst, b, h) do { _Pragma("unroll") for (int m = 0; m < 4; ++m) _Pragma("unroll") for (int k = 0; k < 2; ++k) dst[m][k] = *(const PG8_LAS bf16x8*)(lds + PG8_SA(b, h) + aoff + m * 2048 + k * 1024); } while (0)
; #define PG8_LDB(dst, b, h) do { _Pragma("unroll") for (int n = 0; n < 2; ++n) _Pragma("unroll") for (int k = 0; k < 2; ++k) dst[n][k] = *(const PG8_LAS bf16x8*)(lds + PG8_SB(b, h) + boff + n * 2048 + k * 1024); } while (0)
; #define PG8_WAIT_V(n) asm volatile("s_waitcnt vmcnt(" #n ")" ::: "memory")
; #define PG8_WAIT_L(n) asm volatile("s_waitcnt lgkmcnt(" #n ")" ::: "memory")
; #define PG8_BAR __builtin_amdgcn_s_barrier()
; template <class Epi, class Sched, bool ALIGN_EPI = false, bool SP2 = false, bool F8 = false, bool BTILED = false, bool ATILED = false>
; __device__ __forceinline__ void gemm_phase(PG8_LAS unsigned char* lds, const Gemm g, const Sched& S, const Epi& E) {
;     ...
;         for (int t = 0; t < nt; t += 2) {
;             const bool last = (t == nt - 2);
;             const char* a1 = cA + (size_t)(t + 1) * kstepA;
;             const char* a2 = last ? nA : cA + (size_t)(t + 2) * kstepA; const char* b2 = last ? nB : cB + (size_t)(t + 2) * kstepB;
;             const char* a3 = a2 + kstepA; const char* b3 = b2 + kstepB;
;             if (last && has_next) S.a_ready(nxt);
;             if constexpr (SP2) {
;             PG8_LDB(B0, 0, 0); PG8_LDB(B1, 0, 1); PG8_SCHED; PG8_LDA(At, 0, 0); PG8_STAGE(PG8_SA(1, 1), a1 + hstepA, voffA);
;             PG8_WAIT_V(8); PG8_WAIT_L(0); PG8_BAR; PG8_MMA(0, 0, At, B0); PG8_MMA(0, 1, At, B1); PG8_BAR; PG8_SCHED;
;             PG8_LDA(At, 0, 1); PG8_STAGE(PG8_SB(0, 0), b2, voffB); PG8_STAGE(PG8_SB(0, 1), b2 + hstepB, voffB); PG8_STAGE(PG8_SA(0, 0), a2, voffA);
;             PG8_WAIT_V(8); PG8_WAIT_L(0); PG8_BAR; PG8_MMA(1, 0, At, B0); PG8_MMA(1, 1, At, B1); PG8_BAR; PG8_SCHED;
;             PG8_LDB(B0, 1, 0); PG8_LDB(B1, 1, 1); PG8_SCHED; PG8_LDA(At, 1, 0); PG8_STAGE(PG8_SA(0, 1), a2 + hstepA, voffA);
;             PG8_WAIT_V(8); PG8_WAIT_L(0); PG8_BAR; PG8_MMA(0, 0, At, B0); PG8_MMA(0, 1, At, B1); PG8_BAR; PG8_SCHED;
.LBB0_1803:
	s_add_u32 s2, s6, 0x10000
	s_addc_u32 s3, s7, 0
	s_cmp_eq_u32 s54, 18
	s_cselect_b32 s26, s0, s2
	s_cselect_b32 s27, s1, s3
	s_cselect_b32 s24, s20, s52
	s_cselect_b32 s25, s21, s53
	s_add_u32 s22, s26, 0x8000
	s_addc_u32 s23, s27, 0
	s_add_i32 s56, 0, 0x10000
	s_add_i32 s55, 0, 0x14000
	v_add_u32_e32 v2, s56, v173
	v_add_u32_e32 v6, s55, v173
	ds_read_b128 v[26:29], v2
	ds_read_b128 v[30:33], v2 offset:1024
	ds_read_b128 v[18:21], v2 offset:2048
	ds_read_b128 v[22:25], v2 offset:3072
	ds_read_b128 v[10:13], v6
	ds_read_b128 v[14:17], v6 offset:1024
	ds_read_b128 v[2:5], v6 offset:2048
	ds_read_b128 v[6:9], v6 offset:3072
	v_lshl_add_u64 v[176:177], s[6:7], 0, v[168:169]
	s_add_i32 m0, s38, 0xc000
	ds_read_b128 v[186:189], v175
	ds_read_b128 v[190:193], v175 offset:1024
	ds_read_b128 v[194:197], v175 offset:2048
	ds_read_b128 v[198:201], v175 offset:3072
	ds_read_b128 v[202:205], v175 offset:4096
	ds_read_b128 v[206:209], v175 offset:5120
	ds_read_b128 v[210:213], v175 offset:6144
	ds_read_b128 v[214:217], v175 offset:7168
	global_load_lds_dwordx4 v[176:177], off
	v_lshl_add_u64 v[176:177], s[6:7], 0, v[170:171]
	s_add_i32 m0, s38, 0xe000
	s_nop 0
	global_load_lds_dwordx4 v[176:177], off
	s_waitcnt vmcnt(8)
	s_waitcnt lgkmcnt(0)
	s_barrier
	s_setprio 1
	s_waitcnt lgkmcnt(0)
	v_mfma_f32_16x16x128_f8f6f4 v[158:161], v[26:33], v[186:193], v[158:161]
	v_mfma_f32_16x16x128_f8f6f4 v[154:157], v[18:25], v[186:193], v[154:157]
	v_mfma_f32_16x16x128_f8f6f4 v[142:145], v[26:33], v[194:201], v[142:145]
	v_mfma_f32_16x16x128_f8f6f4 v[138:141], v[18:25], v[194:201], v[138:141]
	v_mfma_f32_16x16x128_f8f6f4 v[126:129], v[26:33], v[202:209], v[126:129]
	v_mfma_f32_16x16x128_f8f6f4 v[122:125], v[18:25], v[202:209], v[122:125]
	v_mfma_f32_16x16x128_f8f6f4 v[110:113], v[26:33], v[210:217], v[110:113]
	v_mfma_f32_16x16x128_f8f6f4 v[106:109], v[18:25], v[210:217], v[106:109]
	s_setprio 0
	s_setprio 1
	v_mfma_f32_16x16x128_f8f6f4 v[150:153], v[10:17], v[186:193], v[150:153]
	v_mfma_f32_16x16x128_f8f6f4 v[146:149], v[2:9], v[186:193], v[146:149]
	v_mfma_f32_16x16x128_f8f6f4 v[134:137], v[10:17], v[194:201], v[134:137]
	v_mfma_f32_16x16x128_f8f6f4 v[130:133], v[2:9], v[194:201], v[130:133]
	v_mfma_f32_16x16x128_f8f6f4 v[118:121], v[10:17], v[202:209], v[118:121]
	v_mfma_f32_16x16x128_f8f6f4 v[114:117], v[2:9], v[202:209], v[114:117]
	v_mfma_f32_16x16x128_f8f6f4 v[102:105], v[10:17], v[210:217], v[102:105]
	v_mfma_f32_16x16x128_f8f6f4 v[98:101], v[2:9], v[210:217], v[98:101]
	s_setprio 0
	s_barrier
	s_add_i32 s6, s56, s37
	v_lshl_add_u64 v[176:177], s[24:25], 0, v[182:183]
	s_mov_b32 m0, s6
	ds_read_b128 v[186:189], v175 offset:16384
	ds_read_b128 v[190:193], v175 offset:17408
	ds_read_b128 v[194:197], v175 offset:18432
	ds_read_b128 v[198:201], v175 offset:19456
	ds_read_b128 v[202:205], v175 offset:20480
	ds_read_b128 v[206:209], v175 offset:21504
	ds_read_b128 v[210:213], v175 offset:22528
	ds_read_b128 v[214:217], v175 offset:23552
	global_load_lds_dwordx4 v[176:177], off
	s_add_i32 m0, s6, 0x2000
	s_add_u32 s6, s24, 0x2000
	v_lshl_add_u64 v[176:177], s[24:25], 0, v[166:167]
	s_addc_u32 s7, s25, 0
	s_add_i32 s55, s55, s37
	global_load_lds_dwordx4 v[176:177], off
	v_lshl_add_u64 v[176:177], s[6:7], 0, v[182:183]
	s_mov_b32 m0, s55
	s_nop 0
	global_load_lds_dwordx4 v[176:177], off
	v_lshl_add_u64 v[176:177], s[6:7], 0, v[166:167]
	s_add_i32 m0, s55, 0x2000
	s_nop 0
	global_load_lds_dwordx4 v[176:177], off
	v_lshl_add_u64 v[176:177], s[26:27], 0, v[162:163]
	s_mov_b32 m0, s38
	s_nop 0
	global_load_lds_dwordx4 v[176:177], off
	v_lshl_add_u64 v[176:177], s[26:27], 0, v[164:165]
	s_mov_b32 m0, s39
	s_nop 0
	global_load_lds_dwordx4 v[176:177], off
	s_waitcnt vmcnt(8)
	s_waitcnt lgkmcnt(0)
	s_barrier
	s_setprio 1
	s_waitcnt lgkmcnt(0)
	v_mfma_f32_16x16x128_f8f6f4 v[94:97], v[26:33], v[186:193], v[94:97]
	v_mfma_f32_16x16x128_f8f6f4 v[90:93], v[18:25], v[186:193], v[90:93]
	v_mfma_f32_16x16x128_f8f6f4 v[78:81], v[26:33], v[194:201], v[78:81]
	v_mfma_f32_16x16x128_f8f6f4 v[74:77], v[18:25], v[194:201], v[74:77]
	v_mfma_f32_16x16x128_f8f6f4 v[62:65], v[26:33], v[202:209], v[62:65]
	v_mfma_f32_16x16x128_f8f6f4 v[58:61], v[18:25], v[202:209], v[58:61]
	v_mfma_f32_16x16x128_f8f6f4 v[46:49], v[26:33], v[210:217], v[46:49]
	v_mfma_f32_16x16x128_f8f6f4 v[42:45], v[18:25], v[210:217], v[42:45]
	s_setprio 0
	s_setprio 1
	v_mfma_f32_16x16x128_f8f6f4 v[86:89], v[10:17], v[186:193], v[86:89]
	v_mfma_f32_16x16x128_f8f6f4 v[82:85], v[2:9], v[186:193], v[82:85]
	v_mfma_f32_16x16x128_f8f6f4 v[70:73], v[10:17], v[194:201], v[70:73]
	v_mfma_f32_16x16x128_f8f6f4 v[66:69], v[2:9], v[194:201], v[66:69]
	v_mfma_f32_16x16x128_f8f6f4 v[54:57], v[10:17], v[202:209], v[54:57]
	v_mfma_f32_16x16x128_f8f6f4 v[50:53], v[2:9], v[202:209], v[50:53]
	v_mfma_f32_16x16x128_f8f6f4 v[38:41], v[10:17], v[210:217], v[38:41]
	v_mfma_f32_16x16x128_f8f6f4 v[34:37], v[2:9], v[210:217], v[34:37]
	s_setprio 0
	s_barrier
; #define PG8_STAGE(bufoff, gbase, voff) do { _Pragma("unroll") for (int _i = 0; _i < 2; ++_i) \
;         __builtin_amdgcn_global_load_lds((const unsigned*)((const char*)(gbase) + (voff)[_i]), (PG8_LAS unsigned*)(lds + (bufoff) + ldsw + _i * 8192), 16, 0, 0); } while (0)
; #define PG8_LDA(dst, b, h) do { _Pragma("unroll") for (int m = 0; m < 4; ++m) _Pragma("unroll") for (int k = 0; k < 2; ++k) dst[m][k] = *(const PG8_LAS bf16x8*)(lds + PG8_SA(b, h) + aoff + m * 2048 + k * 1024); } while (0)
; #define PG8_LDB(dst, b, h) do { _Pragma("unroll") for (int n = 0; n < 2; ++n) _Pragma("unroll") for (int k = 0; k < 2; ++k) dst[n][k] = *(const PG8_LAS bf16x8*)(lds + PG8_SB(b, h) + boff + n * 2048 + k * 1024); } while (0)
; #define PG8_WAIT_V(n) asm volatile("s_waitcnt vmcnt(" #n ")" ::: "memory")
; #define PG8_WAIT_L(n) asm volatile("s_waitcnt lgkmcnt(" #n ")" ::: "memory")
; #define PG8_BAR __builtin_amdgcn_s_barrier()
; #define PG8_SCHED __builtin_amdgcn_sched_barrier(0)
; template <class Epi, class Sched, bool ALIGN_EPI = false, bool SP2 = false, bool F8 = false, bool BTILED = false, bool ATILED = false>
; __device__ __forceinline__ void gemm_phase(PG8_LAS unsigned char* lds, const Gemm g, const Sched& S, const Epi& E) {
;     ...
;             PG8_LDB(B0, 1, 0); PG8_LDB(B1, 1, 1); PG8_SCHED; PG8_LDA(At, 1, 0); PG8_STAGE(PG8_SA(0, 1), a2 + hstepA, voffA);
;             PG8_WAIT_V(8); PG8_WAIT_L(0); PG8_BAR; PG8_MMA(0, 0, At, B0); PG8_MMA(0, 1, At, B1); PG8_BAR; PG8_SCHED;
;             PG8_LDA(At, 1, 1); PG8_STAGE(PG8_SB(1, 0), b3, voffB); PG8_STAGE(PG8_SB(1, 1), b3 + hstepB, voffB); PG8_STAGE(PG8_SA(1, 0), a3, voffA);
;             PG8_WAIT_V(8); PG8_WAIT_L(0); PG8_BAR; PG8_MMA(1, 0, At, B0); PG8_MMA(1, 1, At, B1); PG8_BAR; PG8_SCHED;
	s_add_i32 s55, 0, 0x18000
	s_add_i32 s56, 0, 0x1c000
	v_add_u32_e32 v14, s55, v173
	v_add_u32_e32 v30, s56, v173
	ds_read_b128 v[2:5], v14
	ds_read_b128 v[6:9], v14 offset:1024
	ds_read_b128 v[10:13], v14 offset:2048
	ds_read_b128 v[14:17], v14 offset:3072
	ds_read_b128 v[18:21], v30
	ds_read_b128 v[22:25], v30 offset:1024
	ds_read_b128 v[26:29], v30 offset:2048
	ds_read_b128 v[30:33], v30 offset:3072
	s_add_u32 s6, s26, 0x2000
	s_addc_u32 s7, s27, 0
	s_mov_b32 m0, s40
	v_lshl_add_u64 v[176:177], s[6:7], 0, v[162:163]
	ds_read_b128 v[186:189], v175 offset:32768
	ds_read_b128 v[190:193], v175 offset:33792
	ds_read_b128 v[194:197], v175 offset:34816
	ds_read_b128 v[198:201], v175 offset:35840
	ds_read_b128 v[202:205], v175 offset:36864
	ds_read_b128 v[206:209], v175 offset:37888
	ds_read_b128 v[210:213], v175 offset:38912
	ds_read_b128 v[214:217], v175 offset:39936
	global_load_lds_dwordx4 v[176:177], off
	v_lshl_add_u64 v[176:177], s[6:7], 0, v[164:165]
	s_mov_b32 m0, s41
	s_nop 0
	global_load_lds_dwordx4 v[176:177], off
	s_waitcnt vmcnt(8)
	s_waitcnt lgkmcnt(0)
	s_barrier
	s_setprio 1
	s_waitcnt lgkmcnt(0)
	v_mfma_f32_16x16x128_f8f6f4 v[158:161], v[2:9], v[186:193], v[158:161]
	v_mfma_f32_16x16x128_f8f6f4 v[154:157], v[10:17], v[186:193], v[154:157]
	v_mfma_f32_16x16x128_f8f6f4 v[142:145], v[2:9], v[194:201], v[142:145]
	v_mfma_f32_16x16x128_f8f6f4 v[138:141], v[10:17], v[194:201], v[138:141]
	v_mfma_f32_16x16x128_f8f6f4 v[126:129], v[2:9], v[202:209], v[126:129]
	v_mfma_f32_16x16x128_f8f6f4 v[122:125], v[10:17], v[202:209], v[122:125]
	v_mfma_f32_16x16x128_f8f6f4 v[110:113], v[2:9], v[210:217], v[110:113]
	v_mfma_f32_16x16x128_f8f6f4 v[106:109], v[10:17], v[210:217], v[106:109]
	s_setprio 0
	s_setprio 1
	v_mfma_f32_16x16x128_f8f6f4 v[150:153], v[18:25], v[186:193], v[150:153]
	v_mfma_f32_16x16x128_f8f6f4 v[146:149], v[26:33], v[186:193], v[146:149]
	v_mfma_f32_16x16x128_f8f6f4 v[134:137], v[18:25], v[194:201], v[134:137]
	v_mfma_f32_16x16x128_f8f6f4 v[130:133], v[26:33], v[194:201], v[130:133]
	v_mfma_f32_16x16x128_f8f6f4 v[118:121], v[18:25], v[202:209], v[118:121]
	v_mfma_f32_16x16x128_f8f6f4 v[114:117], v[26:33], v[202:209], v[114:117]
	v_mfma_f32_16x16x128_f8f6f4 v[102:105], v[18:25], v[210:217], v[102:105]
	v_mfma_f32_16x16x128_f8f6f4 v[98:101], v[26:33], v[210:217], v[98:101]
	s_setprio 0
	s_barrier
	s_add_u32 s6, s24, 0x8000
	s_addc_u32 s7, s25, 0
	s_add_i32 s26, s55, s37
	v_lshl_add_u64 v[176:177], s[6:7], 0, v[182:183]
	s_mov_b32 m0, s26
	ds_read_b128 v[186:189], v175 offset:49152
	ds_read_b128 v[190:193], v175 offset:50176
	ds_read_b128 v[194:197], v175 offset:51200
	ds_read_b128 v[198:201], v175 offset:52224
	ds_read_b128 v[202:205], v175 offset:53248
	ds_read_b128 v[206:209], v175 offset:54272
	ds_read_b128 v[210:213], v175 offset:55296
	ds_read_b128 v[214:217], v175 offset:56320
	global_load_lds_dwordx4 v[176:177], off
	s_add_i32 m0, s26, 0x2000
	v_lshl_add_u64 v[176:177], s[6:7], 0, v[166:167]
	s_add_u32 s6, s24, 0xa000
	s_addc_u32 s7, s25, 0
	s_add_i32 s24, s56, s37
	global_load_lds_dwordx4 v[176:177], off
	v_lshl_add_u64 v[176:177], s[6:7], 0, v[182:183]
	s_mov_b32 m0, s24
	s_nop 0
	global_load_lds_dwordx4 v[176:177], off
	v_lshl_add_u64 v[176:177], s[6:7], 0, v[166:167]
	s_add_i32 m0, s24, 0x2000
	s_nop 0
	global_load_lds_dwordx4 v[176:177], off
	v_lshl_add_u64 v[176:177], s[22:23], 0, v[162:163]
	s_mov_b32 m0, s42
	s_nop 0
	global_load_lds_dwordx4 v[176:177], off
	v_lshl_add_u64 v[176:177], s[22:23], 0, v[164:165]
	s_mov_b32 m0, s43
	s_nop 0
	global_load_lds_dwordx4 v[176:177], off
	s_waitcnt vmcnt(8)
	s_waitcnt lgkmcnt(0)
	s_barrier
	s_setprio 1
	s_waitcnt lgkmcnt(0)
	v_mfma_f32_16x16x128_f8f6f4 v[94:97], v[2:9], v[186:193], v[94:97]
	s_add_i32 s54, s54, 2
	s_add_u32 s52, s52, 0x10000
	s_addc_u32 s53, s53, 0
	s_cmp_gt_u32 s54, 19
	s_mov_b64 s[6:7], s[2:3]
	v_mfma_f32_16x16x128_f8f6f4 v[90:93], v[10:17], v[186:193], v[90:93]
	v_mfma_f32_16x16x128_f8f6f4 v[78:81], v[2:9], v[194:201], v[78:81]
	v_mfma_f32_16x16x128_f8f6f4 v[74:77], v[10:17], v[194:201], v[74:77]
	v_mfma_f32_16x16x128_f8f6f4 v[62:65], v[2:9], v[202:209], v[62:65]
	v_mfma_f32_16x16x128_f8f6f4 v[58:61], v[10:17], v[202:209], v[58:61]
	v_mfma_f32_16x16x128_f8f6f4 v[46:49], v[2:9], v[210:217], v[46:49]
	v_mfma_f32_16x16x128_f8f6f4 v[42:45], v[10:17], v[210:217], v[42:45]
	s_setprio 0
	s_setprio 1
	v_mfma_f32_16x16x128_f8f6f4 v[86:89], v[18:25], v[186:193], v[86:89]
	v_mfma_f32_16x16x128_f8f6f4 v[82:85], v[26:33], v[186:193], v[82:85]
	v_mfma_f32_16x16x128_f8f6f4 v[70:73], v[18:25], v[194:201], v[70:73]
	v_mfma_f32_16x16x128_f8f6f4 v[66:69], v[26:33], v[194:201], v[66:69]
	v_mfma_f32_16x16x128_f8f6f4 v[54:57], v[18:25], v[202:209], v[54:57]
	v_mfma_f32_16x16x128_f8f6f4 v[50:53], v[26:33], v[202:209], v[50:53]
	v_mfma_f32_16x16x128_f8f6f4 v[38:41], v[18:25], v[210:217], v[38:41]
	v_mfma_f32_16x16x128_f8f6f4 v[34:37], v[26:33], v[210:217], v[34:37]
	s_setprio 0
	s_barrier
	s_cbranch_scc0 .LBB0_1803
	s_and_b64 vcc, exec, s[16:17]
	s_cbranch_vccz .LBB0_1806
	s_barrier
